# v10: v7 + ph1 modreduce loads all in flight + ph7 branch-GEMM gate loads (mid-K rescale and final epilogue) issued together into free registers instead of one fully-waited load per row group
# speedup vs baseline: 1.0203x; 1.0178x over previous
; __device__ __forceinline__ void ph1_modreduce(const Frame& F, const Args& A) {
;     const float* MODP = (const float*)(A.ws + WS_MODP); float* MOD = (float*)(A.ws + WS_MOD); const float* ab = A.in[I_ADAB];
;     for (int j = F.vcu * 512 + F.tid; j < 12288; j += F.G * 512) { float s = ab[j];
; #pragma unroll 8
;         for (int sl = 0; sl < 64; ++sl) s += MODP[(size_t)sl * 12288 + j];
;         MOD[j] = s; }
.LBB0_106:
	v_ashrrev_i32_e32 v3, 31, v2
	v_lshl_add_u64 v[6:7], v[2:3], 2, s[54:55]
	global_load_dword v1, v[6:7], off
	s_add_u32 s12, s88, 0x100000
	s_addc_u32 s13, s89, 0
	v_lshlrev_b32_e32 v10, 2, v2
	global_load_dword v14, v10, s[12:13]
	s_add_u32 s12, s12, 0xc000
	s_addc_u32 s13, s13, 0
	global_load_dword v15, v10, s[12:13]
	s_add_u32 s12, s12, 0xc000
	s_addc_u32 s13, s13, 0
	global_load_dword v16, v10, s[12:13]
	s_add_u32 s12, s12, 0xc000
	s_addc_u32 s13, s13, 0
	global_load_dword v17, v10, s[12:13]
	s_add_u32 s12, s12, 0xc000
	s_addc_u32 s13, s13, 0
	global_load_dword v18, v10, s[12:13]
	s_add_u32 s12, s12, 0xc000
	s_addc_u32 s13, s13, 0
	global_load_dword v19, v10, s[12:13]
	s_add_u32 s12, s12, 0xc000
	s_addc_u32 s13, s13, 0
	global_load_dword v20, v10, s[12:13]
	s_add_u32 s12, s12, 0xc000
	s_addc_u32 s13, s13, 0
	global_load_dword v21, v10, s[12:13]
	s_add_u32 s12, s12, 0xc000
	s_addc_u32 s13, s13, 0
	global_load_dword v22, v10, s[12:13]
	s_add_u32 s12, s12, 0xc000
	s_addc_u32 s13, s13, 0
	global_load_dword v23, v10, s[12:13]
	s_add_u32 s12, s12, 0xc000
	s_addc_u32 s13, s13, 0
	global_load_dword v24, v10, s[12:13]
	s_add_u32 s12, s12, 0xc000
	s_addc_u32 s13, s13, 0
	global_load_dword v25, v10, s[12:13]
	s_add_u32 s12, s12, 0xc000
	s_addc_u32 s13, s13, 0
	global_load_dword v26, v10, s[12:13]
	s_add_u32 s12, s12, 0xc000
	s_addc_u32 s13, s13, 0
	global_load_dword v27, v10, s[12:13]
	s_add_u32 s12, s12, 0xc000
	s_addc_u32 s13, s13, 0
	global_load_dword v28, v10, s[12:13]
	s_add_u32 s12, s12, 0xc000
	s_addc_u32 s13, s13, 0
	global_load_dword v29, v10, s[12:13]
	s_add_u32 s12, s12, 0xc000
	s_addc_u32 s13, s13, 0
	global_load_dword v30, v10, s[12:13]
	s_add_u32 s12, s12, 0xc000
	s_addc_u32 s13, s13, 0
	global_load_dword v31, v10, s[12:13]
	s_add_u32 s12, s12, 0xc000
	s_addc_u32 s13, s13, 0
	global_load_dword v32, v10, s[12:13]
	s_add_u32 s12, s12, 0xc000
	s_addc_u32 s13, s13, 0
	global_load_dword v33, v10, s[12:13]
	s_add_u32 s12, s12, 0xc000
	s_addc_u32 s13, s13, 0
	global_load_dword v34, v10, s[12:13]
	s_add_u32 s12, s12, 0xc000
	s_addc_u32 s13, s13, 0
	global_load_dword v35, v10, s[12:13]
	s_add_u32 s12, s12, 0xc000
	s_addc_u32 s13, s13, 0
	global_load_dword v36, v10, s[12:13]
	s_add_u32 s12, s12, 0xc000
	s_addc_u32 s13, s13, 0
	global_load_dword v37, v10, s[12:13]
	s_add_u32 s12, s12, 0xc000
	s_addc_u32 s13, s13, 0
	global_load_dword v38, v10, s[12:13]
	s_add_u32 s12, s12, 0xc000
	s_addc_u32 s13, s13, 0
	global_load_dword v39, v10, s[12:13]
	s_add_u32 s12, s12, 0xc000
	s_addc_u32 s13, s13, 0
	global_load_dword v40, v10, s[12:13]
	s_add_u32 s12, s12, 0xc000
	s_addc_u32 s13, s13, 0
	global_load_dword v41, v10, s[12:13]
	s_add_u32 s12, s12, 0xc000
	s_addc_u32 s13, s13, 0
	global_load_dword v42, v10, s[12:13]
	s_add_u32 s12, s12, 0xc000
	s_addc_u32 s13, s13, 0
	global_load_dword v43, v10, s[12:13]
	s_add_u32 s12, s12, 0xc000
	s_addc_u32 s13, s13, 0
	global_load_dword v44, v10, s[12:13]
	s_add_u32 s12, s12, 0xc000
	s_addc_u32 s13, s13, 0
	global_load_dword v45, v10, s[12:13]
	s_add_u32 s12, s12, 0xc000
	s_addc_u32 s13, s13, 0
	global_load_dword v46, v10, s[12:13]
	s_add_u32 s12, s12, 0xc000
	s_addc_u32 s13, s13, 0
	global_load_dword v47, v10, s[12:13]
	s_add_u32 s12, s12, 0xc000
	s_addc_u32 s13, s13, 0
	global_load_dword v48, v10, s[12:13]
	s_add_u32 s12, s12, 0xc000
	s_addc_u32 s13, s13, 0
	global_load_dword v49, v10, s[12:13]
	s_add_u32 s12, s12, 0xc000
	s_addc_u32 s13, s13, 0
	global_load_dword v50, v10, s[12:13]
	s_add_u32 s12, s12, 0xc000
	s_addc_u32 s13, s13, 0
	global_load_dword v51, v10, s[12:13]
	s_add_u32 s12, s12, 0xc000
	s_addc_u32 s13, s13, 0
	global_load_dword v52, v10, s[12:13]
	s_add_u32 s12, s12, 0xc000
	s_addc_u32 s13, s13, 0
	global_load_dword v53, v10, s[12:13]
	s_add_u32 s12, s12, 0xc000
	s_addc_u32 s13, s13, 0
	global_load_dword v54, v10, s[12:13]
	s_add_u32 s12, s12, 0xc000
	s_addc_u32 s13, s13, 0
	global_load_dword v55, v10, s[12:13]
	s_add_u32 s12, s12, 0xc000
	s_addc_u32 s13, s13, 0
	global_load_dword v56, v10, s[12:13]
	s_add_u32 s12, s12, 0xc000
	s_addc_u32 s13, s13, 0
	global_load_dword v57, v10, s[12:13]
	s_add_u32 s12, s12, 0xc000
	s_addc_u32 s13, s13, 0
	global_load_dword v58, v10, s[12:13]
	s_add_u32 s12, s12, 0xc000
	s_addc_u32 s13, s13, 0
	global_load_dword v59, v10, s[12:13]
	s_add_u32 s12, s12, 0xc000
	s_addc_u32 s13, s13, 0
	global_load_dword v60, v10, s[12:13]
	s_add_u32 s12, s12, 0xc000
	s_addc_u32 s13, s13, 0
	global_load_dword v61, v10, s[12:13]
	s_add_u32 s12, s12, 0xc000
	s_addc_u32 s13, s13, 0
	global_load_dword v62, v10, s[12:13]
	s_add_u32 s12, s12, 0xc000
	s_addc_u32 s13, s13, 0
	global_load_dword v63, v10, s[12:13]
	s_add_u32 s12, s12, 0xc000
	s_addc_u32 s13, s13, 0
	global_load_dword v64, v10, s[12:13]
	s_add_u32 s12, s12, 0xc000
	s_addc_u32 s13, s13, 0
	global_load_dword v65, v10, s[12:13]
	s_add_u32 s12, s12, 0xc000
	s_addc_u32 s13, s13, 0
	global_load_dword v66, v10, s[12:13]
	s_add_u32 s12, s12, 0xc000
	s_addc_u32 s13, s13, 0
	global_load_dword v67, v10, s[12:13]
	s_add_u32 s12, s12, 0xc000
	s_addc_u32 s13, s13, 0
	global_load_dword v68, v10, s[12:13]
	s_add_u32 s12, s12, 0xc000
	s_addc_u32 s13, s13, 0
	global_load_dword v69, v10, s[12:13]
	s_add_u32 s12, s12, 0xc000
	s_addc_u32 s13, s13, 0
	global_load_dword v70, v10, s[12:13]
	s_add_u32 s12, s12, 0xc000
	s_addc_u32 s13, s13, 0
	global_load_dword v71, v10, s[12:13]
	s_add_u32 s12, s12, 0xc000
	s_addc_u32 s13, s13, 0
	global_load_dword v72, v10, s[12:13]
	s_add_u32 s12, s12, 0xc000
	s_addc_u32 s13, s13, 0
	global_load_dword v73, v10, s[12:13]
	s_add_u32 s12, s12, 0xc000
	s_addc_u32 s13, s13, 0
	global_load_dword v74, v10, s[12:13]
	s_add_u32 s12, s12, 0xc000
	s_addc_u32 s13, s13, 0
	global_load_dword v75, v10, s[12:13]
	s_add_u32 s12, s12, 0xc000
	s_addc_u32 s13, s13, 0
	global_load_dword v76, v10, s[12:13]
	s_add_u32 s12, s12, 0xc000
	s_addc_u32 s13, s13, 0
	global_load_dword v77, v10, s[12:13]
	s_waitcnt vmcnt(0)
; __device__ __forceinline__ void ph1_modreduce(const Frame& F, const Args& A) {
;     ...
;     for (int j = F.vcu * 512 + F.tid; j < 12288; j += F.G * 512) { float s = ab[j];
; #pragma unroll 8
;         for (int sl = 0; sl < 64; ++sl) s += MODP[(size_t)sl * 12288 + j];
;         MOD[j] = s; }
	v_add_f32_e32 v1, v1, v14
	v_add_f32_e32 v1, v1, v15
	v_add_f32_e32 v1, v1, v16
	v_add_f32_e32 v1, v1, v17
	v_add_f32_e32 v1, v1, v18
	v_add_f32_e32 v1, v1, v19
	v_add_f32_e32 v1, v1, v20
	v_add_f32_e32 v1, v1, v21
	v_add_f32_e32 v1, v1, v22
	v_add_f32_e32 v1, v1, v23
	v_add_f32_e32 v1, v1, v24
	v_add_f32_e32 v1, v1, v25
	v_add_f32_e32 v1, v1, v26
	v_add_f32_e32 v1, v1, v27
	v_add_f32_e32 v1, v1, v28
	v_add_f32_e32 v1, v1, v29
	v_add_f32_e32 v1, v1, v30
	v_add_f32_e32 v1, v1, v31
	v_add_f32_e32 v1, v1, v32
	v_add_f32_e32 v1, v1, v33
	v_add_f32_e32 v1, v1, v34
	v_add_f32_e32 v1, v1, v35
	v_add_f32_e32 v1, v1, v36
	v_add_f32_e32 v1, v1, v37
	v_add_f32_e32 v1, v1, v38
	v_add_f32_e32 v1, v1, v39
	v_add_f32_e32 v1, v1, v40
	v_add_f32_e32 v1, v1, v41
	v_add_f32_e32 v1, v1, v42
	v_add_f32_e32 v1, v1, v43
	v_add_f32_e32 v1, v1, v44
	v_add_f32_e32 v1, v1, v45
	v_add_f32_e32 v1, v1, v46
	v_add_f32_e32 v1, v1, v47
	v_add_f32_e32 v1, v1, v48
	v_add_f32_e32 v1, v1, v49
	v_add_f32_e32 v1, v1, v50
	v_add_f32_e32 v1, v1, v51
	v_add_f32_e32 v1, v1, v52
	v_add_f32_e32 v1, v1, v53
	v_add_f32_e32 v1, v1, v54
	v_add_f32_e32 v1, v1, v55
	v_add_f32_e32 v1, v1, v56
	v_add_f32_e32 v1, v1, v57
	v_add_f32_e32 v1, v1, v58
	v_add_f32_e32 v1, v1, v59
	v_add_f32_e32 v1, v1, v60
	v_add_f32_e32 v1, v1, v61
	v_add_f32_e32 v1, v1, v62
	v_add_f32_e32 v1, v1, v63
	v_add_f32_e32 v1, v1, v64
	v_add_f32_e32 v1, v1, v65
	v_add_f32_e32 v1, v1, v66
	v_add_f32_e32 v1, v1, v67
	v_add_f32_e32 v1, v1, v68
	v_add_f32_e32 v1, v1, v69
	v_add_f32_e32 v1, v1, v70
	v_add_f32_e32 v1, v1, v71
	v_add_f32_e32 v1, v1, v72
	v_add_f32_e32 v1, v1, v73
	v_add_f32_e32 v1, v1, v74
	v_add_f32_e32 v1, v1, v75
	v_add_f32_e32 v1, v1, v76
	v_add_f32_e32 v1, v1, v77
	v_lshl_add_u64 v[6:7], v[2:3], 2, s[4:5]
	v_add_u32_e32 v2, s6, v2
	v_cmp_lt_i32_e32 vcc, s7, v2
	s_or_b64 s[10:11], vcc, s[10:11]
	v_lshl_add_u64 v[4:5], v[4:5], 0, s[8:9]
	global_store_dword v[6:7], v1, off
	s_andn2_b64 exec, exec, s[10:11]
	s_cbranch_execnz .LBB0_106

;     static __device__ __forceinline__ float f8(unsigned w, int i) { const auto p = (i & 2) ? __builtin_amdgcn_cvt_pk_f32_fp8((int)w, true) : __builtin_amdgcn_cvt_pk_f32_fp8((int)w, false); return (i & 1) ? p[1] : p[0]; }
; #define PG8_WAIT_V(n) asm volatile("s_waitcnt vmcnt(" #n ")" ::: "memory")
;     __device__ __forceinline__ void mid(f32x4 (&acc)[2][2][4][2], const Unit& u, int wr, int wc, int fr, int fq) const {
;         asm volatile("" : "+v"(fr), "+v"(fq));
;         const int row0 = u.pm * BM + wr * 64 + fr, col0 = u.pn * BM + wc * 32 + 8 * fq;
; #pragma unroll
;         for (int ai = 0; ai < 2; ++ai)
; #pragma unroll
;             for (int m = 0; m < 4; ++m) { const unsigned char* zr = Z8 + (size_t)(row0 + ai * HALF + m * 16) * Z8LD + col0;
; #pragma unroll
;                 for (int bj = 0; bj < 2; ++bj) { const uint2 ga2 = *(const uint2*)(zr + zga + bj * HALF), gb2 = *(const uint2*)(zr + zgb + bj * HALF);
; #pragma unroll
;                     for (int n = 0; n < 2; ++n) { f32x4 r; const unsigned wa = n ? ga2.y : ga2.x, wb = n ? gb2.y : gb2.x;
; #pragma unroll
;                         for (int i = 0; i < 4; ++i) { const float xa = f8(wa, i), xb = f8(wb, i);
;                             r[i] = (1.f + __builtin_amdgcn_exp2f(-1.4426950408889634f * fmaxf(xb, -80.f))) * __builtin_amdgcn_rcpf(1.f + __builtin_amdgcn_exp2f(-1.4426950408889634f * fmaxf(xa, -80.f))); }
;                         acc[ai][bj][m][n] *= r; } } }
; template <class Epi, class Sched, bool ALIGN_EPI = false, bool SP2 = false, bool FP8 = false>
; __device__ __forceinline__ void gemm_phase(PG8_LAS unsigned char* lds, const Gemm g, const Sched& S, const Epi& E) {
;     ...
;             if constexpr (Epi::HAS_MID) { if (t == nt / 2) { E.mid(acc, cur, wr, wc, fr, fq); PG8_WAIT_V(0); } }
.LBB0_1048:
	s_cmpk_lg_i32 s26, 0x800
	s_cbranch_scc1 .LBB0_1047
	v_mov_b32_e32 v3, v1
	v_mov_b32_e32 v4, v164
	v_mov_b64_e32 v[154:155], s[8:9]
	v_lshl_add_u32 v4, v4, 3, s17
	v_add_u32_e32 v3, s55, v3
	v_ashrrev_i32_e32 v5, 31, v4
	v_mad_i64_i32 v[156:157], s[28:29], v3, s50, v[154:155]
	v_lshl_add_u64 v[156:157], v[156:157], 0, v[4:5]
	global_load_dwordx2 v[160:161], v[156:157], off offset:2048
	global_load_dwordx2 v[182:183], v[156:157], off offset:2176
	v_add_co_u32_e32 v246, vcc, 0x1000, v156
	s_nop 1
	v_addc_co_u32_e32 v247, vcc, 0, v157, vcc
	global_load_dwordx2 v[184:185], v[246:247], off
	global_load_dwordx2 v[186:187], v[246:247], off offset:128
	v_add_co_u32_e32 v244, vcc, 0x18000, v156
	s_nop 1
	v_addc_co_u32_e32 v245, vcc, 0, v157, vcc
	global_load_dwordx2 v[188:189], v[244:245], off offset:2048
	global_load_dwordx2 v[190:191], v[244:245], off offset:2176
	v_add_co_u32_e32 v246, vcc, 0x1000, v244
	s_nop 1
	v_addc_co_u32_e32 v247, vcc, 0, v245, vcc
	global_load_dwordx2 v[192:193], v[246:247], off
	global_load_dwordx2 v[194:195], v[246:247], off offset:128
	v_add_co_u32_e32 v244, vcc, 0x18000, v244
	s_nop 1
	v_addc_co_u32_e32 v245, vcc, 0, v245, vcc
	global_load_dwordx2 v[196:197], v[244:245], off offset:2048
	global_load_dwordx2 v[198:199], v[244:245], off offset:2176
	v_add_co_u32_e32 v246, vcc, 0x1000, v244
	s_nop 1
	v_addc_co_u32_e32 v247, vcc, 0, v245, vcc
	global_load_dwordx2 v[200:201], v[246:247], off
	global_load_dwordx2 v[202:203], v[246:247], off offset:128
	v_add_co_u32_e32 v244, vcc, 0x18000, v244
	s_nop 1
	v_addc_co_u32_e32 v245, vcc, 0, v245, vcc
	global_load_dwordx2 v[204:205], v[244:245], off offset:2048
	global_load_dwordx2 v[206:207], v[244:245], off offset:2176
	v_add_co_u32_e32 v246, vcc, 0x1000, v244
	s_nop 1
	v_addc_co_u32_e32 v247, vcc, 0, v245, vcc
	global_load_dwordx2 v[208:209], v[246:247], off
	global_load_dwordx2 v[210:211], v[246:247], off offset:128
	v_add_co_u32_e32 v244, vcc, 0xc0000, v156
	s_nop 1
	v_addc_co_u32_e32 v245, vcc, 0, v157, vcc
	global_load_dwordx2 v[212:213], v[244:245], off offset:2048
	global_load_dwordx2 v[214:215], v[244:245], off offset:2176
	v_add_co_u32_e32 v246, vcc, 0x1000, v244
	s_nop 1
	v_addc_co_u32_e32 v247, vcc, 0, v245, vcc
	global_load_dwordx2 v[216:217], v[246:247], off
	global_load_dwordx2 v[218:219], v[246:247], off offset:128
	v_add_co_u32_e32 v244, vcc, 0x18000, v244
	s_nop 1
	v_addc_co_u32_e32 v245, vcc, 0, v245, vcc
	global_load_dwordx2 v[220:221], v[244:245], off offset:2048
	global_load_dwordx2 v[222:223], v[244:245], off offset:2176
	v_add_co_u32_e32 v246, vcc, 0x1000, v244
	s_nop 1
	v_addc_co_u32_e32 v247, vcc, 0, v245, vcc
	global_load_dwordx2 v[224:225], v[246:247], off
	global_load_dwordx2 v[226:227], v[246:247], off offset:128
	v_add_co_u32_e32 v244, vcc, 0x18000, v244
	s_nop 1
	v_addc_co_u32_e32 v245, vcc, 0, v245, vcc
	global_load_dwordx2 v[228:229], v[244:245], off offset:2048
	global_load_dwordx2 v[230:231], v[244:245], off offset:2176
	v_add_co_u32_e32 v246, vcc, 0x1000, v244
	s_nop 1
	v_addc_co_u32_e32 v247, vcc, 0, v245, vcc
	global_load_dwordx2 v[232:233], v[246:247], off
	global_load_dwordx2 v[234:235], v[246:247], off offset:128
	v_add_co_u32_e32 v244, vcc, 0x18000, v244
	s_nop 1
	v_addc_co_u32_e32 v245, vcc, 0, v245, vcc
	global_load_dwordx2 v[236:237], v[244:245], off offset:2048
	global_load_dwordx2 v[238:239], v[244:245], off offset:2176
	v_add_co_u32_e32 v246, vcc, 0x1000, v244
	s_nop 1
	v_addc_co_u32_e32 v247, vcc, 0, v245, vcc
	global_load_dwordx2 v[240:241], v[246:247], off
	global_load_dwordx2 v[242:243], v[246:247], off offset:128
	v_add_co_u32_e32 v158, vcc, 0x1000, v156
	s_waitcnt vmcnt(0)
	v_cvt_pk_f32_fp8_e32 v[168:169], v160
	v_addc_co_u32_e32 v159, vcc, 0, v157, vcc
	v_mov_b64_e32 v[162:163], v[184:185]
	s_nop 0
	v_mov_b64_e32 v[158:159], v[186:187]
	s_nop 0
	v_mov_b64_e32 v[156:157], v[182:183]
	v_cvt_pk_f32_fp8_sdwa v[170:171], v160 src0_sel:WORD_1
	v_cvt_pk_f32_fp8_e32 v[172:173], v161
	v_cvt_pk_f32_fp8_sdwa v[160:161], v161 src0_sel:WORD_1
	v_max_f32_e32 v167, v168, v168
	v_max_f32_e32 v168, v169, v169
	v_max_f32_e32 v169, v170, v170
	v_max_f32_e32 v170, v171, v171
	v_max_f32_e32 v171, v172, v172
	v_max_f32_e32 v172, v173, v173
	v_max_f32_e32 v167, 0xc2a00000, v167
	v_max_f32_e32 v168, 0xc2a00000, v168
	v_max_f32_e32 v169, 0xc2a00000, v169
	v_max_f32_e32 v170, 0xc2a00000, v170
	v_max_f32_e32 v171, 0xc2a00000, v171
	v_max_f32_e32 v172, 0xc2a00000, v172
	v_mul_f32_e32 v167, 0xbfb8aa3b, v167
	v_mul_f32_e32 v168, 0xbfb8aa3b, v168
	v_max_f32_e32 v160, v160, v160
	v_mul_f32_e32 v169, 0xbfb8aa3b, v169
	v_mul_f32_e32 v170, 0xbfb8aa3b, v170
	v_mul_f32_e32 v171, 0xbfb8aa3b, v171
	v_mul_f32_e32 v172, 0xbfb8aa3b, v172
	v_exp_f32_e32 v167, v167
	v_max_f32_e32 v160, 0xc2a00000, v160
	v_exp_f32_e32 v172, v172
	v_mul_f32_e32 v160, 0xbfb8aa3b, v160
	v_add_f32_e32 v167, 1.0, v167
	v_max_f32_e32 v161, v161, v161
	v_max_f32_e32 v161, 0xc2a00000, v161
	v_mul_f32_e32 v161, 0xbfb8aa3b, v161
	s_waitcnt vmcnt(0)
;     static __device__ __forceinline__ float f8(unsigned w, int i) { const auto p = (i & 2) ? __builtin_amdgcn_cvt_pk_f32_fp8((int)w, true) : __builtin_amdgcn_cvt_pk_f32_fp8((int)w, false); return (i & 1) ? p[1] : p[0]; }
;     __device__ __forceinline__ void mid(f32x4 (&acc)[2][2][4][2], const Unit& u, int wr, int wc, int fr, int fq) const {
;     ...
;             for (int m = 0; m < 4; ++m) { const unsigned char* zr = Z8 + (size_t)(row0 + ai * HALF + m * 16) * Z8LD + col0;
; #pragma unroll
;                 for (int bj = 0; bj < 2; ++bj) { const uint2 ga2 = *(const uint2*)(zr + zga + bj * HALF), gb2 = *(const uint2*)(zr + zgb + bj * HALF);
; #pragma unroll
;                     for (int n = 0; n < 2; ++n) { f32x4 r; const unsigned wa = n ? ga2.y : ga2.x, wb = n ? gb2.y : gb2.x;
; #pragma unroll
;                         for (int i = 0; i < 4; ++i) { const float xa = f8(wa, i), xb = f8(wb, i);
;                             r[i] = (1.f + __builtin_amdgcn_exp2f(-1.4426950408889634f * fmaxf(xb, -80.f))) * __builtin_amdgcn_rcpf(1.f + __builtin_amdgcn_exp2f(-1.4426950408889634f * fmaxf(xa, -80.f))); }
;                         acc[ai][bj][m][n] *= r; } } }
	v_cvt_pk_f32_fp8_e32 v[174:175], v162
	v_cvt_pk_f32_fp8_sdwa v[176:177], v162 src0_sel:WORD_1
	v_cvt_pk_f32_fp8_e32 v[178:179], v163
	v_cvt_pk_f32_fp8_sdwa v[162:163], v163 src0_sel:WORD_1
	v_max_f32_e32 v173, v174, v174
	v_max_f32_e32 v174, v175, v175
	v_max_f32_e32 v175, v176, v176
	v_max_f32_e32 v176, v177, v177
	v_max_f32_e32 v177, v178, v178
	v_max_f32_e32 v178, v179, v179
	v_max_f32_e32 v179, v163, v163
	v_max_f32_e32 v163, 0xc2a00000, v173
	v_max_f32_e32 v173, 0xc2a00000, v174
	v_exp_f32_e32 v174, v168
	v_max_f32_e32 v162, v162, v162
	v_max_f32_e32 v168, 0xc2a00000, v175
	v_exp_f32_e32 v175, v169
	v_max_f32_e32 v169, 0xc2a00000, v176
	v_exp_f32_e32 v176, v170
	v_max_f32_e32 v170, 0xc2a00000, v177
	v_exp_f32_e32 v177, v171
	v_max_f32_e32 v162, 0xc2a00000, v162
	v_max_f32_e32 v171, 0xc2a00000, v178
	v_exp_f32_e32 v178, v160
	v_mul_f32_e32 v160, 0xbfb8aa3b, v163
	v_mul_f32_e32 v163, 0xbfb8aa3b, v173
	v_mul_f32_e32 v173, 0xbfb8aa3b, v162
	v_exp_f32_e32 v162, v160
	v_exp_f32_e32 v163, v163
	v_exp_f32_e32 v160, v173
	v_add_f32_e32 v173, 1.0, v174
	v_add_f32_e32 v174, 1.0, v175
	v_add_f32_e32 v175, 1.0, v176
	v_add_f32_e32 v176, 1.0, v177
	v_add_f32_e32 v177, 1.0, v172
	v_rcp_f32_e32 v172, v167
	v_rcp_f32_e32 v173, v173
	v_pk_add_f32 v[162:163], v[162:163], 1.0 op_sel_hi:[1,0]
	v_mul_f32_e32 v168, 0xbfb8aa3b, v168
	v_mul_f32_e32 v169, 0xbfb8aa3b, v169
	v_pk_mul_f32 v[162:163], v[172:173], v[162:163]
	v_exp_f32_e32 v168, v168
	v_exp_f32_e32 v169, v169
	v_pk_mul_f32 v[130:131], v[130:131], v[162:163]
	v_exp_f32_e32 v163, v161
	v_mul_f32_e32 v170, 0xbfb8aa3b, v170
	v_mul_f32_e32 v171, 0xbfb8aa3b, v171
	v_rcp_f32_e32 v174, v174
	v_rcp_f32_e32 v175, v175
	v_exp_f32_e32 v170, v170
	v_exp_f32_e32 v171, v171
	v_max_f32_e32 v162, 0xc2a00000, v179
	v_mul_f32_e32 v161, 0xbfb8aa3b, v162
	v_add_f32_e32 v178, 1.0, v178
	v_pk_add_f32 v[168:169], v[168:169], 1.0 op_sel_hi:[1,0]
	v_exp_f32_e32 v161, v161
	v_add_f32_e32 v163, 1.0, v163
	v_pk_mul_f32 v[168:169], v[174:175], v[168:169]
	v_rcp_f32_e32 v162, v178
	v_rcp_f32_e32 v163, v163
	v_pk_mul_f32 v[132:133], v[132:133], v[168:169]
	v_pk_add_f32 v[168:169], v[170:171], 1.0 op_sel_hi:[1,0]
	v_cvt_pk_f32_fp8_e32 v[170:171], v156
	v_pk_add_f32 v[160:161], v[160:161], 1.0 op_sel_hi:[1,0]
	v_rcp_f32_e32 v176, v176
	v_pk_mul_f32 v[160:161], v[162:163], v[160:161]
	v_cvt_pk_f32_fp8_e32 v[162:163], v158
	v_pk_mul_f32 v[128:129], v[128:129], v[160:161]
	v_max_f32_e32 v161, v170, v170
	v_max_f32_e32 v161, 0xc2a00000, v161
	v_rcp_f32_e32 v177, v177
	v_mul_f32_e32 v161, 0xbfb8aa3b, v161
	v_exp_f32_e32 v161, v161
	v_max_f32_e32 v160, v162, v162
	v_max_f32_e32 v160, 0xc2a00000, v160
	v_pk_mul_f32 v[168:169], v[176:177], v[168:169]
	v_mul_f32_e32 v160, 0xbfb8aa3b, v160
	v_pk_mul_f32 v[126:127], v[126:127], v[168:169]
	v_exp_f32_e32 v168, v160
	v_add_f32_e32 v160, 1.0, v161
	v_rcp_f32_e32 v170, v160
	v_max_f32_e32 v160, v163, v163
	v_max_f32_e32 v160, 0xc2a00000, v160
	v_mul_f32_e32 v160, 0xbfb8aa3b, v160
	v_exp_f32_e32 v169, v160
	v_max_f32_e32 v160, v171, v171
	v_max_f32_e32 v160, 0xc2a00000, v160
	v_mul_f32_e32 v160, 0xbfb8aa3b, v160
	v_cvt_pk_f32_fp8_sdwa v[172:173], v156 src0_sel:WORD_1
	v_add_u32_e32 v156, 16, v3
	v_exp_f32_e32 v167, v160
	v_mad_i64_i32 v[160:161], s[28:29], v156, s50, v[154:155]
	v_lshl_add_u64 v[176:177], v[160:161], 0, v[4:5]
	v_add_co_u32_e32 v178, vcc, s51, v176
	v_cvt_pk_f32_fp8_sdwa v[174:175], v158 src0_sel:WORD_1
	s_nop 0
	v_addc_co_u32_e32 v179, vcc, 0, v177, vcc
	v_mov_b64_e32 v[162:163], v[192:193]
	v_mov_b64_e32 v[160:161], v[188:189]
	v_max_f32_e32 v158, v172, v172
	v_max_f32_e32 v158, 0xc2a00000, v158
	v_mul_f32_e32 v158, 0xbfb8aa3b, v158
	v_add_f32_e32 v156, 1.0, v167
	v_exp_f32_e32 v158, v158
	v_max_f32_e32 v167, v173, v173
	v_rcp_f32_e32 v171, v156
	v_max_f32_e32 v156, v174, v174
	v_max_f32_e32 v167, 0xc2a00000, v167
	v_max_f32_e32 v156, 0xc2a00000, v156
	v_mul_f32_e32 v167, 0xbfb8aa3b, v167
	v_mul_f32_e32 v156, 0xbfb8aa3b, v156
	v_exp_f32_e32 v167, v167
	v_exp_f32_e32 v172, v156
	v_add_f32_e32 v156, 1.0, v158
	v_max_f32_e32 v158, v175, v175
	v_max_f32_e32 v158, 0xc2a00000, v158
	v_mul_f32_e32 v158, 0xbfb8aa3b, v158
	v_exp_f32_e32 v173, v158
	v_rcp_f32_e32 v174, v156
	v_add_f32_e32 v156, 1.0, v167
	v_rcp_f32_e32 v175, v156
	v_pk_add_f32 v[172:173], v[172:173], 1.0 op_sel_hi:[1,0]
	v_pk_add_f32 v[168:169], v[168:169], 1.0 op_sel_hi:[1,0]
	s_nop 0
	v_pk_mul_f32 v[168:169], v[170:171], v[168:169]
	v_pk_mul_f32 v[170:171], v[174:175], v[172:173]
	v_cvt_pk_f32_fp8_e32 v[174:175], v157
	v_cvt_pk_f32_fp8_e32 v[172:173], v159
	v_pk_mul_f32 v[124:125], v[124:125], v[170:171]
	v_cvt_pk_f32_fp8_sdwa v[170:171], v157 src0_sel:WORD_1
	v_max_f32_e32 v158, v174, v174
	v_max_f32_e32 v158, 0xc2a00000, v158
	v_mul_f32_e32 v158, 0xbfb8aa3b, v158
	v_max_f32_e32 v167, v175, v175
	v_exp_f32_e32 v158, v158
	v_max_f32_e32 v167, 0xc2a00000, v167
	v_max_f32_e32 v156, v172, v172
	v_mul_f32_e32 v167, 0xbfb8aa3b, v167
	v_max_f32_e32 v156, 0xc2a00000, v156
	v_exp_f32_e32 v167, v167
	v_mul_f32_e32 v156, 0xbfb8aa3b, v156
	v_pk_mul_f32 v[122:123], v[122:123], v[168:169]
	v_exp_f32_e32 v168, v156
	v_add_f32_e32 v156, 1.0, v158
	v_max_f32_e32 v158, v173, v173
	v_max_f32_e32 v158, 0xc2a00000, v158
	v_mul_f32_e32 v158, 0xbfb8aa3b, v158
	v_add_f32_e32 v157, 1.0, v167
	v_max_f32_e32 v167, v170, v170
	v_exp_f32_e32 v169, v158
	v_cvt_pk_f32_fp8_sdwa v[158:159], v159 src0_sel:WORD_1
	v_max_f32_e32 v167, 0xc2a00000, v167
	v_max_f32_e32 v170, v171, v171
	v_mul_f32_e32 v167, 0xbfb8aa3b, v167
	v_max_f32_e32 v170, 0xc2a00000, v170
	v_exp_f32_e32 v167, v167
	v_mul_f32_e32 v170, 0xbfb8aa3b, v170
	v_exp_f32_e32 v171, v170
	v_max_f32_e32 v158, v158, v158
	v_max_f32_e32 v159, v159, v159
	v_max_f32_e32 v158, 0xc2a00000, v158
	v_max_f32_e32 v159, 0xc2a00000, v159
	v_mul_f32_e32 v158, 0xbfb8aa3b, v158
	v_add_f32_e32 v167, 1.0, v167
	v_mul_f32_e32 v159, 0xbfb8aa3b, v159
	v_exp_f32_e32 v158, v158
	v_exp_f32_e32 v159, v159
	v_rcp_f32_e32 v170, v167
	v_add_f32_e32 v167, 1.0, v171
	v_rcp_f32_e32 v156, v156
	v_rcp_f32_e32 v157, v157
	v_rcp_f32_e32 v171, v167
	v_pk_add_f32 v[158:159], v[158:159], 1.0 op_sel_hi:[1,0]
	v_pk_add_f32 v[168:169], v[168:169], 1.0 op_sel_hi:[1,0]
	v_pk_mul_f32 v[170:171], v[170:171], v[158:159]
	v_pk_mul_f32 v[168:169], v[156:157], v[168:169]
	v_mov_b64_e32 v[158:159], v[194:195]
	v_mov_b64_e32 v[156:157], v[190:191]
	s_waitcnt vmcnt(0)
;     static __device__ __forceinline__ float f8(unsigned w, int i) { const auto p = (i & 2) ? __builtin_amdgcn_cvt_pk_f32_fp8((int)w, true) : __builtin_amdgcn_cvt_pk_f32_fp8((int)w, false); return (i & 1) ? p[1] : p[0]; }
;     __device__ __forceinline__ void mid(f32x4 (&acc)[2][2][4][2], const Unit& u, int wr, int wc, int fr, int fq) const {
;     ...
;             for (int m = 0; m < 4; ++m) { const unsigned char* zr = Z8 + (size_t)(row0 + ai * HALF + m * 16) * Z8LD + col0;
; #pragma unroll
;                 for (int bj = 0; bj < 2; ++bj) { const uint2 ga2 = *(const uint2*)(zr + zga + bj * HALF), gb2 = *(const uint2*)(zr + zgb + bj * HALF);
; #pragma unroll
;                     for (int n = 0; n < 2; ++n) { f32x4 r; const unsigned wa = n ? ga2.y : ga2.x, wb = n ? gb2.y : gb2.x;
; #pragma unroll
;                         for (int i = 0; i < 4; ++i) { const float xa = f8(wa, i), xb = f8(wb, i);
;                             r[i] = (1.f + __builtin_amdgcn_exp2f(-1.4426950408889634f * fmaxf(xb, -80.f))) * __builtin_amdgcn_rcpf(1.f + __builtin_amdgcn_exp2f(-1.4426950408889634f * fmaxf(xa, -80.f))); }
;                         acc[ai][bj][m][n] *= r; } } }
	v_cvt_pk_f32_fp8_e32 v[174:175], v160
	v_cvt_pk_f32_fp8_e32 v[172:173], v162
	v_pk_mul_f32 v[118:119], v[118:119], v[168:169]
	v_pk_mul_f32 v[120:121], v[120:121], v[170:171]
	v_max_f32_e32 v168, v174, v174
	v_max_f32_e32 v168, 0xc2a00000, v168
	v_mul_f32_e32 v168, 0xbfb8aa3b, v168
	v_exp_f32_e32 v169, v168
	v_max_f32_e32 v167, v172, v172
	v_max_f32_e32 v167, 0xc2a00000, v167
	v_mul_f32_e32 v167, 0xbfb8aa3b, v167
	v_exp_f32_e32 v168, v167
	v_add_f32_e32 v167, 1.0, v169
	v_max_f32_e32 v169, v175, v175
	v_cvt_pk_f32_fp8_sdwa v[174:175], v160 src0_sel:WORD_1
	v_max_f32_e32 v169, 0xc2a00000, v169
	v_mul_f32_e32 v169, 0xbfb8aa3b, v169
	v_exp_f32_e32 v171, v169
	v_rcp_f32_e32 v170, v167
	v_max_f32_e32 v167, v173, v173
	v_cvt_pk_f32_fp8_sdwa v[172:173], v162 src0_sel:WORD_1
	v_max_f32_e32 v162, v174, v174
	v_max_f32_e32 v167, 0xc2a00000, v167
	v_max_f32_e32 v162, 0xc2a00000, v162
	v_mul_f32_e32 v167, 0xbfb8aa3b, v167
	v_mul_f32_e32 v162, 0xbfb8aa3b, v162
	v_exp_f32_e32 v169, v167
	v_add_f32_e32 v160, 1.0, v171
	v_exp_f32_e32 v162, v162
	v_max_f32_e32 v167, v175, v175
	v_rcp_f32_e32 v171, v160
	v_max_f32_e32 v160, v172, v172
	v_max_f32_e32 v167, 0xc2a00000, v167
	v_max_f32_e32 v160, 0xc2a00000, v160
	v_mul_f32_e32 v167, 0xbfb8aa3b, v167
	v_mul_f32_e32 v160, 0xbfb8aa3b, v160
	v_exp_f32_e32 v167, v167
	v_exp_f32_e32 v172, v160
	v_add_f32_e32 v160, 1.0, v162
	v_max_f32_e32 v162, v173, v173
	v_max_f32_e32 v162, 0xc2a00000, v162
	v_mul_f32_e32 v162, 0xbfb8aa3b, v162
	v_exp_f32_e32 v173, v162
	v_rcp_f32_e32 v174, v160
	v_add_f32_e32 v160, 1.0, v167
	v_rcp_f32_e32 v175, v160
	v_pk_add_f32 v[172:173], v[172:173], 1.0 op_sel_hi:[1,0]
	v_pk_add_f32 v[168:169], v[168:169], 1.0 op_sel_hi:[1,0]
	s_nop 0
	v_pk_mul_f32 v[168:169], v[170:171], v[168:169]
	v_pk_mul_f32 v[170:171], v[174:175], v[172:173]
	v_cvt_pk_f32_fp8_e32 v[174:175], v161
	v_cvt_pk_f32_fp8_e32 v[172:173], v163
	v_pk_mul_f32 v[116:117], v[116:117], v[170:171]
	v_cvt_pk_f32_fp8_sdwa v[170:171], v161 src0_sel:WORD_1
	v_max_f32_e32 v162, v174, v174
	v_max_f32_e32 v162, 0xc2a00000, v162
	v_mul_f32_e32 v162, 0xbfb8aa3b, v162
	v_max_f32_e32 v167, v175, v175
	v_exp_f32_e32 v162, v162
	v_max_f32_e32 v167, 0xc2a00000, v167
	v_max_f32_e32 v160, v172, v172
	v_mul_f32_e32 v167, 0xbfb8aa3b, v167
	v_max_f32_e32 v160, 0xc2a00000, v160
	v_exp_f32_e32 v167, v167
	v_mul_f32_e32 v160, 0xbfb8aa3b, v160
	v_pk_mul_f32 v[114:115], v[114:115], v[168:169]
	v_exp_f32_e32 v168, v160
	v_add_f32_e32 v160, 1.0, v162
	v_max_f32_e32 v162, v173, v173
	v_max_f32_e32 v162, 0xc2a00000, v162
	v_mul_f32_e32 v162, 0xbfb8aa3b, v162
	v_add_f32_e32 v161, 1.0, v167
	v_max_f32_e32 v167, v170, v170
	v_exp_f32_e32 v169, v162
	v_cvt_pk_f32_fp8_sdwa v[162:163], v163 src0_sel:WORD_1
	v_max_f32_e32 v167, 0xc2a00000, v167
	v_max_f32_e32 v170, v171, v171
	v_mul_f32_e32 v167, 0xbfb8aa3b, v167
	v_max_f32_e32 v170, 0xc2a00000, v170
	v_exp_f32_e32 v167, v167
	v_mul_f32_e32 v170, 0xbfb8aa3b, v170
	v_exp_f32_e32 v171, v170
	v_max_f32_e32 v162, v162, v162
	v_max_f32_e32 v163, v163, v163
	v_max_f32_e32 v162, 0xc2a00000, v162
	v_max_f32_e32 v163, 0xc2a00000, v163
	v_mul_f32_e32 v162, 0xbfb8aa3b, v162
	v_add_f32_e32 v167, 1.0, v167
	v_mul_f32_e32 v163, 0xbfb8aa3b, v163
	v_exp_f32_e32 v162, v162
	v_exp_f32_e32 v163, v163
	v_rcp_f32_e32 v170, v167
	v_add_f32_e32 v167, 1.0, v171
	v_rcp_f32_e32 v171, v167
	v_rcp_f32_e32 v160, v160
	v_rcp_f32_e32 v161, v161
	v_pk_add_f32 v[162:163], v[162:163], 1.0 op_sel_hi:[1,0]
	v_pk_add_f32 v[168:169], v[168:169], 1.0 op_sel_hi:[1,0]
	v_pk_mul_f32 v[162:163], v[170:171], v[162:163]
	v_cvt_pk_f32_fp8_e32 v[170:171], v156
	v_pk_mul_f32 v[160:161], v[160:161], v[168:169]
	v_cvt_pk_f32_fp8_e32 v[168:169], v158
	v_pk_mul_f32 v[110:111], v[110:111], v[160:161]
	v_max_f32_e32 v161, v170, v170
	v_max_f32_e32 v161, 0xc2a00000, v161
	v_mul_f32_e32 v161, 0xbfb8aa3b, v161
	v_exp_f32_e32 v161, v161
	v_max_f32_e32 v160, v168, v168
	v_max_f32_e32 v160, 0xc2a00000, v160
	v_mul_f32_e32 v160, 0xbfb8aa3b, v160
	v_exp_f32_e32 v168, v160
	v_add_f32_e32 v160, 1.0, v161
	v_rcp_f32_e32 v170, v160
	v_max_f32_e32 v160, v169, v169
	v_max_f32_e32 v160, 0xc2a00000, v160
	v_mul_f32_e32 v160, 0xbfb8aa3b, v160
	v_exp_f32_e32 v169, v160
	v_max_f32_e32 v160, v171, v171
	v_max_f32_e32 v160, 0xc2a00000, v160
	v_mul_f32_e32 v160, 0xbfb8aa3b, v160
	v_cvt_pk_f32_fp8_sdwa v[172:173], v156 src0_sel:WORD_1
	v_add_u32_e32 v156, 32, v3
	v_exp_f32_e32 v167, v160
	v_mad_i64_i32 v[160:161], s[28:29], v156, s50, v[154:155]
	v_lshl_add_u64 v[176:177], v[160:161], 0, v[4:5]
	v_add_co_u32_e32 v178, vcc, s51, v176
	v_pk_mul_f32 v[112:113], v[112:113], v[162:163]
	s_nop 0
	v_addc_co_u32_e32 v179, vcc, 0, v177, vcc
	v_mov_b64_e32 v[162:163], v[200:201]
	v_mov_b64_e32 v[160:161], v[196:197]
	v_cvt_pk_f32_fp8_sdwa v[174:175], v158 src0_sel:WORD_1
	v_max_f32_e32 v158, v172, v172
	v_max_f32_e32 v158, 0xc2a00000, v158
	v_mul_f32_e32 v158, 0xbfb8aa3b, v158
	v_add_f32_e32 v156, 1.0, v167
	v_exp_f32_e32 v158, v158
	v_max_f32_e32 v167, v173, v173
	v_rcp_f32_e32 v171, v156
	v_max_f32_e32 v156, v174, v174
	v_max_f32_e32 v167, 0xc2a00000, v167
	v_max_f32_e32 v156, 0xc2a00000, v156
	v_mul_f32_e32 v167, 0xbfb8aa3b, v167
	v_mul_f32_e32 v156, 0xbfb8aa3b, v156
	v_exp_f32_e32 v167, v167
	v_exp_f32_e32 v172, v156
	v_add_f32_e32 v156, 1.0, v158
	v_max_f32_e32 v158, v175, v175
	v_max_f32_e32 v158, 0xc2a00000, v158
	v_mul_f32_e32 v158, 0xbfb8aa3b, v158
	v_exp_f32_e32 v173, v158
	v_rcp_f32_e32 v174, v156
	v_add_f32_e32 v156, 1.0, v167
	v_rcp_f32_e32 v175, v156
	v_pk_add_f32 v[172:173], v[172:173], 1.0 op_sel_hi:[1,0]
	v_pk_add_f32 v[168:169], v[168:169], 1.0 op_sel_hi:[1,0]
	s_nop 0
;     static __device__ __forceinline__ float f8(unsigned w, int i) { const auto p = (i & 2) ? __builtin_amdgcn_cvt_pk_f32_fp8((int)w, true) : __builtin_amdgcn_cvt_pk_f32_fp8((int)w, false); return (i & 1) ? p[1] : p[0]; }
;     __device__ __forceinline__ void mid(f32x4 (&acc)[2][2][4][2], const Unit& u, int wr, int wc, int fr, int fq) const {
;     ...
;             for (int m = 0; m < 4; ++m) { const unsigned char* zr = Z8 + (size_t)(row0 + ai * HALF + m * 16) * Z8LD + col0;
; #pragma unroll
;                 for (int bj = 0; bj < 2; ++bj) { const uint2 ga2 = *(const uint2*)(zr + zga + bj * HALF), gb2 = *(const uint2*)(zr + zgb + bj * HALF);
; #pragma unroll
;                     for (int n = 0; n < 2; ++n) { f32x4 r; const unsigned wa = n ? ga2.y : ga2.x, wb = n ? gb2.y : gb2.x;
; #pragma unroll
;                         for (int i = 0; i < 4; ++i) { const float xa = f8(wa, i), xb = f8(wb, i);
;                             r[i] = (1.f + __builtin_amdgcn_exp2f(-1.4426950408889634f * fmaxf(xb, -80.f))) * __builtin_amdgcn_rcpf(1.f + __builtin_amdgcn_exp2f(-1.4426950408889634f * fmaxf(xa, -80.f))); }
;                         acc[ai][bj][m][n] *= r; } } }
	v_pk_mul_f32 v[168:169], v[170:171], v[168:169]
	v_pk_mul_f32 v[170:171], v[174:175], v[172:173]
	v_cvt_pk_f32_fp8_e32 v[174:175], v157
	v_cvt_pk_f32_fp8_e32 v[172:173], v159
	v_pk_mul_f32 v[108:109], v[108:109], v[170:171]
	v_cvt_pk_f32_fp8_sdwa v[170:171], v157 src0_sel:WORD_1
	v_max_f32_e32 v158, v174, v174
	v_max_f32_e32 v158, 0xc2a00000, v158
	v_mul_f32_e32 v158, 0xbfb8aa3b, v158
	v_max_f32_e32 v167, v175, v175
	v_exp_f32_e32 v158, v158
	v_max_f32_e32 v167, 0xc2a00000, v167
	v_max_f32_e32 v156, v172, v172
	v_mul_f32_e32 v167, 0xbfb8aa3b, v167
	v_max_f32_e32 v156, 0xc2a00000, v156
	v_exp_f32_e32 v167, v167
	v_mul_f32_e32 v156, 0xbfb8aa3b, v156
	v_pk_mul_f32 v[106:107], v[106:107], v[168:169]
	v_exp_f32_e32 v168, v156
	v_add_f32_e32 v156, 1.0, v158
	v_max_f32_e32 v158, v173, v173
	v_max_f32_e32 v158, 0xc2a00000, v158
	v_mul_f32_e32 v158, 0xbfb8aa3b, v158
	v_add_f32_e32 v157, 1.0, v167
	v_max_f32_e32 v167, v170, v170
	v_exp_f32_e32 v169, v158
	v_cvt_pk_f32_fp8_sdwa v[158:159], v159 src0_sel:WORD_1
	v_max_f32_e32 v167, 0xc2a00000, v167
	v_max_f32_e32 v170, v171, v171
	v_mul_f32_e32 v167, 0xbfb8aa3b, v167
	v_max_f32_e32 v170, 0xc2a00000, v170
	v_exp_f32_e32 v167, v167
	v_mul_f32_e32 v170, 0xbfb8aa3b, v170
	v_exp_f32_e32 v171, v170
	v_max_f32_e32 v158, v158, v158
	v_max_f32_e32 v159, v159, v159
	v_max_f32_e32 v158, 0xc2a00000, v158
	v_max_f32_e32 v159, 0xc2a00000, v159
	v_mul_f32_e32 v158, 0xbfb8aa3b, v158
	v_add_f32_e32 v167, 1.0, v167
	v_mul_f32_e32 v159, 0xbfb8aa3b, v159
	v_exp_f32_e32 v158, v158
	v_exp_f32_e32 v159, v159
	v_rcp_f32_e32 v170, v167
	v_add_f32_e32 v167, 1.0, v171
	v_rcp_f32_e32 v156, v156
	v_rcp_f32_e32 v157, v157
	v_rcp_f32_e32 v171, v167
	v_pk_add_f32 v[158:159], v[158:159], 1.0 op_sel_hi:[1,0]
	v_pk_add_f32 v[168:169], v[168:169], 1.0 op_sel_hi:[1,0]
	v_pk_mul_f32 v[170:171], v[170:171], v[158:159]
	v_pk_mul_f32 v[168:169], v[156:157], v[168:169]
	v_mov_b64_e32 v[158:159], v[202:203]
	v_mov_b64_e32 v[156:157], v[198:199]
	s_waitcnt vmcnt(0)
	v_cvt_pk_f32_fp8_e32 v[174:175], v160
	v_cvt_pk_f32_fp8_e32 v[172:173], v162
	v_pk_mul_f32 v[102:103], v[102:103], v[168:169]
	v_pk_mul_f32 v[104:105], v[104:105], v[170:171]
	v_max_f32_e32 v168, v174, v174
	v_max_f32_e32 v168, 0xc2a00000, v168
	v_mul_f32_e32 v168, 0xbfb8aa3b, v168
	v_exp_f32_e32 v169, v168
	v_max_f32_e32 v167, v172, v172
	v_max_f32_e32 v167, 0xc2a00000, v167
	v_mul_f32_e32 v167, 0xbfb8aa3b, v167
	v_exp_f32_e32 v168, v167
	v_add_f32_e32 v167, 1.0, v169
	v_max_f32_e32 v169, v175, v175
	v_cvt_pk_f32_fp8_sdwa v[174:175], v160 src0_sel:WORD_1
	v_max_f32_e32 v169, 0xc2a00000, v169
	v_mul_f32_e32 v169, 0xbfb8aa3b, v169
	v_exp_f32_e32 v171, v169
	v_rcp_f32_e32 v170, v167
	v_max_f32_e32 v167, v173, v173
	v_cvt_pk_f32_fp8_sdwa v[172:173], v162 src0_sel:WORD_1
	v_max_f32_e32 v162, v174, v174
	v_max_f32_e32 v167, 0xc2a00000, v167
	v_max_f32_e32 v162, 0xc2a00000, v162
	v_mul_f32_e32 v167, 0xbfb8aa3b, v167
	v_mul_f32_e32 v162, 0xbfb8aa3b, v162
	v_exp_f32_e32 v169, v167
	v_add_f32_e32 v160, 1.0, v171
	v_exp_f32_e32 v162, v162
	v_max_f32_e32 v167, v175, v175
	v_rcp_f32_e32 v171, v160
	v_max_f32_e32 v160, v172, v172
	v_max_f32_e32 v167, 0xc2a00000, v167
	v_max_f32_e32 v160, 0xc2a00000, v160
	v_mul_f32_e32 v167, 0xbfb8aa3b, v167
	v_mul_f32_e32 v160, 0xbfb8aa3b, v160
	v_exp_f32_e32 v167, v167
	v_exp_f32_e32 v172, v160
	v_add_f32_e32 v160, 1.0, v162
	v_max_f32_e32 v162, v173, v173
	v_max_f32_e32 v162, 0xc2a00000, v162
	v_mul_f32_e32 v162, 0xbfb8aa3b, v162
	v_exp_f32_e32 v173, v162
	v_rcp_f32_e32 v174, v160
	v_add_f32_e32 v160, 1.0, v167
	v_rcp_f32_e32 v175, v160
	v_pk_add_f32 v[172:173], v[172:173], 1.0 op_sel_hi:[1,0]
	v_pk_add_f32 v[168:169], v[168:169], 1.0 op_sel_hi:[1,0]
	s_nop 0
	v_pk_mul_f32 v[168:169], v[170:171], v[168:169]
	v_pk_mul_f32 v[170:171], v[174:175], v[172:173]
	v_cvt_pk_f32_fp8_e32 v[174:175], v161
	v_cvt_pk_f32_fp8_e32 v[172:173], v163
	v_pk_mul_f32 v[100:101], v[100:101], v[170:171]
	v_cvt_pk_f32_fp8_sdwa v[170:171], v161 src0_sel:WORD_1
	v_max_f32_e32 v162, v174, v174
	v_max_f32_e32 v162, 0xc2a00000, v162
	v_mul_f32_e32 v162, 0xbfb8aa3b, v162
	v_max_f32_e32 v167, v175, v175
	v_exp_f32_e32 v162, v162
	v_max_f32_e32 v167, 0xc2a00000, v167
	v_max_f32_e32 v160, v172, v172
	v_mul_f32_e32 v167, 0xbfb8aa3b, v167
	v_max_f32_e32 v160, 0xc2a00000, v160
	v_exp_f32_e32 v167, v167
	v_mul_f32_e32 v160, 0xbfb8aa3b, v160
	v_pk_mul_f32 v[98:99], v[98:99], v[168:169]
	v_exp_f32_e32 v168, v160
	v_add_f32_e32 v160, 1.0, v162
	v_max_f32_e32 v162, v173, v173
	v_max_f32_e32 v162, 0xc2a00000, v162
	v_mul_f32_e32 v162, 0xbfb8aa3b, v162
	v_add_f32_e32 v161, 1.0, v167
	v_max_f32_e32 v167, v170, v170
	v_exp_f32_e32 v169, v162
	v_cvt_pk_f32_fp8_sdwa v[162:163], v163 src0_sel:WORD_1
	v_max_f32_e32 v167, 0xc2a00000, v167
	v_max_f32_e32 v170, v171, v171
	v_mul_f32_e32 v167, 0xbfb8aa3b, v167
	v_max_f32_e32 v170, 0xc2a00000, v170
	v_exp_f32_e32 v167, v167
	v_mul_f32_e32 v170, 0xbfb8aa3b, v170
	v_exp_f32_e32 v171, v170
	v_max_f32_e32 v162, v162, v162
	v_max_f32_e32 v163, v163, v163
	v_max_f32_e32 v162, 0xc2a00000, v162
	v_max_f32_e32 v163, 0xc2a00000, v163
	v_mul_f32_e32 v162, 0xbfb8aa3b, v162
	v_add_f32_e32 v167, 1.0, v167
	v_mul_f32_e32 v163, 0xbfb8aa3b, v163
	v_exp_f32_e32 v162, v162
	v_exp_f32_e32 v163, v163
	v_rcp_f32_e32 v170, v167
	v_add_f32_e32 v167, 1.0, v171
	v_rcp_f32_e32 v171, v167
	v_rcp_f32_e32 v160, v160
	v_rcp_f32_e32 v161, v161
	v_pk_add_f32 v[162:163], v[162:163], 1.0 op_sel_hi:[1,0]
	v_pk_add_f32 v[168:169], v[168:169], 1.0 op_sel_hi:[1,0]
	v_pk_mul_f32 v[162:163], v[170:171], v[162:163]
	v_cvt_pk_f32_fp8_e32 v[170:171], v156
	v_pk_mul_f32 v[160:161], v[160:161], v[168:169]
;     static __device__ __forceinline__ float f8(unsigned w, int i) { const auto p = (i & 2) ? __builtin_amdgcn_cvt_pk_f32_fp8((int)w, true) : __builtin_amdgcn_cvt_pk_f32_fp8((int)w, false); return (i & 1) ? p[1] : p[0]; }
;     __device__ __forceinline__ void mid(f32x4 (&acc)[2][2][4][2], const Unit& u, int wr, int wc, int fr, int fq) const {
;     ...
;             for (int m = 0; m < 4; ++m) { const unsigned char* zr = Z8 + (size_t)(row0 + ai * HALF + m * 16) * Z8LD + col0;
; #pragma unroll
;                 for (int bj = 0; bj < 2; ++bj) { const uint2 ga2 = *(const uint2*)(zr + zga + bj * HALF), gb2 = *(const uint2*)(zr + zgb + bj * HALF);
; #pragma unroll
;                     for (int n = 0; n < 2; ++n) { f32x4 r; const unsigned wa = n ? ga2.y : ga2.x, wb = n ? gb2.y : gb2.x;
; #pragma unroll
;                         for (int i = 0; i < 4; ++i) { const float xa = f8(wa, i), xb = f8(wb, i);
;                             r[i] = (1.f + __builtin_amdgcn_exp2f(-1.4426950408889634f * fmaxf(xb, -80.f))) * __builtin_amdgcn_rcpf(1.f + __builtin_amdgcn_exp2f(-1.4426950408889634f * fmaxf(xa, -80.f))); }
;                         acc[ai][bj][m][n] *= r; } } }
	v_cvt_pk_f32_fp8_e32 v[168:169], v158
	v_pk_mul_f32 v[94:95], v[94:95], v[160:161]
	v_max_f32_e32 v161, v170, v170
	v_max_f32_e32 v161, 0xc2a00000, v161
	v_mul_f32_e32 v161, 0xbfb8aa3b, v161
	v_exp_f32_e32 v161, v161
	v_max_f32_e32 v160, v168, v168
	v_max_f32_e32 v160, 0xc2a00000, v160
	v_mul_f32_e32 v160, 0xbfb8aa3b, v160
	v_exp_f32_e32 v168, v160
	v_add_f32_e32 v160, 1.0, v161
	v_rcp_f32_e32 v170, v160
	v_max_f32_e32 v160, v169, v169
	v_max_f32_e32 v160, 0xc2a00000, v160
	v_mul_f32_e32 v160, 0xbfb8aa3b, v160
	v_exp_f32_e32 v169, v160
	v_max_f32_e32 v160, v171, v171
	v_max_f32_e32 v160, 0xc2a00000, v160
	v_mul_f32_e32 v160, 0xbfb8aa3b, v160
	v_cvt_pk_f32_fp8_sdwa v[172:173], v156 src0_sel:WORD_1
	v_add_u32_e32 v156, 48, v3
	v_exp_f32_e32 v167, v160
	v_mad_i64_i32 v[160:161], s[28:29], v156, s50, v[154:155]
	v_lshl_add_u64 v[176:177], v[160:161], 0, v[4:5]
	v_add_co_u32_e32 v178, vcc, s51, v176
	v_pk_mul_f32 v[96:97], v[96:97], v[162:163]
	s_nop 0
	v_addc_co_u32_e32 v179, vcc, 0, v177, vcc
	v_mov_b64_e32 v[162:163], v[208:209]
	v_mov_b64_e32 v[160:161], v[204:205]
	v_cvt_pk_f32_fp8_sdwa v[174:175], v158 src0_sel:WORD_1
	v_max_f32_e32 v158, v172, v172
	v_max_f32_e32 v158, 0xc2a00000, v158
	v_mul_f32_e32 v158, 0xbfb8aa3b, v158
	v_add_f32_e32 v156, 1.0, v167
	v_exp_f32_e32 v158, v158
	v_max_f32_e32 v167, v173, v173
	v_rcp_f32_e32 v171, v156
	v_max_f32_e32 v156, v174, v174
	v_max_f32_e32 v167, 0xc2a00000, v167
	v_max_f32_e32 v156, 0xc2a00000, v156
	v_mul_f32_e32 v167, 0xbfb8aa3b, v167
	v_mul_f32_e32 v156, 0xbfb8aa3b, v156
	v_exp_f32_e32 v167, v167
	v_exp_f32_e32 v172, v156
	v_add_f32_e32 v156, 1.0, v158
	v_max_f32_e32 v158, v175, v175
	v_max_f32_e32 v158, 0xc2a00000, v158
	v_mul_f32_e32 v158, 0xbfb8aa3b, v158
	v_exp_f32_e32 v173, v158
	v_rcp_f32_e32 v174, v156
	v_add_f32_e32 v156, 1.0, v167
	v_rcp_f32_e32 v175, v156
	v_pk_add_f32 v[172:173], v[172:173], 1.0 op_sel_hi:[1,0]
	v_pk_add_f32 v[168:169], v[168:169], 1.0 op_sel_hi:[1,0]
	s_nop 0
	v_pk_mul_f32 v[168:169], v[170:171], v[168:169]
	v_pk_mul_f32 v[170:171], v[174:175], v[172:173]
	v_cvt_pk_f32_fp8_e32 v[174:175], v157
	v_cvt_pk_f32_fp8_e32 v[172:173], v159
	v_pk_mul_f32 v[92:93], v[92:93], v[170:171]
	v_cvt_pk_f32_fp8_sdwa v[170:171], v157 src0_sel:WORD_1
	v_max_f32_e32 v158, v174, v174
	v_max_f32_e32 v158, 0xc2a00000, v158
	v_mul_f32_e32 v158, 0xbfb8aa3b, v158
	v_max_f32_e32 v167, v175, v175
	v_exp_f32_e32 v158, v158
	v_max_f32_e32 v167, 0xc2a00000, v167
	v_max_f32_e32 v156, v172, v172
	v_mul_f32_e32 v167, 0xbfb8aa3b, v167
	v_max_f32_e32 v156, 0xc2a00000, v156
	v_exp_f32_e32 v167, v167
	v_mul_f32_e32 v156, 0xbfb8aa3b, v156
	v_pk_mul_f32 v[90:91], v[90:91], v[168:169]
	v_exp_f32_e32 v168, v156
	v_add_f32_e32 v156, 1.0, v158
	v_max_f32_e32 v158, v173, v173
	v_max_f32_e32 v158, 0xc2a00000, v158
	v_mul_f32_e32 v158, 0xbfb8aa3b, v158
	v_add_f32_e32 v157, 1.0, v167
	v_max_f32_e32 v167, v170, v170
	v_exp_f32_e32 v169, v158
	v_cvt_pk_f32_fp8_sdwa v[158:159], v159 src0_sel:WORD_1
	v_max_f32_e32 v167, 0xc2a00000, v167
	v_max_f32_e32 v170, v171, v171
	v_mul_f32_e32 v167, 0xbfb8aa3b, v167
	v_max_f32_e32 v170, 0xc2a00000, v170
	v_exp_f32_e32 v167, v167
	v_mul_f32_e32 v170, 0xbfb8aa3b, v170
	v_exp_f32_e32 v171, v170
	v_max_f32_e32 v158, v158, v158
	v_max_f32_e32 v159, v159, v159
	v_max_f32_e32 v158, 0xc2a00000, v158
	v_max_f32_e32 v159, 0xc2a00000, v159
	v_mul_f32_e32 v158, 0xbfb8aa3b, v158
	v_add_f32_e32 v167, 1.0, v167
	v_mul_f32_e32 v159, 0xbfb8aa3b, v159
	v_exp_f32_e32 v158, v158
	v_exp_f32_e32 v159, v159
	v_rcp_f32_e32 v170, v167
	v_add_f32_e32 v167, 1.0, v171
	v_rcp_f32_e32 v156, v156
	v_rcp_f32_e32 v157, v157
	v_rcp_f32_e32 v171, v167
	v_pk_add_f32 v[158:159], v[158:159], 1.0 op_sel_hi:[1,0]
	v_pk_add_f32 v[168:169], v[168:169], 1.0 op_sel_hi:[1,0]
	v_pk_mul_f32 v[170:171], v[170:171], v[158:159]
	v_pk_mul_f32 v[168:169], v[156:157], v[168:169]
	v_mov_b64_e32 v[158:159], v[210:211]
	v_mov_b64_e32 v[156:157], v[206:207]
	s_waitcnt vmcnt(0)
	v_cvt_pk_f32_fp8_e32 v[174:175], v160
	v_cvt_pk_f32_fp8_e32 v[172:173], v162
	v_pk_mul_f32 v[86:87], v[86:87], v[168:169]
	v_pk_mul_f32 v[88:89], v[88:89], v[170:171]
	v_max_f32_e32 v168, v174, v174
	v_max_f32_e32 v168, 0xc2a00000, v168
	v_mul_f32_e32 v168, 0xbfb8aa3b, v168
	v_exp_f32_e32 v169, v168
	v_max_f32_e32 v167, v172, v172
	v_max_f32_e32 v167, 0xc2a00000, v167
	v_mul_f32_e32 v167, 0xbfb8aa3b, v167
	v_exp_f32_e32 v168, v167
	v_add_f32_e32 v167, 1.0, v169
	v_max_f32_e32 v169, v175, v175
	v_cvt_pk_f32_fp8_sdwa v[174:175], v160 src0_sel:WORD_1
	v_max_f32_e32 v169, 0xc2a00000, v169
	v_mul_f32_e32 v169, 0xbfb8aa3b, v169
	v_exp_f32_e32 v171, v169
	v_rcp_f32_e32 v170, v167
	v_max_f32_e32 v167, v173, v173
	v_cvt_pk_f32_fp8_sdwa v[172:173], v162 src0_sel:WORD_1
	v_max_f32_e32 v162, v174, v174
	v_max_f32_e32 v167, 0xc2a00000, v167
	v_max_f32_e32 v162, 0xc2a00000, v162
	v_mul_f32_e32 v167, 0xbfb8aa3b, v167
	v_mul_f32_e32 v162, 0xbfb8aa3b, v162
	v_exp_f32_e32 v169, v167
	v_add_f32_e32 v160, 1.0, v171
	v_exp_f32_e32 v162, v162
	v_max_f32_e32 v167, v175, v175
	v_rcp_f32_e32 v171, v160
	v_max_f32_e32 v160, v172, v172
	v_max_f32_e32 v167, 0xc2a00000, v167
	v_max_f32_e32 v160, 0xc2a00000, v160
	v_mul_f32_e32 v167, 0xbfb8aa3b, v167
	v_mul_f32_e32 v160, 0xbfb8aa3b, v160
	v_exp_f32_e32 v167, v167
	v_exp_f32_e32 v172, v160
	v_add_f32_e32 v160, 1.0, v162
	v_max_f32_e32 v162, v173, v173
	v_max_f32_e32 v162, 0xc2a00000, v162
	v_mul_f32_e32 v162, 0xbfb8aa3b, v162
	v_exp_f32_e32 v173, v162
	v_rcp_f32_e32 v174, v160
	v_add_f32_e32 v160, 1.0, v167
	v_rcp_f32_e32 v175, v160
	v_pk_add_f32 v[172:173], v[172:173], 1.0 op_sel_hi:[1,0]
	v_pk_add_f32 v[168:169], v[168:169], 1.0 op_sel_hi:[1,0]
;     static __device__ __forceinline__ float f8(unsigned w, int i) { const auto p = (i & 2) ? __builtin_amdgcn_cvt_pk_f32_fp8((int)w, true) : __builtin_amdgcn_cvt_pk_f32_fp8((int)w, false); return (i & 1) ? p[1] : p[0]; }
;     __device__ __forceinline__ void mid(f32x4 (&acc)[2][2][4][2], const Unit& u, int wr, int wc, int fr, int fq) const {
;     ...
;             for (int m = 0; m < 4; ++m) { const unsigned char* zr = Z8 + (size_t)(row0 + ai * HALF + m * 16) * Z8LD + col0;
; #pragma unroll
;                 for (int bj = 0; bj < 2; ++bj) { const uint2 ga2 = *(const uint2*)(zr + zga + bj * HALF), gb2 = *(const uint2*)(zr + zgb + bj * HALF);
; #pragma unroll
;                     for (int n = 0; n < 2; ++n) { f32x4 r; const unsigned wa = n ? ga2.y : ga2.x, wb = n ? gb2.y : gb2.x;
; #pragma unroll
;                         for (int i = 0; i < 4; ++i) { const float xa = f8(wa, i), xb = f8(wb, i);
;                             r[i] = (1.f + __builtin_amdgcn_exp2f(-1.4426950408889634f * fmaxf(xb, -80.f))) * __builtin_amdgcn_rcpf(1.f + __builtin_amdgcn_exp2f(-1.4426950408889634f * fmaxf(xa, -80.f))); }
;                         acc[ai][bj][m][n] *= r; } } }
	s_nop 0
	v_pk_mul_f32 v[168:169], v[170:171], v[168:169]
	v_pk_mul_f32 v[170:171], v[174:175], v[172:173]
	v_cvt_pk_f32_fp8_e32 v[174:175], v161
	v_cvt_pk_f32_fp8_e32 v[172:173], v163
	v_pk_mul_f32 v[84:85], v[84:85], v[170:171]
	v_cvt_pk_f32_fp8_sdwa v[170:171], v161 src0_sel:WORD_1
	v_max_f32_e32 v162, v174, v174
	v_max_f32_e32 v162, 0xc2a00000, v162
	v_mul_f32_e32 v162, 0xbfb8aa3b, v162
	v_max_f32_e32 v167, v175, v175
	v_exp_f32_e32 v162, v162
	v_max_f32_e32 v167, 0xc2a00000, v167
	v_max_f32_e32 v160, v172, v172
	v_mul_f32_e32 v167, 0xbfb8aa3b, v167
	v_max_f32_e32 v160, 0xc2a00000, v160
	v_exp_f32_e32 v167, v167
	v_mul_f32_e32 v160, 0xbfb8aa3b, v160
	v_pk_mul_f32 v[82:83], v[82:83], v[168:169]
	v_exp_f32_e32 v168, v160
	v_add_f32_e32 v160, 1.0, v162
	v_max_f32_e32 v162, v173, v173
	v_max_f32_e32 v162, 0xc2a00000, v162
	v_mul_f32_e32 v162, 0xbfb8aa3b, v162
	v_add_f32_e32 v161, 1.0, v167
	v_max_f32_e32 v167, v170, v170
	v_exp_f32_e32 v169, v162
	v_cvt_pk_f32_fp8_sdwa v[162:163], v163 src0_sel:WORD_1
	v_max_f32_e32 v167, 0xc2a00000, v167
	v_max_f32_e32 v170, v171, v171
	v_mul_f32_e32 v167, 0xbfb8aa3b, v167
	v_max_f32_e32 v170, 0xc2a00000, v170
	v_exp_f32_e32 v167, v167
	v_mul_f32_e32 v170, 0xbfb8aa3b, v170
	v_exp_f32_e32 v171, v170
	v_max_f32_e32 v162, v162, v162
	v_max_f32_e32 v163, v163, v163
	v_max_f32_e32 v162, 0xc2a00000, v162
	v_max_f32_e32 v163, 0xc2a00000, v163
	v_mul_f32_e32 v162, 0xbfb8aa3b, v162
	v_add_f32_e32 v167, 1.0, v167
	v_mul_f32_e32 v163, 0xbfb8aa3b, v163
	v_exp_f32_e32 v162, v162
	v_exp_f32_e32 v163, v163
	v_rcp_f32_e32 v170, v167
	v_add_f32_e32 v167, 1.0, v171
	v_rcp_f32_e32 v171, v167
	v_rcp_f32_e32 v160, v160
	v_rcp_f32_e32 v161, v161
	v_pk_add_f32 v[162:163], v[162:163], 1.0 op_sel_hi:[1,0]
	v_pk_add_f32 v[168:169], v[168:169], 1.0 op_sel_hi:[1,0]
	v_pk_mul_f32 v[162:163], v[170:171], v[162:163]
	v_cvt_pk_f32_fp8_e32 v[170:171], v156
	v_pk_mul_f32 v[160:161], v[160:161], v[168:169]
	v_cvt_pk_f32_fp8_e32 v[168:169], v158
	v_pk_mul_f32 v[78:79], v[78:79], v[160:161]
	v_max_f32_e32 v161, v170, v170
	v_max_f32_e32 v161, 0xc2a00000, v161
	v_mul_f32_e32 v161, 0xbfb8aa3b, v161
	v_exp_f32_e32 v161, v161
	v_max_f32_e32 v160, v168, v168
	v_max_f32_e32 v160, 0xc2a00000, v160
	v_mul_f32_e32 v160, 0xbfb8aa3b, v160
	v_exp_f32_e32 v168, v160
	v_add_f32_e32 v160, 1.0, v161
	v_rcp_f32_e32 v170, v160
	v_max_f32_e32 v160, v169, v169
	v_max_f32_e32 v160, 0xc2a00000, v160
	v_mul_f32_e32 v160, 0xbfb8aa3b, v160
	v_exp_f32_e32 v169, v160
	v_max_f32_e32 v160, v171, v171
	v_max_f32_e32 v160, 0xc2a00000, v160
	v_mul_f32_e32 v160, 0xbfb8aa3b, v160
	v_cvt_pk_f32_fp8_sdwa v[172:173], v156 src0_sel:WORD_1
	v_add_u32_e32 v156, 0x80, v3
	v_exp_f32_e32 v167, v160
	v_mad_i64_i32 v[160:161], s[28:29], v156, s50, v[154:155]
	v_lshl_add_u64 v[176:177], v[160:161], 0, v[4:5]
	v_add_co_u32_e32 v178, vcc, s51, v176
	v_pk_mul_f32 v[80:81], v[80:81], v[162:163]
	s_nop 0
	v_addc_co_u32_e32 v179, vcc, 0, v177, vcc
	v_mov_b64_e32 v[162:163], v[216:217]
	v_mov_b64_e32 v[160:161], v[212:213]
	v_cvt_pk_f32_fp8_sdwa v[174:175], v158 src0_sel:WORD_1
	v_max_f32_e32 v158, v172, v172
	v_max_f32_e32 v158, 0xc2a00000, v158
	v_mul_f32_e32 v158, 0xbfb8aa3b, v158
	v_add_f32_e32 v156, 1.0, v167
	v_exp_f32_e32 v158, v158
	v_max_f32_e32 v167, v173, v173
	v_rcp_f32_e32 v171, v156
	v_max_f32_e32 v156, v174, v174
	v_max_f32_e32 v167, 0xc2a00000, v167
	v_max_f32_e32 v156, 0xc2a00000, v156
	v_mul_f32_e32 v167, 0xbfb8aa3b, v167
	v_mul_f32_e32 v156, 0xbfb8aa3b, v156
	v_exp_f32_e32 v167, v167
	v_exp_f32_e32 v172, v156
	v_add_f32_e32 v156, 1.0, v158
	v_max_f32_e32 v158, v175, v175
	v_max_f32_e32 v158, 0xc2a00000, v158
	v_mul_f32_e32 v158, 0xbfb8aa3b, v158
	v_exp_f32_e32 v173, v158
	v_rcp_f32_e32 v174, v156
	v_add_f32_e32 v156, 1.0, v167
	v_rcp_f32_e32 v175, v156
	v_pk_add_f32 v[172:173], v[172:173], 1.0 op_sel_hi:[1,0]
	v_pk_add_f32 v[168:169], v[168:169], 1.0 op_sel_hi:[1,0]
	s_nop 0
	v_pk_mul_f32 v[168:169], v[170:171], v[168:169]
	v_pk_mul_f32 v[170:171], v[174:175], v[172:173]
	v_cvt_pk_f32_fp8_e32 v[174:175], v157
	v_cvt_pk_f32_fp8_e32 v[172:173], v159
	v_pk_mul_f32 v[76:77], v[76:77], v[170:171]
	v_cvt_pk_f32_fp8_sdwa v[170:171], v157 src0_sel:WORD_1
	v_max_f32_e32 v158, v174, v174
	v_max_f32_e32 v158, 0xc2a00000, v158
	v_mul_f32_e32 v158, 0xbfb8aa3b, v158
	v_max_f32_e32 v167, v175, v175
	v_exp_f32_e32 v158, v158
	v_max_f32_e32 v167, 0xc2a00000, v167
	v_max_f32_e32 v156, v172, v172
	v_mul_f32_e32 v167, 0xbfb8aa3b, v167
	v_max_f32_e32 v156, 0xc2a00000, v156
	v_exp_f32_e32 v167, v167
	v_mul_f32_e32 v156, 0xbfb8aa3b, v156
	v_pk_mul_f32 v[74:75], v[74:75], v[168:169]
	v_exp_f32_e32 v168, v156
	v_add_f32_e32 v156, 1.0, v158
	v_max_f32_e32 v158, v173, v173
	v_max_f32_e32 v158, 0xc2a00000, v158
	v_mul_f32_e32 v158, 0xbfb8aa3b, v158
	v_add_f32_e32 v157, 1.0, v167
	v_max_f32_e32 v167, v170, v170
	v_exp_f32_e32 v169, v158
	v_cvt_pk_f32_fp8_sdwa v[158:159], v159 src0_sel:WORD_1
	v_max_f32_e32 v167, 0xc2a00000, v167
	v_max_f32_e32 v170, v171, v171
	v_mul_f32_e32 v167, 0xbfb8aa3b, v167
	v_max_f32_e32 v170, 0xc2a00000, v170
	v_exp_f32_e32 v167, v167
	v_mul_f32_e32 v170, 0xbfb8aa3b, v170
	v_exp_f32_e32 v171, v170
	v_max_f32_e32 v158, v158, v158
	v_max_f32_e32 v159, v159, v159
	v_max_f32_e32 v158, 0xc2a00000, v158
	v_max_f32_e32 v159, 0xc2a00000, v159
	v_mul_f32_e32 v158, 0xbfb8aa3b, v158
	v_add_f32_e32 v167, 1.0, v167
	v_mul_f32_e32 v159, 0xbfb8aa3b, v159
	v_exp_f32_e32 v158, v158
	v_exp_f32_e32 v159, v159
	v_rcp_f32_e32 v170, v167
	v_add_f32_e32 v167, 1.0, v171
	v_rcp_f32_e32 v156, v156
	v_rcp_f32_e32 v157, v157
	v_rcp_f32_e32 v171, v167
	v_pk_add_f32 v[158:159], v[158:159], 1.0 op_sel_hi:[1,0]
	v_pk_add_f32 v[168:169], v[168:169], 1.0 op_sel_hi:[1,0]
	v_pk_mul_f32 v[170:171], v[170:171], v[158:159]
	v_pk_mul_f32 v[168:169], v[156:157], v[168:169]
	v_mov_b64_e32 v[158:159], v[218:219]
	v_mov_b64_e32 v[156:157], v[214:215]
	s_waitcnt vmcnt(0)
;     static __device__ __forceinline__ float f8(unsigned w, int i) { const auto p = (i & 2) ? __builtin_amdgcn_cvt_pk_f32_fp8((int)w, true) : __builtin_amdgcn_cvt_pk_f32_fp8((int)w, false); return (i & 1) ? p[1] : p[0]; }
;     __device__ __forceinline__ void mid(f32x4 (&acc)[2][2][4][2], const Unit& u, int wr, int wc, int fr, int fq) const {
;     ...
;             for (int m = 0; m < 4; ++m) { const unsigned char* zr = Z8 + (size_t)(row0 + ai * HALF + m * 16) * Z8LD + col0;
; #pragma unroll
;                 for (int bj = 0; bj < 2; ++bj) { const uint2 ga2 = *(const uint2*)(zr + zga + bj * HALF), gb2 = *(const uint2*)(zr + zgb + bj * HALF);
; #pragma unroll
;                     for (int n = 0; n < 2; ++n) { f32x4 r; const unsigned wa = n ? ga2.y : ga2.x, wb = n ? gb2.y : gb2.x;
; #pragma unroll
;                         for (int i = 0; i < 4; ++i) { const float xa = f8(wa, i), xb = f8(wb, i);
;                             r[i] = (1.f + __builtin_amdgcn_exp2f(-1.4426950408889634f * fmaxf(xb, -80.f))) * __builtin_amdgcn_rcpf(1.f + __builtin_amdgcn_exp2f(-1.4426950408889634f * fmaxf(xa, -80.f))); }
;                         acc[ai][bj][m][n] *= r; } } }
	v_cvt_pk_f32_fp8_e32 v[174:175], v160
	v_cvt_pk_f32_fp8_e32 v[172:173], v162
	v_pk_mul_f32 v[70:71], v[70:71], v[168:169]
	v_pk_mul_f32 v[72:73], v[72:73], v[170:171]
	v_max_f32_e32 v168, v174, v174
	v_max_f32_e32 v168, 0xc2a00000, v168
	v_mul_f32_e32 v168, 0xbfb8aa3b, v168
	v_exp_f32_e32 v169, v168
	v_max_f32_e32 v167, v172, v172
	v_max_f32_e32 v167, 0xc2a00000, v167
	v_mul_f32_e32 v167, 0xbfb8aa3b, v167
	v_exp_f32_e32 v168, v167
	v_add_f32_e32 v167, 1.0, v169
	v_max_f32_e32 v169, v175, v175
	v_cvt_pk_f32_fp8_sdwa v[174:175], v160 src0_sel:WORD_1
	v_max_f32_e32 v169, 0xc2a00000, v169
	v_mul_f32_e32 v169, 0xbfb8aa3b, v169
	v_exp_f32_e32 v171, v169
	v_rcp_f32_e32 v170, v167
	v_max_f32_e32 v167, v173, v173
	v_cvt_pk_f32_fp8_sdwa v[172:173], v162 src0_sel:WORD_1
	v_max_f32_e32 v162, v174, v174
	v_max_f32_e32 v167, 0xc2a00000, v167
	v_max_f32_e32 v162, 0xc2a00000, v162
	v_mul_f32_e32 v167, 0xbfb8aa3b, v167
	v_mul_f32_e32 v162, 0xbfb8aa3b, v162
	v_exp_f32_e32 v169, v167
	v_add_f32_e32 v160, 1.0, v171
	v_exp_f32_e32 v162, v162
	v_max_f32_e32 v167, v175, v175
	v_rcp_f32_e32 v171, v160
	v_max_f32_e32 v160, v172, v172
	v_max_f32_e32 v167, 0xc2a00000, v167
	v_max_f32_e32 v160, 0xc2a00000, v160
	v_mul_f32_e32 v167, 0xbfb8aa3b, v167
	v_mul_f32_e32 v160, 0xbfb8aa3b, v160
	v_exp_f32_e32 v167, v167
	v_exp_f32_e32 v172, v160
	v_add_f32_e32 v160, 1.0, v162
	v_max_f32_e32 v162, v173, v173
	v_max_f32_e32 v162, 0xc2a00000, v162
	v_mul_f32_e32 v162, 0xbfb8aa3b, v162
	v_exp_f32_e32 v173, v162
	v_rcp_f32_e32 v174, v160
	v_add_f32_e32 v160, 1.0, v167
	v_rcp_f32_e32 v175, v160
	v_pk_add_f32 v[172:173], v[172:173], 1.0 op_sel_hi:[1,0]
	v_pk_add_f32 v[168:169], v[168:169], 1.0 op_sel_hi:[1,0]
	s_nop 0
	v_pk_mul_f32 v[168:169], v[170:171], v[168:169]
	v_pk_mul_f32 v[170:171], v[174:175], v[172:173]
	v_cvt_pk_f32_fp8_e32 v[174:175], v161
	v_cvt_pk_f32_fp8_e32 v[172:173], v163
	v_pk_mul_f32 v[68:69], v[68:69], v[170:171]
	v_cvt_pk_f32_fp8_sdwa v[170:171], v161 src0_sel:WORD_1
	v_max_f32_e32 v162, v174, v174
	v_max_f32_e32 v162, 0xc2a00000, v162
	v_mul_f32_e32 v162, 0xbfb8aa3b, v162
	v_max_f32_e32 v167, v175, v175
	v_exp_f32_e32 v162, v162
	v_max_f32_e32 v167, 0xc2a00000, v167
	v_max_f32_e32 v160, v172, v172
	v_mul_f32_e32 v167, 0xbfb8aa3b, v167
	v_max_f32_e32 v160, 0xc2a00000, v160
	v_exp_f32_e32 v167, v167
	v_mul_f32_e32 v160, 0xbfb8aa3b, v160
	v_pk_mul_f32 v[66:67], v[66:67], v[168:169]
	v_exp_f32_e32 v168, v160
	v_add_f32_e32 v160, 1.0, v162
	v_max_f32_e32 v162, v173, v173
	v_max_f32_e32 v162, 0xc2a00000, v162
	v_mul_f32_e32 v162, 0xbfb8aa3b, v162
	v_add_f32_e32 v161, 1.0, v167
	v_max_f32_e32 v167, v170, v170
	v_exp_f32_e32 v169, v162
	v_cvt_pk_f32_fp8_sdwa v[162:163], v163 src0_sel:WORD_1
	v_max_f32_e32 v167, 0xc2a00000, v167
	v_max_f32_e32 v170, v171, v171
	v_mul_f32_e32 v167, 0xbfb8aa3b, v167
	v_max_f32_e32 v170, 0xc2a00000, v170
	v_exp_f32_e32 v167, v167
	v_mul_f32_e32 v170, 0xbfb8aa3b, v170
	v_exp_f32_e32 v171, v170
	v_max_f32_e32 v162, v162, v162
	v_max_f32_e32 v163, v163, v163
	v_max_f32_e32 v162, 0xc2a00000, v162
	v_max_f32_e32 v163, 0xc2a00000, v163
	v_mul_f32_e32 v162, 0xbfb8aa3b, v162
	v_add_f32_e32 v167, 1.0, v167
	v_mul_f32_e32 v163, 0xbfb8aa3b, v163
	v_exp_f32_e32 v162, v162
	v_exp_f32_e32 v163, v163
	v_rcp_f32_e32 v170, v167
	v_add_f32_e32 v167, 1.0, v171
	v_rcp_f32_e32 v171, v167
	v_rcp_f32_e32 v160, v160
	v_rcp_f32_e32 v161, v161
	v_pk_add_f32 v[162:163], v[162:163], 1.0 op_sel_hi:[1,0]
	v_pk_add_f32 v[168:169], v[168:169], 1.0 op_sel_hi:[1,0]
	v_pk_mul_f32 v[162:163], v[170:171], v[162:163]
	v_cvt_pk_f32_fp8_e32 v[170:171], v156
	v_pk_mul_f32 v[160:161], v[160:161], v[168:169]
	v_cvt_pk_f32_fp8_e32 v[168:169], v158
	v_pk_mul_f32 v[62:63], v[62:63], v[160:161]
	v_max_f32_e32 v161, v170, v170
	v_max_f32_e32 v161, 0xc2a00000, v161
	v_mul_f32_e32 v161, 0xbfb8aa3b, v161
	v_exp_f32_e32 v161, v161
	v_max_f32_e32 v160, v168, v168
	v_max_f32_e32 v160, 0xc2a00000, v160
	v_mul_f32_e32 v160, 0xbfb8aa3b, v160
	v_exp_f32_e32 v168, v160
	v_add_f32_e32 v160, 1.0, v161
	v_rcp_f32_e32 v170, v160
	v_max_f32_e32 v160, v169, v169
	v_max_f32_e32 v160, 0xc2a00000, v160
	v_mul_f32_e32 v160, 0xbfb8aa3b, v160
	v_exp_f32_e32 v169, v160
	v_max_f32_e32 v160, v171, v171
	v_max_f32_e32 v160, 0xc2a00000, v160
	v_mul_f32_e32 v160, 0xbfb8aa3b, v160
	v_cvt_pk_f32_fp8_sdwa v[172:173], v156 src0_sel:WORD_1
	v_add_u32_e32 v156, 0x90, v3
	v_exp_f32_e32 v167, v160
	v_mad_i64_i32 v[160:161], s[28:29], v156, s50, v[154:155]
	v_lshl_add_u64 v[176:177], v[160:161], 0, v[4:5]
	v_add_co_u32_e32 v178, vcc, s51, v176
	v_pk_mul_f32 v[64:65], v[64:65], v[162:163]
	s_nop 0
	v_addc_co_u32_e32 v179, vcc, 0, v177, vcc
	v_mov_b64_e32 v[162:163], v[224:225]
	v_mov_b64_e32 v[160:161], v[220:221]
	v_cvt_pk_f32_fp8_sdwa v[174:175], v158 src0_sel:WORD_1
	v_max_f32_e32 v158, v172, v172
	v_max_f32_e32 v158, 0xc2a00000, v158
	v_mul_f32_e32 v158, 0xbfb8aa3b, v158
	v_add_f32_e32 v156, 1.0, v167
	v_exp_f32_e32 v158, v158
	v_max_f32_e32 v167, v173, v173
	v_rcp_f32_e32 v171, v156
	v_max_f32_e32 v156, v174, v174
	v_max_f32_e32 v167, 0xc2a00000, v167
	v_max_f32_e32 v156, 0xc2a00000, v156
	v_mul_f32_e32 v167, 0xbfb8aa3b, v167
	v_mul_f32_e32 v156, 0xbfb8aa3b, v156
	v_exp_f32_e32 v167, v167
	v_exp_f32_e32 v172, v156
	v_add_f32_e32 v156, 1.0, v158
	v_max_f32_e32 v158, v175, v175
	v_max_f32_e32 v158, 0xc2a00000, v158
	v_mul_f32_e32 v158, 0xbfb8aa3b, v158
	v_exp_f32_e32 v173, v158
	v_rcp_f32_e32 v174, v156
	v_add_f32_e32 v156, 1.0, v167
	v_rcp_f32_e32 v175, v156
	v_pk_add_f32 v[172:173], v[172:173], 1.0 op_sel_hi:[1,0]
	v_pk_add_f32 v[168:169], v[168:169], 1.0 op_sel_hi:[1,0]
	s_nop 0
	v_pk_mul_f32 v[168:169], v[170:171], v[168:169]
;     static __device__ __forceinline__ float f8(unsigned w, int i) { const auto p = (i & 2) ? __builtin_amdgcn_cvt_pk_f32_fp8((int)w, true) : __builtin_amdgcn_cvt_pk_f32_fp8((int)w, false); return (i & 1) ? p[1] : p[0]; }
;     __device__ __forceinline__ void mid(f32x4 (&acc)[2][2][4][2], const Unit& u, int wr, int wc, int fr, int fq) const {
;     ...
;             for (int m = 0; m < 4; ++m) { const unsigned char* zr = Z8 + (size_t)(row0 + ai * HALF + m * 16) * Z8LD + col0;
; #pragma unroll
;                 for (int bj = 0; bj < 2; ++bj) { const uint2 ga2 = *(const uint2*)(zr + zga + bj * HALF), gb2 = *(const uint2*)(zr + zgb + bj * HALF);
; #pragma unroll
;                     for (int n = 0; n < 2; ++n) { f32x4 r; const unsigned wa = n ? ga2.y : ga2.x, wb = n ? gb2.y : gb2.x;
; #pragma unroll
;                         for (int i = 0; i < 4; ++i) { const float xa = f8(wa, i), xb = f8(wb, i);
;                             r[i] = (1.f + __builtin_amdgcn_exp2f(-1.4426950408889634f * fmaxf(xb, -80.f))) * __builtin_amdgcn_rcpf(1.f + __builtin_amdgcn_exp2f(-1.4426950408889634f * fmaxf(xa, -80.f))); }
;                         acc[ai][bj][m][n] *= r; } } }
	v_pk_mul_f32 v[170:171], v[174:175], v[172:173]
	v_cvt_pk_f32_fp8_e32 v[174:175], v157
	v_cvt_pk_f32_fp8_e32 v[172:173], v159
	v_pk_mul_f32 v[60:61], v[60:61], v[170:171]
	v_cvt_pk_f32_fp8_sdwa v[170:171], v157 src0_sel:WORD_1
	v_max_f32_e32 v158, v174, v174
	v_max_f32_e32 v158, 0xc2a00000, v158
	v_mul_f32_e32 v158, 0xbfb8aa3b, v158
	v_max_f32_e32 v167, v175, v175
	v_exp_f32_e32 v158, v158
	v_max_f32_e32 v167, 0xc2a00000, v167
	v_max_f32_e32 v156, v172, v172
	v_mul_f32_e32 v167, 0xbfb8aa3b, v167
	v_max_f32_e32 v156, 0xc2a00000, v156
	v_exp_f32_e32 v167, v167
	v_mul_f32_e32 v156, 0xbfb8aa3b, v156
	v_pk_mul_f32 v[58:59], v[58:59], v[168:169]
	v_exp_f32_e32 v168, v156
	v_add_f32_e32 v156, 1.0, v158
	v_max_f32_e32 v158, v173, v173
	v_max_f32_e32 v158, 0xc2a00000, v158
	v_mul_f32_e32 v158, 0xbfb8aa3b, v158
	v_add_f32_e32 v157, 1.0, v167
	v_max_f32_e32 v167, v170, v170
	v_exp_f32_e32 v169, v158
	v_cvt_pk_f32_fp8_sdwa v[158:159], v159 src0_sel:WORD_1
	v_max_f32_e32 v167, 0xc2a00000, v167
	v_max_f32_e32 v170, v171, v171
	v_mul_f32_e32 v167, 0xbfb8aa3b, v167
	v_max_f32_e32 v170, 0xc2a00000, v170
	v_exp_f32_e32 v167, v167
	v_mul_f32_e32 v170, 0xbfb8aa3b, v170
	v_exp_f32_e32 v171, v170
	v_max_f32_e32 v158, v158, v158
	v_max_f32_e32 v159, v159, v159
	v_max_f32_e32 v158, 0xc2a00000, v158
	v_max_f32_e32 v159, 0xc2a00000, v159
	v_mul_f32_e32 v158, 0xbfb8aa3b, v158
	v_add_f32_e32 v167, 1.0, v167
	v_mul_f32_e32 v159, 0xbfb8aa3b, v159
	v_exp_f32_e32 v158, v158
	v_exp_f32_e32 v159, v159
	v_rcp_f32_e32 v170, v167
	v_add_f32_e32 v167, 1.0, v171
	v_rcp_f32_e32 v156, v156
	v_rcp_f32_e32 v157, v157
	v_rcp_f32_e32 v171, v167
	v_pk_add_f32 v[158:159], v[158:159], 1.0 op_sel_hi:[1,0]
	v_pk_add_f32 v[168:169], v[168:169], 1.0 op_sel_hi:[1,0]
	v_pk_mul_f32 v[170:171], v[170:171], v[158:159]
	v_pk_mul_f32 v[168:169], v[156:157], v[168:169]
	v_mov_b64_e32 v[158:159], v[226:227]
	v_mov_b64_e32 v[156:157], v[222:223]
	s_waitcnt vmcnt(0)
	v_cvt_pk_f32_fp8_e32 v[174:175], v160
	v_cvt_pk_f32_fp8_e32 v[172:173], v162
	v_pk_mul_f32 v[54:55], v[54:55], v[168:169]
	v_pk_mul_f32 v[56:57], v[56:57], v[170:171]
	v_max_f32_e32 v168, v174, v174
	v_max_f32_e32 v168, 0xc2a00000, v168
	v_mul_f32_e32 v168, 0xbfb8aa3b, v168
	v_exp_f32_e32 v169, v168
	v_max_f32_e32 v167, v172, v172
	v_max_f32_e32 v167, 0xc2a00000, v167
	v_mul_f32_e32 v167, 0xbfb8aa3b, v167
	v_exp_f32_e32 v168, v167
	v_add_f32_e32 v167, 1.0, v169
	v_max_f32_e32 v169, v175, v175
	v_cvt_pk_f32_fp8_sdwa v[174:175], v160 src0_sel:WORD_1
	v_max_f32_e32 v169, 0xc2a00000, v169
	v_mul_f32_e32 v169, 0xbfb8aa3b, v169
	v_exp_f32_e32 v171, v169
	v_rcp_f32_e32 v170, v167
	v_max_f32_e32 v167, v173, v173
	v_cvt_pk_f32_fp8_sdwa v[172:173], v162 src0_sel:WORD_1
	v_max_f32_e32 v162, v174, v174
	v_max_f32_e32 v167, 0xc2a00000, v167
	v_max_f32_e32 v162, 0xc2a00000, v162
	v_mul_f32_e32 v167, 0xbfb8aa3b, v167
	v_mul_f32_e32 v162, 0xbfb8aa3b, v162
	v_exp_f32_e32 v169, v167
	v_add_f32_e32 v160, 1.0, v171
	v_exp_f32_e32 v162, v162
	v_max_f32_e32 v167, v175, v175
	v_rcp_f32_e32 v171, v160
	v_max_f32_e32 v160, v172, v172
	v_max_f32_e32 v167, 0xc2a00000, v167
	v_max_f32_e32 v160, 0xc2a00000, v160
	v_mul_f32_e32 v167, 0xbfb8aa3b, v167
	v_mul_f32_e32 v160, 0xbfb8aa3b, v160
	v_exp_f32_e32 v167, v167
	v_exp_f32_e32 v172, v160
	v_add_f32_e32 v160, 1.0, v162
	v_max_f32_e32 v162, v173, v173
	v_max_f32_e32 v162, 0xc2a00000, v162
	v_mul_f32_e32 v162, 0xbfb8aa3b, v162
	v_exp_f32_e32 v173, v162
	v_rcp_f32_e32 v174, v160
	v_add_f32_e32 v160, 1.0, v167
	v_rcp_f32_e32 v175, v160
	v_pk_add_f32 v[172:173], v[172:173], 1.0 op_sel_hi:[1,0]
	v_pk_add_f32 v[168:169], v[168:169], 1.0 op_sel_hi:[1,0]
	s_nop 0
	v_pk_mul_f32 v[168:169], v[170:171], v[168:169]
	v_pk_mul_f32 v[170:171], v[174:175], v[172:173]
	v_cvt_pk_f32_fp8_e32 v[174:175], v161
	v_cvt_pk_f32_fp8_e32 v[172:173], v163
	v_pk_mul_f32 v[52:53], v[52:53], v[170:171]
	v_cvt_pk_f32_fp8_sdwa v[170:171], v161 src0_sel:WORD_1
	v_max_f32_e32 v162, v174, v174
	v_max_f32_e32 v162, 0xc2a00000, v162
	v_mul_f32_e32 v162, 0xbfb8aa3b, v162
	v_max_f32_e32 v167, v175, v175
	v_exp_f32_e32 v162, v162
	v_max_f32_e32 v167, 0xc2a00000, v167
	v_max_f32_e32 v160, v172, v172
	v_mul_f32_e32 v167, 0xbfb8aa3b, v167
	v_max_f32_e32 v160, 0xc2a00000, v160
	v_exp_f32_e32 v167, v167
	v_mul_f32_e32 v160, 0xbfb8aa3b, v160
	v_pk_mul_f32 v[50:51], v[50:51], v[168:169]
	v_exp_f32_e32 v168, v160
	v_add_f32_e32 v160, 1.0, v162
	v_max_f32_e32 v162, v173, v173
	v_max_f32_e32 v162, 0xc2a00000, v162
	v_mul_f32_e32 v162, 0xbfb8aa3b, v162
	v_add_f32_e32 v161, 1.0, v167
	v_max_f32_e32 v167, v170, v170
	v_exp_f32_e32 v169, v162
	v_cvt_pk_f32_fp8_sdwa v[162:163], v163 src0_sel:WORD_1
	v_max_f32_e32 v167, 0xc2a00000, v167
	v_max_f32_e32 v170, v171, v171
	v_mul_f32_e32 v167, 0xbfb8aa3b, v167
	v_max_f32_e32 v170, 0xc2a00000, v170
	v_exp_f32_e32 v167, v167
	v_mul_f32_e32 v170, 0xbfb8aa3b, v170
	v_exp_f32_e32 v171, v170
	v_max_f32_e32 v162, v162, v162
	v_max_f32_e32 v163, v163, v163
	v_max_f32_e32 v162, 0xc2a00000, v162
	v_max_f32_e32 v163, 0xc2a00000, v163
	v_mul_f32_e32 v162, 0xbfb8aa3b, v162
	v_add_f32_e32 v167, 1.0, v167
	v_mul_f32_e32 v163, 0xbfb8aa3b, v163
	v_exp_f32_e32 v162, v162
	v_exp_f32_e32 v163, v163
	v_rcp_f32_e32 v170, v167
	v_add_f32_e32 v167, 1.0, v171
	v_rcp_f32_e32 v171, v167
	v_rcp_f32_e32 v160, v160
	v_rcp_f32_e32 v161, v161
	v_pk_add_f32 v[162:163], v[162:163], 1.0 op_sel_hi:[1,0]
	v_pk_add_f32 v[168:169], v[168:169], 1.0 op_sel_hi:[1,0]
	v_pk_mul_f32 v[162:163], v[170:171], v[162:163]
	v_cvt_pk_f32_fp8_e32 v[170:171], v156
	v_pk_mul_f32 v[160:161], v[160:161], v[168:169]
	v_cvt_pk_f32_fp8_e32 v[168:169], v158
	v_pk_mul_f32 v[46:47], v[46:47], v[160:161]
;     static __device__ __forceinline__ float f8(unsigned w, int i) { const auto p = (i & 2) ? __builtin_amdgcn_cvt_pk_f32_fp8((int)w, true) : __builtin_amdgcn_cvt_pk_f32_fp8((int)w, false); return (i & 1) ? p[1] : p[0]; }
;     __device__ __forceinline__ void mid(f32x4 (&acc)[2][2][4][2], const Unit& u, int wr, int wc, int fr, int fq) const {
;     ...
;             for (int m = 0; m < 4; ++m) { const unsigned char* zr = Z8 + (size_t)(row0 + ai * HALF + m * 16) * Z8LD + col0;
; #pragma unroll
;                 for (int bj = 0; bj < 2; ++bj) { const uint2 ga2 = *(const uint2*)(zr + zga + bj * HALF), gb2 = *(const uint2*)(zr + zgb + bj * HALF);
; #pragma unroll
;                     for (int n = 0; n < 2; ++n) { f32x4 r; const unsigned wa = n ? ga2.y : ga2.x, wb = n ? gb2.y : gb2.x;
; #pragma unroll
;                         for (int i = 0; i < 4; ++i) { const float xa = f8(wa, i), xb = f8(wb, i);
;                             r[i] = (1.f + __builtin_amdgcn_exp2f(-1.4426950408889634f * fmaxf(xb, -80.f))) * __builtin_amdgcn_rcpf(1.f + __builtin_amdgcn_exp2f(-1.4426950408889634f * fmaxf(xa, -80.f))); }
;                         acc[ai][bj][m][n] *= r; } } }
	v_max_f32_e32 v161, v170, v170
	v_max_f32_e32 v161, 0xc2a00000, v161
	v_mul_f32_e32 v161, 0xbfb8aa3b, v161
	v_exp_f32_e32 v161, v161
	v_max_f32_e32 v160, v168, v168
	v_max_f32_e32 v160, 0xc2a00000, v160
	v_mul_f32_e32 v160, 0xbfb8aa3b, v160
	v_exp_f32_e32 v168, v160
	v_add_f32_e32 v160, 1.0, v161
	v_rcp_f32_e32 v170, v160
	v_max_f32_e32 v160, v169, v169
	v_max_f32_e32 v160, 0xc2a00000, v160
	v_mul_f32_e32 v160, 0xbfb8aa3b, v160
	v_exp_f32_e32 v169, v160
	v_max_f32_e32 v160, v171, v171
	v_max_f32_e32 v160, 0xc2a00000, v160
	v_mul_f32_e32 v160, 0xbfb8aa3b, v160
	v_cvt_pk_f32_fp8_sdwa v[172:173], v156 src0_sel:WORD_1
	v_add_u32_e32 v156, 0xa0, v3
	v_exp_f32_e32 v167, v160
	v_mad_i64_i32 v[160:161], s[28:29], v156, s50, v[154:155]
	v_lshl_add_u64 v[176:177], v[160:161], 0, v[4:5]
	v_add_co_u32_e32 v178, vcc, s51, v176
	v_pk_mul_f32 v[48:49], v[48:49], v[162:163]
	s_nop 0
	v_addc_co_u32_e32 v179, vcc, 0, v177, vcc
	v_mov_b64_e32 v[162:163], v[232:233]
	v_mov_b64_e32 v[160:161], v[228:229]
	v_cvt_pk_f32_fp8_sdwa v[174:175], v158 src0_sel:WORD_1
	v_max_f32_e32 v158, v172, v172
	v_max_f32_e32 v158, 0xc2a00000, v158
	v_mul_f32_e32 v158, 0xbfb8aa3b, v158
	v_add_f32_e32 v156, 1.0, v167
	v_exp_f32_e32 v158, v158
	v_max_f32_e32 v167, v173, v173
	v_rcp_f32_e32 v171, v156
	v_max_f32_e32 v156, v174, v174
	v_max_f32_e32 v167, 0xc2a00000, v167
	v_max_f32_e32 v156, 0xc2a00000, v156
	v_mul_f32_e32 v167, 0xbfb8aa3b, v167
	v_mul_f32_e32 v156, 0xbfb8aa3b, v156
	v_exp_f32_e32 v167, v167
	v_exp_f32_e32 v172, v156
	v_add_f32_e32 v156, 1.0, v158
	v_max_f32_e32 v158, v175, v175
	v_max_f32_e32 v158, 0xc2a00000, v158
	v_mul_f32_e32 v158, 0xbfb8aa3b, v158
	v_exp_f32_e32 v173, v158
	v_rcp_f32_e32 v174, v156
	v_add_f32_e32 v156, 1.0, v167
	v_rcp_f32_e32 v175, v156
	v_pk_add_f32 v[172:173], v[172:173], 1.0 op_sel_hi:[1,0]
	v_pk_add_f32 v[168:169], v[168:169], 1.0 op_sel_hi:[1,0]
	v_add_u32_e32 v3, 0xb0, v3
	v_pk_mul_f32 v[168:169], v[170:171], v[168:169]
	v_pk_mul_f32 v[170:171], v[174:175], v[172:173]
	v_cvt_pk_f32_fp8_e32 v[174:175], v157
	v_cvt_pk_f32_fp8_e32 v[172:173], v159
	v_pk_mul_f32 v[44:45], v[44:45], v[170:171]
	v_cvt_pk_f32_fp8_sdwa v[170:171], v157 src0_sel:WORD_1
	v_max_f32_e32 v158, v174, v174
	v_max_f32_e32 v158, 0xc2a00000, v158
	v_mul_f32_e32 v158, 0xbfb8aa3b, v158
	v_max_f32_e32 v167, v175, v175
	v_exp_f32_e32 v158, v158
	v_max_f32_e32 v167, 0xc2a00000, v167
	v_max_f32_e32 v156, v172, v172
	v_mul_f32_e32 v167, 0xbfb8aa3b, v167
	v_max_f32_e32 v156, 0xc2a00000, v156
	v_exp_f32_e32 v167, v167
	v_mul_f32_e32 v156, 0xbfb8aa3b, v156
	v_pk_mul_f32 v[42:43], v[42:43], v[168:169]
	v_exp_f32_e32 v168, v156
	v_add_f32_e32 v156, 1.0, v158
	v_max_f32_e32 v158, v173, v173
	v_max_f32_e32 v158, 0xc2a00000, v158
	v_mul_f32_e32 v158, 0xbfb8aa3b, v158
	v_add_f32_e32 v157, 1.0, v167
	v_max_f32_e32 v167, v170, v170
	v_exp_f32_e32 v169, v158
	v_cvt_pk_f32_fp8_sdwa v[158:159], v159 src0_sel:WORD_1
	v_max_f32_e32 v167, 0xc2a00000, v167
	v_max_f32_e32 v170, v171, v171
	v_mul_f32_e32 v167, 0xbfb8aa3b, v167
	v_max_f32_e32 v170, 0xc2a00000, v170
	v_exp_f32_e32 v167, v167
	v_mul_f32_e32 v170, 0xbfb8aa3b, v170
	v_exp_f32_e32 v171, v170
	v_max_f32_e32 v158, v158, v158
	v_max_f32_e32 v159, v159, v159
	v_max_f32_e32 v158, 0xc2a00000, v158
	v_max_f32_e32 v159, 0xc2a00000, v159
	v_mul_f32_e32 v158, 0xbfb8aa3b, v158
	v_add_f32_e32 v167, 1.0, v167
	v_mul_f32_e32 v159, 0xbfb8aa3b, v159
	v_exp_f32_e32 v158, v158
	v_exp_f32_e32 v159, v159
	v_rcp_f32_e32 v170, v167
	v_add_f32_e32 v167, 1.0, v171
	v_rcp_f32_e32 v156, v156
	v_rcp_f32_e32 v157, v157
	v_rcp_f32_e32 v171, v167
	v_pk_add_f32 v[158:159], v[158:159], 1.0 op_sel_hi:[1,0]
	v_pk_add_f32 v[168:169], v[168:169], 1.0 op_sel_hi:[1,0]
	v_mad_i64_i32 v[154:155], s[28:29], v3, s50, v[154:155]
	v_pk_mul_f32 v[168:169], v[156:157], v[168:169]
	v_pk_mul_f32 v[170:171], v[170:171], v[158:159]
	v_mov_b64_e32 v[158:159], v[234:235]
	v_mov_b64_e32 v[156:157], v[230:231]
	s_waitcnt vmcnt(0)
	v_cvt_pk_f32_fp8_e32 v[174:175], v160
	v_cvt_pk_f32_fp8_e32 v[172:173], v162
	v_pk_mul_f32 v[38:39], v[38:39], v[168:169]
	v_pk_mul_f32 v[40:41], v[40:41], v[170:171]
	v_max_f32_e32 v168, v174, v174
	v_max_f32_e32 v168, 0xc2a00000, v168
	v_mul_f32_e32 v168, 0xbfb8aa3b, v168
	v_exp_f32_e32 v169, v168
	v_max_f32_e32 v167, v172, v172
	v_max_f32_e32 v167, 0xc2a00000, v167
	v_mul_f32_e32 v167, 0xbfb8aa3b, v167
	v_exp_f32_e32 v168, v167
	v_add_f32_e32 v167, 1.0, v169
	v_max_f32_e32 v169, v175, v175
	v_cvt_pk_f32_fp8_sdwa v[174:175], v160 src0_sel:WORD_1
	v_max_f32_e32 v169, 0xc2a00000, v169
	v_mul_f32_e32 v169, 0xbfb8aa3b, v169
	v_exp_f32_e32 v171, v169
	v_rcp_f32_e32 v170, v167
	v_max_f32_e32 v167, v173, v173
	v_cvt_pk_f32_fp8_sdwa v[172:173], v162 src0_sel:WORD_1
	v_max_f32_e32 v162, v174, v174
	v_max_f32_e32 v167, 0xc2a00000, v167
	v_max_f32_e32 v162, 0xc2a00000, v162
	v_mul_f32_e32 v167, 0xbfb8aa3b, v167
	v_mul_f32_e32 v162, 0xbfb8aa3b, v162
	v_exp_f32_e32 v169, v167
	v_add_f32_e32 v160, 1.0, v171
	v_exp_f32_e32 v162, v162
	v_max_f32_e32 v167, v175, v175
	v_rcp_f32_e32 v171, v160
	v_max_f32_e32 v160, v172, v172
	v_max_f32_e32 v167, 0xc2a00000, v167
	v_max_f32_e32 v160, 0xc2a00000, v160
	v_mul_f32_e32 v167, 0xbfb8aa3b, v167
	v_mul_f32_e32 v160, 0xbfb8aa3b, v160
	v_exp_f32_e32 v167, v167
	v_exp_f32_e32 v172, v160
	v_add_f32_e32 v160, 1.0, v162
	v_max_f32_e32 v162, v173, v173
	v_max_f32_e32 v162, 0xc2a00000, v162
	v_mul_f32_e32 v162, 0xbfb8aa3b, v162
	v_exp_f32_e32 v173, v162
	v_rcp_f32_e32 v174, v160
	v_add_f32_e32 v160, 1.0, v167
	v_rcp_f32_e32 v175, v160
	v_pk_add_f32 v[172:173], v[172:173], 1.0 op_sel_hi:[1,0]
	v_pk_add_f32 v[168:169], v[168:169], 1.0 op_sel_hi:[1,0]
;     static __device__ __forceinline__ float f8(unsigned w, int i) { const auto p = (i & 2) ? __builtin_amdgcn_cvt_pk_f32_fp8((int)w, true) : __builtin_amdgcn_cvt_pk_f32_fp8((int)w, false); return (i & 1) ? p[1] : p[0]; }
;     __device__ __forceinline__ void mid(f32x4 (&acc)[2][2][4][2], const Unit& u, int wr, int wc, int fr, int fq) const {
;     ...
;             for (int m = 0; m < 4; ++m) { const unsigned char* zr = Z8 + (size_t)(row0 + ai * HALF + m * 16) * Z8LD + col0;
; #pragma unroll
;                 for (int bj = 0; bj < 2; ++bj) { const uint2 ga2 = *(const uint2*)(zr + zga + bj * HALF), gb2 = *(const uint2*)(zr + zgb + bj * HALF);
; #pragma unroll
;                     for (int n = 0; n < 2; ++n) { f32x4 r; const unsigned wa = n ? ga2.y : ga2.x, wb = n ? gb2.y : gb2.x;
; #pragma unroll
;                         for (int i = 0; i < 4; ++i) { const float xa = f8(wa, i), xb = f8(wb, i);
;                             r[i] = (1.f + __builtin_amdgcn_exp2f(-1.4426950408889634f * fmaxf(xb, -80.f))) * __builtin_amdgcn_rcpf(1.f + __builtin_amdgcn_exp2f(-1.4426950408889634f * fmaxf(xa, -80.f))); }
;                         acc[ai][bj][m][n] *= r; } } }
	s_nop 0
	v_pk_mul_f32 v[168:169], v[170:171], v[168:169]
	v_pk_mul_f32 v[170:171], v[174:175], v[172:173]
	v_cvt_pk_f32_fp8_e32 v[174:175], v161
	v_cvt_pk_f32_fp8_e32 v[172:173], v163
	v_pk_mul_f32 v[36:37], v[36:37], v[170:171]
	v_cvt_pk_f32_fp8_sdwa v[170:171], v161 src0_sel:WORD_1
	v_max_f32_e32 v162, v174, v174
	v_max_f32_e32 v162, 0xc2a00000, v162
	v_mul_f32_e32 v162, 0xbfb8aa3b, v162
	v_max_f32_e32 v167, v175, v175
	v_exp_f32_e32 v162, v162
	v_max_f32_e32 v167, 0xc2a00000, v167
	v_max_f32_e32 v160, v172, v172
	v_mul_f32_e32 v167, 0xbfb8aa3b, v167
	v_max_f32_e32 v160, 0xc2a00000, v160
	v_exp_f32_e32 v167, v167
	v_mul_f32_e32 v160, 0xbfb8aa3b, v160
	v_pk_mul_f32 v[34:35], v[34:35], v[168:169]
	v_exp_f32_e32 v168, v160
	v_add_f32_e32 v160, 1.0, v162
	v_max_f32_e32 v162, v173, v173
	v_max_f32_e32 v162, 0xc2a00000, v162
	v_mul_f32_e32 v162, 0xbfb8aa3b, v162
	v_add_f32_e32 v161, 1.0, v167
	v_max_f32_e32 v167, v170, v170
	v_exp_f32_e32 v169, v162
	v_cvt_pk_f32_fp8_sdwa v[162:163], v163 src0_sel:WORD_1
	v_max_f32_e32 v167, 0xc2a00000, v167
	v_max_f32_e32 v170, v171, v171
	v_mul_f32_e32 v167, 0xbfb8aa3b, v167
	v_max_f32_e32 v170, 0xc2a00000, v170
	v_exp_f32_e32 v167, v167
	v_mul_f32_e32 v170, 0xbfb8aa3b, v170
	v_exp_f32_e32 v171, v170
	v_max_f32_e32 v162, v162, v162
	v_max_f32_e32 v163, v163, v163
	v_max_f32_e32 v162, 0xc2a00000, v162
	v_max_f32_e32 v163, 0xc2a00000, v163
	v_mul_f32_e32 v162, 0xbfb8aa3b, v162
	v_add_f32_e32 v167, 1.0, v167
	v_mul_f32_e32 v163, 0xbfb8aa3b, v163
	v_exp_f32_e32 v162, v162
	v_exp_f32_e32 v163, v163
	v_rcp_f32_e32 v170, v167
	v_add_f32_e32 v167, 1.0, v171
	v_rcp_f32_e32 v171, v167
	v_lshl_add_u64 v[172:173], v[154:155], 0, v[4:5]
	v_rcp_f32_e32 v160, v160
	v_rcp_f32_e32 v161, v161
	v_pk_add_f32 v[162:163], v[162:163], 1.0 op_sel_hi:[1,0]
	v_add_co_u32_e32 v174, vcc, s51, v172
	v_pk_mul_f32 v[162:163], v[170:171], v[162:163]
	v_cvt_pk_f32_fp8_e32 v[170:171], v156
	v_addc_co_u32_e32 v175, vcc, 0, v173, vcc
	v_mov_b64_e32 v[154:155], v[240:241]
	v_mov_b64_e32 v[4:5], v[236:237]
	v_pk_add_f32 v[168:169], v[168:169], 1.0 op_sel_hi:[1,0]
	v_pk_mul_f32 v[32:33], v[32:33], v[162:163]
	v_pk_mul_f32 v[160:161], v[160:161], v[168:169]
	v_cvt_pk_f32_fp8_e32 v[168:169], v158
	v_pk_mul_f32 v[30:31], v[30:31], v[160:161]
	v_max_f32_e32 v161, v170, v170
	v_max_f32_e32 v161, 0xc2a00000, v161
	v_mul_f32_e32 v161, 0xbfb8aa3b, v161
	v_exp_f32_e32 v161, v161
	v_max_f32_e32 v160, v168, v168
	v_max_f32_e32 v163, v171, v171
	v_max_f32_e32 v163, 0xc2a00000, v163
	v_add_f32_e32 v161, 1.0, v161
	v_rcp_f32_e32 v162, v161
	v_max_f32_e32 v161, v169, v169
	v_cvt_pk_f32_fp8_sdwa v[168:169], v156 src0_sel:WORD_1
	v_mul_f32_e32 v163, 0xbfb8aa3b, v163
	v_exp_f32_e32 v163, v163
	v_cvt_pk_f32_fp8_sdwa v[170:171], v158 src0_sel:WORD_1
	v_max_f32_e32 v156, v168, v168
	v_max_f32_e32 v156, 0xc2a00000, v156
	v_mul_f32_e32 v156, 0xbfb8aa3b, v156
	v_add_f32_e32 v3, 1.0, v163
	v_exp_f32_e32 v156, v156
	v_max_f32_e32 v158, v169, v169
	v_rcp_f32_e32 v163, v3
	v_max_f32_e32 v3, v170, v170
	v_max_f32_e32 v158, 0xc2a00000, v158
	v_max_f32_e32 v3, 0xc2a00000, v3
	v_mul_f32_e32 v158, 0xbfb8aa3b, v158
	v_mul_f32_e32 v3, 0xbfb8aa3b, v3
	v_exp_f32_e32 v158, v158
	v_exp_f32_e32 v168, v3
	v_add_f32_e32 v3, 1.0, v156
	v_max_f32_e32 v156, v171, v171
	v_max_f32_e32 v160, 0xc2a00000, v160
	v_max_f32_e32 v161, 0xc2a00000, v161
	v_max_f32_e32 v156, 0xc2a00000, v156
	v_mul_f32_e32 v160, 0xbfb8aa3b, v160
	v_mul_f32_e32 v161, 0xbfb8aa3b, v161
	v_mul_f32_e32 v156, 0xbfb8aa3b, v156
	v_exp_f32_e32 v160, v160
	v_exp_f32_e32 v161, v161
	v_exp_f32_e32 v169, v156
	v_rcp_f32_e32 v170, v3
	v_add_f32_e32 v3, 1.0, v158
	v_rcp_f32_e32 v171, v3
	v_pk_add_f32 v[168:169], v[168:169], 1.0 op_sel_hi:[1,0]
	v_pk_add_f32 v[160:161], v[160:161], 1.0 op_sel_hi:[1,0]
	s_nop 0
	v_pk_mul_f32 v[160:161], v[162:163], v[160:161]
	v_pk_mul_f32 v[162:163], v[170:171], v[168:169]
	v_cvt_pk_f32_fp8_e32 v[170:171], v157
	v_cvt_pk_f32_fp8_e32 v[168:169], v159
	v_pk_mul_f32 v[26:27], v[26:27], v[160:161]
	v_pk_mul_f32 v[28:29], v[28:29], v[162:163]
	v_max_f32_e32 v156, v170, v170
	v_max_f32_e32 v156, 0xc2a00000, v156
	v_mul_f32_e32 v156, 0xbfb8aa3b, v156
	v_exp_f32_e32 v156, v156
	v_max_f32_e32 v3, v168, v168
	v_max_f32_e32 v158, v171, v171
	v_max_f32_e32 v3, 0xc2a00000, v3
	v_max_f32_e32 v158, 0xc2a00000, v158
	v_mul_f32_e32 v3, 0xbfb8aa3b, v3
	v_mul_f32_e32 v158, 0xbfb8aa3b, v158
	v_exp_f32_e32 v160, v3
	v_add_f32_e32 v3, 1.0, v156
	v_exp_f32_e32 v167, v158
	v_rcp_f32_e32 v156, v3
	v_max_f32_e32 v3, v169, v169
	v_cvt_pk_f32_fp8_sdwa v[158:159], v159 src0_sel:WORD_1
	v_cvt_pk_f32_fp8_sdwa v[162:163], v157 src0_sel:WORD_1
	v_max_f32_e32 v3, 0xc2a00000, v3
	v_mul_f32_e32 v3, 0xbfb8aa3b, v3
	v_exp_f32_e32 v161, v3
	v_add_f32_e32 v3, 1.0, v167
	v_rcp_f32_e32 v157, v3
	v_max_f32_e32 v3, v158, v158
	v_max_f32_e32 v158, v162, v162
	v_max_f32_e32 v158, 0xc2a00000, v158
	v_mul_f32_e32 v158, 0xbfb8aa3b, v158
	v_exp_f32_e32 v162, v158
	v_max_f32_e32 v3, 0xc2a00000, v3
	v_mul_f32_e32 v3, 0xbfb8aa3b, v3
	v_exp_f32_e32 v158, v3
	v_add_f32_e32 v3, 1.0, v162
	v_max_f32_e32 v162, v163, v163
	v_max_f32_e32 v162, 0xc2a00000, v162
	v_mul_f32_e32 v162, 0xbfb8aa3b, v162
	v_exp_f32_e32 v163, v162
	v_max_f32_e32 v159, v159, v159
	v_max_f32_e32 v159, 0xc2a00000, v159
	v_mul_f32_e32 v159, 0xbfb8aa3b, v159
	v_exp_f32_e32 v159, v159
	v_rcp_f32_e32 v162, v3
	v_add_f32_e32 v3, 1.0, v163
	v_rcp_f32_e32 v163, v3
	v_pk_add_f32 v[158:159], v[158:159], 1.0 op_sel_hi:[1,0]
	v_pk_add_f32 v[160:161], v[160:161], 1.0 op_sel_hi:[1,0]
	s_waitcnt vmcnt(0)
;     static __device__ __forceinline__ float f8(unsigned w, int i) { const auto p = (i & 2) ? __builtin_amdgcn_cvt_pk_f32_fp8((int)w, true) : __builtin_amdgcn_cvt_pk_f32_fp8((int)w, false); return (i & 1) ? p[1] : p[0]; }
;     __device__ __forceinline__ void mid(f32x4 (&acc)[2][2][4][2], const Unit& u, int wr, int wc, int fr, int fq) const {
;     ...
;             for (int m = 0; m < 4; ++m) { const unsigned char* zr = Z8 + (size_t)(row0 + ai * HALF + m * 16) * Z8LD + col0;
; #pragma unroll
;                 for (int bj = 0; bj < 2; ++bj) { const uint2 ga2 = *(const uint2*)(zr + zga + bj * HALF), gb2 = *(const uint2*)(zr + zgb + bj * HALF);
; #pragma unroll
;                     for (int n = 0; n < 2; ++n) { f32x4 r; const unsigned wa = n ? ga2.y : ga2.x, wb = n ? gb2.y : gb2.x;
; #pragma unroll
;                         for (int i = 0; i < 4; ++i) { const float xa = f8(wa, i), xb = f8(wb, i);
;                             r[i] = (1.f + __builtin_amdgcn_exp2f(-1.4426950408889634f * fmaxf(xb, -80.f))) * __builtin_amdgcn_rcpf(1.f + __builtin_amdgcn_exp2f(-1.4426950408889634f * fmaxf(xa, -80.f))); }
;                         acc[ai][bj][m][n] *= r; } } }
	v_cvt_pk_f32_fp8_e32 v[170:171], v4
	v_pk_mul_f32 v[156:157], v[156:157], v[160:161]
	v_pk_mul_f32 v[158:159], v[162:163], v[158:159]
	v_mov_b64_e32 v[160:161], v[242:243]
	v_mov_b64_e32 v[162:163], v[238:239]
	v_cvt_pk_f32_fp8_e32 v[168:169], v154
	v_pk_mul_f32 v[22:23], v[22:23], v[156:157]
	v_max_f32_e32 v156, v170, v170
	v_max_f32_e32 v156, 0xc2a00000, v156
	v_mul_f32_e32 v156, 0xbfb8aa3b, v156
	v_exp_f32_e32 v157, v156
	v_max_f32_e32 v3, v168, v168
	v_max_f32_e32 v3, 0xc2a00000, v3
	v_mul_f32_e32 v3, 0xbfb8aa3b, v3
	v_exp_f32_e32 v156, v3
	v_add_f32_e32 v3, 1.0, v157
	v_max_f32_e32 v157, v171, v171
	v_cvt_pk_f32_fp8_sdwa v[170:171], v4 src0_sel:WORD_1
	v_max_f32_e32 v157, 0xc2a00000, v157
	v_mul_f32_e32 v157, 0xbfb8aa3b, v157
	v_pk_mul_f32 v[24:25], v[24:25], v[158:159]
	v_exp_f32_e32 v159, v157
	v_rcp_f32_e32 v158, v3
	v_max_f32_e32 v3, v169, v169
	v_cvt_pk_f32_fp8_sdwa v[168:169], v154 src0_sel:WORD_1
	v_max_f32_e32 v4, v170, v170
	v_max_f32_e32 v3, 0xc2a00000, v3
	v_max_f32_e32 v4, 0xc2a00000, v4
	v_mul_f32_e32 v3, 0xbfb8aa3b, v3
	v_mul_f32_e32 v4, 0xbfb8aa3b, v4
	v_exp_f32_e32 v157, v3
	v_add_f32_e32 v3, 1.0, v159
	v_exp_f32_e32 v4, v4
	v_max_f32_e32 v154, v171, v171
	v_rcp_f32_e32 v159, v3
	v_max_f32_e32 v3, v168, v168
	v_max_f32_e32 v154, 0xc2a00000, v154
	v_max_f32_e32 v3, 0xc2a00000, v3
	v_mul_f32_e32 v154, 0xbfb8aa3b, v154
	v_mul_f32_e32 v3, 0xbfb8aa3b, v3
	v_exp_f32_e32 v154, v154
	v_exp_f32_e32 v168, v3
	v_add_f32_e32 v3, 1.0, v4
	v_max_f32_e32 v4, v169, v169
	v_max_f32_e32 v4, 0xc2a00000, v4
	v_mul_f32_e32 v4, 0xbfb8aa3b, v4
	v_exp_f32_e32 v169, v4
	v_rcp_f32_e32 v170, v3
	v_add_f32_e32 v3, 1.0, v154
	v_rcp_f32_e32 v171, v3
	v_pk_add_f32 v[168:169], v[168:169], 1.0 op_sel_hi:[1,0]
	v_pk_add_f32 v[156:157], v[156:157], 1.0 op_sel_hi:[1,0]
	s_waitcnt vmcnt(0)
	s_nop 0
	v_pk_mul_f32 v[156:157], v[158:159], v[156:157]
	v_pk_mul_f32 v[158:159], v[170:171], v[168:169]
	v_cvt_pk_f32_fp8_e32 v[170:171], v5
	v_cvt_pk_f32_fp8_e32 v[168:169], v155
	v_pk_mul_f32 v[18:19], v[18:19], v[156:157]
	v_pk_mul_f32 v[20:21], v[20:21], v[158:159]
	v_max_f32_e32 v4, v170, v170
	v_max_f32_e32 v4, 0xc2a00000, v4
	v_mul_f32_e32 v4, 0xbfb8aa3b, v4
	v_exp_f32_e32 v4, v4
	v_max_f32_e32 v3, v168, v168
	v_max_f32_e32 v154, v171, v171
	v_max_f32_e32 v3, 0xc2a00000, v3
	v_max_f32_e32 v154, 0xc2a00000, v154
	v_mul_f32_e32 v3, 0xbfb8aa3b, v3
	v_mul_f32_e32 v154, 0xbfb8aa3b, v154
	v_exp_f32_e32 v156, v3
	v_add_f32_e32 v3, 1.0, v4
	v_exp_f32_e32 v167, v154
	v_rcp_f32_e32 v4, v3
	v_max_f32_e32 v3, v169, v169
	v_cvt_pk_f32_fp8_sdwa v[154:155], v155 src0_sel:WORD_1
	v_cvt_pk_f32_fp8_sdwa v[158:159], v5 src0_sel:WORD_1
	v_max_f32_e32 v3, 0xc2a00000, v3
	v_mul_f32_e32 v3, 0xbfb8aa3b, v3
	v_exp_f32_e32 v157, v3
	v_add_f32_e32 v3, 1.0, v167
	v_rcp_f32_e32 v5, v3
	v_max_f32_e32 v3, v154, v154
	v_max_f32_e32 v154, v158, v158
	v_max_f32_e32 v154, 0xc2a00000, v154
	v_mul_f32_e32 v154, 0xbfb8aa3b, v154
	v_exp_f32_e32 v158, v154
	v_max_f32_e32 v3, 0xc2a00000, v3
	v_mul_f32_e32 v3, 0xbfb8aa3b, v3
	v_exp_f32_e32 v154, v3
	v_add_f32_e32 v3, 1.0, v158
	v_max_f32_e32 v158, v159, v159
	v_max_f32_e32 v158, 0xc2a00000, v158
	v_mul_f32_e32 v158, 0xbfb8aa3b, v158
	v_exp_f32_e32 v159, v158
	v_max_f32_e32 v155, v155, v155
	v_max_f32_e32 v155, 0xc2a00000, v155
	v_mul_f32_e32 v155, 0xbfb8aa3b, v155
	v_exp_f32_e32 v155, v155
	v_rcp_f32_e32 v158, v3
	v_add_f32_e32 v3, 1.0, v159
	v_rcp_f32_e32 v159, v3
	v_pk_add_f32 v[154:155], v[154:155], 1.0 op_sel_hi:[1,0]
	v_pk_add_f32 v[156:157], v[156:157], 1.0 op_sel_hi:[1,0]
	v_pk_mul_f32 v[154:155], v[158:159], v[154:155]
	s_waitcnt vmcnt(0)
;     static __device__ __forceinline__ float f8(unsigned w, int i) { const auto p = (i & 2) ? __builtin_amdgcn_cvt_pk_f32_fp8((int)w, true) : __builtin_amdgcn_cvt_pk_f32_fp8((int)w, false); return (i & 1) ? p[1] : p[0]; }
;     __device__ __forceinline__ void mid(f32x4 (&acc)[2][2][4][2], const Unit& u, int wr, int wc, int fr, int fq) const {
;     ...
;             for (int m = 0; m < 4; ++m) { const unsigned char* zr = Z8 + (size_t)(row0 + ai * HALF + m * 16) * Z8LD + col0;
; #pragma unroll
;                 for (int bj = 0; bj < 2; ++bj) { const uint2 ga2 = *(const uint2*)(zr + zga + bj * HALF), gb2 = *(const uint2*)(zr + zgb + bj * HALF);
; #pragma unroll
;                     for (int n = 0; n < 2; ++n) { f32x4 r; const unsigned wa = n ? ga2.y : ga2.x, wb = n ? gb2.y : gb2.x;
; #pragma unroll
;                         for (int i = 0; i < 4; ++i) { const float xa = f8(wa, i), xb = f8(wb, i);
;                             r[i] = (1.f + __builtin_amdgcn_exp2f(-1.4426950408889634f * fmaxf(xb, -80.f))) * __builtin_amdgcn_rcpf(1.f + __builtin_amdgcn_exp2f(-1.4426950408889634f * fmaxf(xa, -80.f))); }
;                         acc[ai][bj][m][n] *= r; } } }
	v_cvt_pk_f32_fp8_e32 v[158:159], v162
	v_pk_mul_f32 v[4:5], v[4:5], v[156:157]
	v_cvt_pk_f32_fp8_e32 v[156:157], v160
	v_pk_mul_f32 v[14:15], v[14:15], v[4:5]
	v_max_f32_e32 v4, v158, v158
	v_max_f32_e32 v4, 0xc2a00000, v4
	v_mul_f32_e32 v4, 0xbfb8aa3b, v4
	v_exp_f32_e32 v5, v4
	v_max_f32_e32 v3, v156, v156
	v_max_f32_e32 v3, 0xc2a00000, v3
	v_mul_f32_e32 v3, 0xbfb8aa3b, v3
	v_exp_f32_e32 v4, v3
	v_add_f32_e32 v3, 1.0, v5
	v_max_f32_e32 v5, v159, v159
	v_max_f32_e32 v5, 0xc2a00000, v5
	v_mul_f32_e32 v5, 0xbfb8aa3b, v5
	v_pk_mul_f32 v[16:17], v[16:17], v[154:155]
	v_exp_f32_e32 v155, v5
	v_rcp_f32_e32 v154, v3
	v_max_f32_e32 v3, v157, v157
	v_cvt_pk_f32_fp8_sdwa v[156:157], v160 src0_sel:WORD_1
	v_cvt_pk_f32_fp8_sdwa v[158:159], v162 src0_sel:WORD_1
	v_max_f32_e32 v3, 0xc2a00000, v3
	v_mul_f32_e32 v3, 0xbfb8aa3b, v3
	v_exp_f32_e32 v5, v3
	v_add_f32_e32 v3, 1.0, v155
	v_rcp_f32_e32 v155, v3
	v_max_f32_e32 v3, v156, v156
	v_max_f32_e32 v156, v158, v158
	v_max_f32_e32 v156, 0xc2a00000, v156
	v_mul_f32_e32 v156, 0xbfb8aa3b, v156
	v_exp_f32_e32 v158, v156
	v_max_f32_e32 v3, 0xc2a00000, v3
	v_mul_f32_e32 v3, 0xbfb8aa3b, v3
	v_exp_f32_e32 v156, v3
	v_add_f32_e32 v3, 1.0, v158
	v_max_f32_e32 v158, v159, v159
	v_max_f32_e32 v158, 0xc2a00000, v158
	v_mul_f32_e32 v158, 0xbfb8aa3b, v158
	v_exp_f32_e32 v159, v158
	v_max_f32_e32 v157, v157, v157
	v_pk_add_f32 v[4:5], v[4:5], 1.0 op_sel_hi:[1,0]
	v_max_f32_e32 v157, 0xc2a00000, v157
	v_pk_mul_f32 v[4:5], v[154:155], v[4:5]
	v_cvt_pk_f32_fp8_e32 v[154:155], v163
	v_mul_f32_e32 v157, 0xbfb8aa3b, v157
	v_exp_f32_e32 v157, v157
	v_rcp_f32_e32 v158, v3
	v_add_f32_e32 v3, 1.0, v159
	v_rcp_f32_e32 v159, v3
	v_max_f32_e32 v3, v154, v154
	v_max_f32_e32 v3, 0xc2a00000, v3
	v_pk_add_f32 v[156:157], v[156:157], 1.0 op_sel_hi:[1,0]
	v_mul_f32_e32 v3, 0xbfb8aa3b, v3
	v_pk_mul_f32 v[156:157], v[158:159], v[156:157]
	v_exp_f32_e32 v3, v3
	v_pk_mul_f32 v[12:13], v[12:13], v[156:157]
	v_cvt_pk_f32_fp8_e32 v[156:157], v161
	v_max_f32_e32 v155, v155, v155
	v_max_f32_e32 v155, 0xc2a00000, v155
	v_mul_f32_e32 v155, 0xbfb8aa3b, v155
	v_add_f32_e32 v3, 1.0, v3
	v_exp_f32_e32 v155, v155
	v_cvt_pk_f32_fp8_sdwa v[158:159], v163 src0_sel:WORD_1
	v_rcp_f32_e32 v154, v3
	v_max_f32_e32 v3, v156, v156
	v_max_f32_e32 v3, 0xc2a00000, v3
	v_mul_f32_e32 v3, 0xbfb8aa3b, v3
	v_exp_f32_e32 v156, v3
	v_add_f32_e32 v3, 1.0, v155
	v_rcp_f32_e32 v155, v3
	v_max_f32_e32 v3, v157, v157
	v_max_f32_e32 v157, v158, v158
	v_max_f32_e32 v157, 0xc2a00000, v157
	v_mul_f32_e32 v157, 0xbfb8aa3b, v157
	v_exp_f32_e32 v158, v157
	v_pk_mul_f32 v[10:11], v[10:11], v[4:5]
	v_cvt_pk_f32_fp8_sdwa v[4:5], v161 src0_sel:WORD_1
	v_max_f32_e32 v3, 0xc2a00000, v3
	v_mul_f32_e32 v3, 0xbfb8aa3b, v3
	v_exp_f32_e32 v157, v3
	v_add_f32_e32 v3, 1.0, v158
	v_rcp_f32_e32 v158, v3
	v_max_f32_e32 v3, v4, v4
	v_max_f32_e32 v3, 0xc2a00000, v3
	v_mul_f32_e32 v3, 0xbfb8aa3b, v3
	v_exp_f32_e32 v4, v3
	v_max_f32_e32 v3, v5, v5
	v_max_f32_e32 v5, v159, v159
	v_max_f32_e32 v5, 0xc2a00000, v5
	v_mul_f32_e32 v5, 0xbfb8aa3b, v5
	v_exp_f32_e32 v159, v5
	v_max_f32_e32 v3, 0xc2a00000, v3
	v_mul_f32_e32 v3, 0xbfb8aa3b, v3
	v_exp_f32_e32 v5, v3
	v_add_f32_e32 v3, 1.0, v159
	v_rcp_f32_e32 v159, v3
	v_pk_add_f32 v[156:157], v[156:157], 1.0 op_sel_hi:[1,0]
	v_pk_add_f32 v[4:5], v[4:5], 1.0 op_sel_hi:[1,0]
	v_pk_mul_f32 v[154:155], v[154:155], v[156:157]
	v_pk_mul_f32 v[4:5], v[4:5], v[158:159]
	v_pk_mul_f32 v[6:7], v[6:7], v[154:155]
	v_pk_mul_f32 v[8:9], v[8:9], v[4:5]
	s_branch .LBB0_1047

; __device__ __forceinline__ unsigned cvt_pk_bf16(float lo, float hi) { unsigned r; asm volatile("v_cvt_pk_bf16_f32 %0, %1, %2" : "=v"(r) : "v"(lo), "v"(hi)); return r; }
; __device__ __forceinline__ float sigmoidf_(float x) { return __builtin_amdgcn_rcpf(1.f + __builtin_amdgcn_exp2f(-1.4426950408889634f * x)); }
;     static __device__ __forceinline__ float f8(unsigned w, int i) { const auto p = (i & 2) ? __builtin_amdgcn_cvt_pk_f32_fp8((int)w, true) : __builtin_amdgcn_cvt_pk_f32_fp8((int)w, false); return (i & 1) ? p[1] : p[0]; }
;     __device__ __forceinline__ void operator()(const f32x4 (&acc)[2][2][4][2], const Unit& u, int wr, int wc, int fr, int fq) const {
;         asm volatile("" : "+v"(fr), "+v"(fq));
;         const int row0 = u.pm * BM + wr * 64 + fr, col0 = u.pn * BM + wc * 32 + 8 * fq;
; #pragma unroll
;         for (int ai = 0; ai < 2; ++ai)
; #pragma unroll
;             for (int m = 0; m < 4; ++m) { const size_t row = (size_t)(row0 + ai * HALF + m * 16);
; #pragma unroll
;                 for (int bj = 0; bj < 2; ++bj) { const uint2 gb2 = *(const uint2*)(Z8 + row * Z8LD + zgb + col0 + bj * HALF); float y[8];
; #pragma unroll
;                     for (int n = 0; n < 2; ++n)
; #pragma unroll
;                         for (int i = 0; i < 4; ++i) { const float xb = f8(n ? gb2.y : gb2.x, i);
;                             y[4 * n + i] = acc[ai][bj][m][n][i] * sigmoidf_(fmaxf(xb, -80.f)); }
;                     u32x4 w; w.x = cvt_pk_bf16(y[0], y[1]); w.y = cvt_pk_bf16(y[2], y[3]); w.z = cvt_pk_bf16(y[4], y[5]); w.w = cvt_pk_bf16(y[6], y[7]);
;                     *(u32x4*)(Y + row * 2048 + col0 + bj * HALF) = w; } }
.LBB0_1052:
	v_mov_b32_e32 v3, v1
	v_mov_b32_e32 v4, v164
	v_mov_b64_e32 v[154:155], s[8:9]
	v_add_u32_e32 v152, s55, v3
	v_lshl_add_u32 v150, v4, 3, s17
	v_ashrrev_i32_e32 v151, 31, v150
	v_mad_i64_i32 v[4:5], s[24:25], v152, s50, v[154:155]
	v_lshl_add_u64 v[156:157], v[4:5], 0, v[150:151]
	v_add_co_u32_e32 v4, vcc, 0x1000, v156
	v_ashrrev_i32_e32 v153, 31, v152
	s_nop 0
	v_addc_co_u32_e32 v5, vcc, 0, v157, vcc
	global_load_dwordx2 v[158:159], v[4:5], off
	global_load_dwordx2 v[174:175], v[4:5], off offset:128
	v_add_co_u32_e32 v236, vcc, 0x18000, v4
	s_nop 1
	v_addc_co_u32_e32 v237, vcc, 0, v5, vcc
	global_load_dwordx2 v[176:177], v[236:237], off
	global_load_dwordx2 v[178:179], v[236:237], off offset:128
	v_add_co_u32_e32 v236, vcc, 0x18000, v236
	s_nop 1
	v_addc_co_u32_e32 v237, vcc, 0, v237, vcc
	global_load_dwordx2 v[180:181], v[236:237], off
	global_load_dwordx2 v[182:183], v[236:237], off offset:128
	v_add_co_u32_e32 v236, vcc, 0x18000, v236
	s_nop 1
	v_addc_co_u32_e32 v237, vcc, 0, v237, vcc
	global_load_dwordx2 v[184:185], v[236:237], off
	global_load_dwordx2 v[186:187], v[236:237], off offset:128
	v_add_co_u32_e32 v236, vcc, 0xc0000, v4
	s_nop 1
	v_addc_co_u32_e32 v237, vcc, 0, v5, vcc
	global_load_dwordx2 v[188:189], v[236:237], off
	global_load_dwordx2 v[190:191], v[236:237], off offset:128
	v_add_co_u32_e32 v236, vcc, 0x18000, v236
	s_nop 1
	v_addc_co_u32_e32 v237, vcc, 0, v237, vcc
	global_load_dwordx2 v[192:193], v[236:237], off
	global_load_dwordx2 v[194:195], v[236:237], off offset:128
	v_add_co_u32_e32 v236, vcc, 0x18000, v236
	s_nop 1
	v_addc_co_u32_e32 v237, vcc, 0, v237, vcc
	global_load_dwordx2 v[196:197], v[236:237], off
	global_load_dwordx2 v[198:199], v[236:237], off offset:128
	v_add_co_u32_e32 v236, vcc, 0x18000, v236
	s_nop 1
	v_addc_co_u32_e32 v237, vcc, 0, v237, vcc
	global_load_dwordx2 v[200:201], v[236:237], off
	global_load_dwordx2 v[202:203], v[236:237], off offset:128
	v_lshlrev_b64 v[160:161], 12, v[152:153]
	v_lshlrev_b64 v[4:5], 1, v[150:151]
	v_lshl_add_u64 v[160:161], s[6:7], 0, v[160:161]
	v_lshl_add_u64 v[160:161], v[160:161], 0, v[4:5]
	v_lshl_add_u64 v[156:157], v[156:157], 0, s[14:15]
	s_waitcnt vmcnt(0)
	v_cvt_pk_f32_fp8_e32 v[162:163], v158
	v_cvt_pk_f32_fp8_sdwa v[168:169], v158 src0_sel:WORD_1
	v_cvt_pk_f32_fp8_e32 v[170:171], v159
	v_cvt_pk_f32_fp8_sdwa v[158:159], v159 src0_sel:WORD_1
	v_max_f32_e32 v3, v162, v162
	v_max_f32_e32 v153, v163, v163
	v_max_f32_e32 v162, v168, v168
	v_max_f32_e32 v159, v159, v159
	v_max_f32_e32 v163, v169, v169
	v_max_f32_e32 v167, v170, v170
	v_max_f32_e32 v168, v171, v171
	v_max_f32_e32 v158, v158, v158
	v_max_f32_e32 v159, 0xc2a00000, v159
	v_max_f32_e32 v3, 0xc2a00000, v3
	v_max_f32_e32 v153, 0xc2a00000, v153
	v_max_f32_e32 v162, 0xc2a00000, v162
	v_max_f32_e32 v163, 0xc2a00000, v163
	v_max_f32_e32 v167, 0xc2a00000, v167
	v_max_f32_e32 v168, 0xc2a00000, v168
	v_max_f32_e32 v158, 0xc2a00000, v158
	v_mul_f32_e32 v159, 0xbfb8aa3b, v159
	v_mul_f32_e32 v3, 0xbfb8aa3b, v3
	v_mul_f32_e32 v153, 0xbfb8aa3b, v153
	v_mul_f32_e32 v162, 0xbfb8aa3b, v162
	v_mul_f32_e32 v163, 0xbfb8aa3b, v163
	v_mul_f32_e32 v167, 0xbfb8aa3b, v167
	v_mul_f32_e32 v168, 0xbfb8aa3b, v168
	v_mul_f32_e32 v158, 0xbfb8aa3b, v158
	v_exp_f32_e32 v159, v159
	v_exp_f32_e32 v3, v3
	v_exp_f32_e32 v153, v153
	v_exp_f32_e32 v162, v162
	v_exp_f32_e32 v163, v163
	v_exp_f32_e32 v167, v167
	v_exp_f32_e32 v168, v168
	v_exp_f32_e32 v158, v158
	v_add_f32_e32 v159, 1.0, v159
	v_add_f32_e32 v3, 1.0, v3
	v_add_f32_e32 v153, 1.0, v153
	v_add_f32_e32 v162, 1.0, v162
	v_add_f32_e32 v163, 1.0, v163
	v_add_f32_e32 v167, 1.0, v167
	v_add_f32_e32 v168, 1.0, v168
	v_add_f32_e32 v158, 1.0, v158
	v_rcp_f32_e32 v159, v159
	v_rcp_f32_e32 v3, v3
	v_rcp_f32_e32 v153, v153
	v_rcp_f32_e32 v162, v162
	v_rcp_f32_e32 v163, v163
	v_rcp_f32_e32 v167, v167
	v_rcp_f32_e32 v168, v168
	v_rcp_f32_e32 v158, v158
	v_mul_f32_e32 v129, v129, v159
	v_mul_f32_e32 v3, v130, v3
	v_mul_f32_e32 v130, v131, v153
	v_mul_f32_e32 v131, v132, v162
	v_mul_f32_e32 v132, v133, v163
	v_mul_f32_e32 v133, v126, v167
	v_mul_f32_e32 v153, v127, v168
	v_mul_f32_e32 v158, v128, v158
	v_cvt_pk_bf16_f32 v126, v3, v130
	v_cvt_pk_bf16_f32 v127, v131, v132
	v_cvt_pk_bf16_f32 v128, v133, v153
	v_cvt_pk_bf16_f32 v129, v158, v129
	global_store_dwordx4 v[160:161], v[126:129], off
	s_nop 1
	v_mov_b64_e32 v[126:127], v[174:175]
	v_cvt_pk_f32_fp8_e32 v[156:157], v126
	v_cvt_pk_f32_fp8_sdwa v[158:159], v126 src0_sel:WORD_1
	v_cvt_pk_f32_fp8_e32 v[162:163], v127
	v_cvt_pk_f32_fp8_sdwa v[126:127], v127 src0_sel:WORD_1
	v_max_f32_e32 v3, v156, v156
	v_max_f32_e32 v129, v157, v157
	v_max_f32_e32 v153, v158, v158
	v_max_f32_e32 v127, v127, v127
	v_max_f32_e32 v156, v159, v159
	v_max_f32_e32 v157, v162, v162
	v_max_f32_e32 v158, v163, v163
	v_max_f32_e32 v126, v126, v126
	v_max_f32_e32 v127, 0xc2a00000, v127
	v_max_f32_e32 v3, 0xc2a00000, v3
	v_max_f32_e32 v129, 0xc2a00000, v129
	v_max_f32_e32 v153, 0xc2a00000, v153
	v_max_f32_e32 v156, 0xc2a00000, v156
	v_max_f32_e32 v157, 0xc2a00000, v157
	v_max_f32_e32 v158, 0xc2a00000, v158
	v_max_f32_e32 v126, 0xc2a00000, v126
	v_mul_f32_e32 v127, 0xbfb8aa3b, v127
	v_mul_f32_e32 v3, 0xbfb8aa3b, v3
	v_mul_f32_e32 v129, 0xbfb8aa3b, v129
	v_mul_f32_e32 v153, 0xbfb8aa3b, v153
	v_mul_f32_e32 v156, 0xbfb8aa3b, v156
	v_mul_f32_e32 v157, 0xbfb8aa3b, v157
	v_mul_f32_e32 v158, 0xbfb8aa3b, v158
	v_mul_f32_e32 v126, 0xbfb8aa3b, v126
	v_exp_f32_e32 v127, v127
	v_exp_f32_e32 v3, v3
	v_exp_f32_e32 v129, v129
	v_exp_f32_e32 v153, v153
	v_exp_f32_e32 v156, v156
	v_exp_f32_e32 v157, v157
	v_exp_f32_e32 v158, v158
	v_exp_f32_e32 v126, v126
	v_add_f32_e32 v127, 1.0, v127
; __device__ __forceinline__ unsigned cvt_pk_bf16(float lo, float hi) { unsigned r; asm volatile("v_cvt_pk_bf16_f32 %0, %1, %2" : "=v"(r) : "v"(lo), "v"(hi)); return r; }
; __device__ __forceinline__ float sigmoidf_(float x) { return __builtin_amdgcn_rcpf(1.f + __builtin_amdgcn_exp2f(-1.4426950408889634f * x)); }
;     static __device__ __forceinline__ float f8(unsigned w, int i) { const auto p = (i & 2) ? __builtin_amdgcn_cvt_pk_f32_fp8((int)w, true) : __builtin_amdgcn_cvt_pk_f32_fp8((int)w, false); return (i & 1) ? p[1] : p[0]; }
;     __device__ __forceinline__ void operator()(const f32x4 (&acc)[2][2][4][2], const Unit& u, int wr, int wc, int fr, int fq) const {
;     ...
;             for (int m = 0; m < 4; ++m) { const size_t row = (size_t)(row0 + ai * HALF + m * 16);
; #pragma unroll
;                 for (int bj = 0; bj < 2; ++bj) { const uint2 gb2 = *(const uint2*)(Z8 + row * Z8LD + zgb + col0 + bj * HALF); float y[8];
; #pragma unroll
;                     for (int n = 0; n < 2; ++n)
; #pragma unroll
;                         for (int i = 0; i < 4; ++i) { const float xb = f8(n ? gb2.y : gb2.x, i);
;                             y[4 * n + i] = acc[ai][bj][m][n][i] * sigmoidf_(fmaxf(xb, -80.f)); }
;                     u32x4 w; w.x = cvt_pk_bf16(y[0], y[1]); w.y = cvt_pk_bf16(y[2], y[3]); w.z = cvt_pk_bf16(y[4], y[5]); w.w = cvt_pk_bf16(y[6], y[7]);
;                     *(u32x4*)(Y + row * 2048 + col0 + bj * HALF) = w; } }
	v_add_f32_e32 v3, 1.0, v3
	v_add_f32_e32 v129, 1.0, v129
	v_add_f32_e32 v153, 1.0, v153
	v_add_f32_e32 v156, 1.0, v156
	v_add_f32_e32 v157, 1.0, v157
	v_add_f32_e32 v158, 1.0, v158
	v_add_f32_e32 v126, 1.0, v126
	v_rcp_f32_e32 v127, v127
	v_add_u32_e32 v128, 16, v152
	v_rcp_f32_e32 v3, v3
	v_rcp_f32_e32 v129, v129
	v_rcp_f32_e32 v153, v153
	v_rcp_f32_e32 v156, v156
	v_rcp_f32_e32 v157, v157
	v_rcp_f32_e32 v158, v158
	v_rcp_f32_e32 v126, v126
	v_mad_i64_i32 v[130:131], s[24:25], v128, s50, v[154:155]
	v_lshl_add_u64 v[130:131], v[130:131], 0, v[150:151]
	v_add_co_u32_e32 v132, vcc, s51, v130
	v_mul_f32_e32 v121, v121, v127
	s_nop 0
	v_addc_co_u32_e32 v133, vcc, 0, v131, vcc
	v_mul_f32_e32 v3, v122, v3
	v_mul_f32_e32 v122, v123, v129
	v_mul_f32_e32 v123, v124, v153
	v_mul_f32_e32 v124, v125, v156
	v_mul_f32_e32 v125, v118, v157
	v_mul_f32_e32 v129, v119, v158
	v_mul_f32_e32 v126, v120, v126
	v_cvt_pk_bf16_f32 v118, v3, v122
	v_cvt_pk_bf16_f32 v119, v123, v124
	v_cvt_pk_bf16_f32 v120, v125, v129
	v_cvt_pk_bf16_f32 v121, v126, v121
	global_store_dwordx4 v[160:161], v[118:121], off offset:256
	s_nop 1
	v_mov_b64_e32 v[118:119], v[176:177]
	v_ashrrev_i32_e32 v129, 31, v128
	v_lshlrev_b64 v[120:121], 12, v[128:129]
	v_lshl_add_u64 v[120:121], s[6:7], 0, v[120:121]
	v_lshl_add_u64 v[120:121], v[120:121], 0, v[4:5]
	v_lshl_add_u64 v[122:123], v[130:131], 0, s[14:15]
	v_cvt_pk_f32_fp8_e32 v[124:125], v118
	v_cvt_pk_f32_fp8_sdwa v[126:127], v118 src0_sel:WORD_1
	v_cvt_pk_f32_fp8_e32 v[128:129], v119
	v_cvt_pk_f32_fp8_sdwa v[118:119], v119 src0_sel:WORD_1
	v_max_f32_e32 v3, v124, v124
	v_max_f32_e32 v124, v125, v125
	v_max_f32_e32 v125, v126, v126
	v_max_f32_e32 v119, v119, v119
	v_max_f32_e32 v126, v127, v127
	v_max_f32_e32 v127, v128, v128
	v_max_f32_e32 v128, v129, v129
	v_max_f32_e32 v118, v118, v118
	v_max_f32_e32 v119, 0xc2a00000, v119
	v_max_f32_e32 v3, 0xc2a00000, v3
	v_max_f32_e32 v124, 0xc2a00000, v124
	v_max_f32_e32 v125, 0xc2a00000, v125
	v_max_f32_e32 v126, 0xc2a00000, v126
	v_max_f32_e32 v127, 0xc2a00000, v127
	v_max_f32_e32 v128, 0xc2a00000, v128
	v_max_f32_e32 v118, 0xc2a00000, v118
	v_mul_f32_e32 v119, 0xbfb8aa3b, v119
	v_mul_f32_e32 v3, 0xbfb8aa3b, v3
	v_mul_f32_e32 v124, 0xbfb8aa3b, v124
	v_mul_f32_e32 v125, 0xbfb8aa3b, v125
	v_mul_f32_e32 v126, 0xbfb8aa3b, v126
	v_mul_f32_e32 v127, 0xbfb8aa3b, v127
	v_mul_f32_e32 v128, 0xbfb8aa3b, v128
	v_mul_f32_e32 v118, 0xbfb8aa3b, v118
	v_exp_f32_e32 v119, v119
	v_exp_f32_e32 v3, v3
	v_exp_f32_e32 v124, v124
	v_exp_f32_e32 v125, v125
	v_exp_f32_e32 v126, v126
	v_exp_f32_e32 v127, v127
	v_exp_f32_e32 v128, v128
	v_exp_f32_e32 v118, v118
	v_add_f32_e32 v119, 1.0, v119
	v_add_f32_e32 v3, 1.0, v3
	v_add_f32_e32 v124, 1.0, v124
	v_add_f32_e32 v125, 1.0, v125
	v_add_f32_e32 v126, 1.0, v126
	v_add_f32_e32 v127, 1.0, v127
	v_add_f32_e32 v128, 1.0, v128
	v_add_f32_e32 v118, 1.0, v118
	v_rcp_f32_e32 v119, v119
	v_rcp_f32_e32 v3, v3
	v_rcp_f32_e32 v124, v124
	v_rcp_f32_e32 v125, v125
	v_rcp_f32_e32 v126, v126
	v_rcp_f32_e32 v127, v127
	v_rcp_f32_e32 v128, v128
	v_rcp_f32_e32 v118, v118
	v_mul_f32_e32 v113, v113, v119
	v_mul_f32_e32 v3, v114, v3
	v_mul_f32_e32 v114, v115, v124
	v_mul_f32_e32 v115, v116, v125
	v_mul_f32_e32 v116, v117, v126
	v_mul_f32_e32 v117, v110, v127
	v_mul_f32_e32 v124, v111, v128
	v_mul_f32_e32 v118, v112, v118
	v_cvt_pk_bf16_f32 v110, v3, v114
	v_cvt_pk_bf16_f32 v111, v115, v116
	v_cvt_pk_bf16_f32 v112, v117, v124
	v_cvt_pk_bf16_f32 v113, v118, v113
	global_store_dwordx4 v[120:121], v[110:113], off
	s_nop 1
	v_mov_b64_e32 v[110:111], v[178:179]
	v_cvt_pk_f32_fp8_e32 v[118:119], v110
	v_cvt_pk_f32_fp8_sdwa v[122:123], v110 src0_sel:WORD_1
	v_cvt_pk_f32_fp8_e32 v[124:125], v111
	v_cvt_pk_f32_fp8_sdwa v[110:111], v111 src0_sel:WORD_1
	v_max_f32_e32 v3, v118, v118
	v_max_f32_e32 v113, v119, v119
	v_max_f32_e32 v118, v122, v122
	v_max_f32_e32 v111, v111, v111
	v_max_f32_e32 v119, v123, v123
	v_max_f32_e32 v122, v124, v124
	v_max_f32_e32 v123, v125, v125
	v_max_f32_e32 v110, v110, v110
	v_max_f32_e32 v111, 0xc2a00000, v111
	v_max_f32_e32 v3, 0xc2a00000, v3
	v_max_f32_e32 v113, 0xc2a00000, v113
	v_max_f32_e32 v118, 0xc2a00000, v118
	v_max_f32_e32 v119, 0xc2a00000, v119
	v_max_f32_e32 v122, 0xc2a00000, v122
	v_max_f32_e32 v123, 0xc2a00000, v123
	v_max_f32_e32 v110, 0xc2a00000, v110
	v_mul_f32_e32 v111, 0xbfb8aa3b, v111
	v_mul_f32_e32 v3, 0xbfb8aa3b, v3
	v_mul_f32_e32 v113, 0xbfb8aa3b, v113
	v_mul_f32_e32 v118, 0xbfb8aa3b, v118
	v_mul_f32_e32 v119, 0xbfb8aa3b, v119
	v_mul_f32_e32 v122, 0xbfb8aa3b, v122
	v_mul_f32_e32 v123, 0xbfb8aa3b, v123
	v_mul_f32_e32 v110, 0xbfb8aa3b, v110
	v_exp_f32_e32 v111, v111
	v_exp_f32_e32 v3, v3
	v_exp_f32_e32 v113, v113
	v_exp_f32_e32 v118, v118
	v_exp_f32_e32 v119, v119
	v_exp_f32_e32 v122, v122
	v_exp_f32_e32 v123, v123
	v_exp_f32_e32 v110, v110
	v_add_f32_e32 v111, 1.0, v111
	v_add_f32_e32 v3, 1.0, v3
	v_add_f32_e32 v113, 1.0, v113
	v_add_f32_e32 v118, 1.0, v118
	v_add_f32_e32 v119, 1.0, v119
	v_add_f32_e32 v122, 1.0, v122
	v_add_f32_e32 v123, 1.0, v123
	v_add_f32_e32 v110, 1.0, v110
	v_rcp_f32_e32 v111, v111
	v_add_u32_e32 v112, 32, v152
	v_rcp_f32_e32 v3, v3
	v_rcp_f32_e32 v113, v113
	v_rcp_f32_e32 v118, v118
	v_rcp_f32_e32 v119, v119
	v_rcp_f32_e32 v122, v122
	v_rcp_f32_e32 v123, v123
	v_rcp_f32_e32 v110, v110
	v_mad_i64_i32 v[114:115], s[24:25], v112, s50, v[154:155]
	v_lshl_add_u64 v[114:115], v[114:115], 0, v[150:151]
	v_add_co_u32_e32 v116, vcc, s51, v114
	v_mul_f32_e32 v105, v105, v111
	s_nop 0
	v_addc_co_u32_e32 v117, vcc, 0, v115, vcc
	v_mul_f32_e32 v3, v106, v3
	v_mul_f32_e32 v106, v107, v113
	v_mul_f32_e32 v107, v108, v118
	v_mul_f32_e32 v108, v109, v119
; __device__ __forceinline__ unsigned cvt_pk_bf16(float lo, float hi) { unsigned r; asm volatile("v_cvt_pk_bf16_f32 %0, %1, %2" : "=v"(r) : "v"(lo), "v"(hi)); return r; }
;     static __device__ __forceinline__ float f8(unsigned w, int i) { const auto p = (i & 2) ? __builtin_amdgcn_cvt_pk_f32_fp8((int)w, true) : __builtin_amdgcn_cvt_pk_f32_fp8((int)w, false); return (i & 1) ? p[1] : p[0]; }
; __device__ __forceinline__ float sigmoidf_(float x) { return __builtin_amdgcn_rcpf(1.f + __builtin_amdgcn_exp2f(-1.4426950408889634f * x)); }
;     __device__ __forceinline__ void operator()(const f32x4 (&acc)[2][2][4][2], const Unit& u, int wr, int wc, int fr, int fq) const {
;     ...
;             for (int m = 0; m < 4; ++m) { const size_t row = (size_t)(row0 + ai * HALF + m * 16);
; #pragma unroll
;                 for (int bj = 0; bj < 2; ++bj) { const uint2 gb2 = *(const uint2*)(Z8 + row * Z8LD + zgb + col0 + bj * HALF); float y[8];
; #pragma unroll
;                     for (int n = 0; n < 2; ++n)
; #pragma unroll
;                         for (int i = 0; i < 4; ++i) { const float xb = f8(n ? gb2.y : gb2.x, i);
;                             y[4 * n + i] = acc[ai][bj][m][n][i] * sigmoidf_(fmaxf(xb, -80.f)); }
;                     u32x4 w; w.x = cvt_pk_bf16(y[0], y[1]); w.y = cvt_pk_bf16(y[2], y[3]); w.z = cvt_pk_bf16(y[4], y[5]); w.w = cvt_pk_bf16(y[6], y[7]);
;                     *(u32x4*)(Y + row * 2048 + col0 + bj * HALF) = w; } }
	v_mul_f32_e32 v109, v102, v122
	v_mul_f32_e32 v113, v103, v123
	v_mul_f32_e32 v110, v104, v110
	v_cvt_pk_bf16_f32 v102, v3, v106
	v_cvt_pk_bf16_f32 v103, v107, v108
	v_cvt_pk_bf16_f32 v104, v109, v113
	v_cvt_pk_bf16_f32 v105, v110, v105
	global_store_dwordx4 v[120:121], v[102:105], off offset:256
	s_nop 1
	v_mov_b64_e32 v[102:103], v[180:181]
	v_ashrrev_i32_e32 v113, 31, v112
	v_lshlrev_b64 v[104:105], 12, v[112:113]
	v_lshl_add_u64 v[104:105], s[6:7], 0, v[104:105]
	v_lshl_add_u64 v[104:105], v[104:105], 0, v[4:5]
	v_lshl_add_u64 v[106:107], v[114:115], 0, s[14:15]
	v_cvt_pk_f32_fp8_e32 v[108:109], v102
	v_cvt_pk_f32_fp8_sdwa v[110:111], v102 src0_sel:WORD_1
	v_cvt_pk_f32_fp8_e32 v[112:113], v103
	v_cvt_pk_f32_fp8_sdwa v[102:103], v103 src0_sel:WORD_1
	v_max_f32_e32 v3, v108, v108
	v_max_f32_e32 v108, v109, v109
	v_max_f32_e32 v109, v110, v110
	v_max_f32_e32 v103, v103, v103
	v_max_f32_e32 v110, v111, v111
	v_max_f32_e32 v111, v112, v112
	v_max_f32_e32 v112, v113, v113
	v_max_f32_e32 v102, v102, v102
	v_max_f32_e32 v103, 0xc2a00000, v103
	v_max_f32_e32 v3, 0xc2a00000, v3
	v_max_f32_e32 v108, 0xc2a00000, v108
	v_max_f32_e32 v109, 0xc2a00000, v109
	v_max_f32_e32 v110, 0xc2a00000, v110
	v_max_f32_e32 v111, 0xc2a00000, v111
	v_max_f32_e32 v112, 0xc2a00000, v112
	v_max_f32_e32 v102, 0xc2a00000, v102
	v_mul_f32_e32 v103, 0xbfb8aa3b, v103
	v_mul_f32_e32 v3, 0xbfb8aa3b, v3
	v_mul_f32_e32 v108, 0xbfb8aa3b, v108
	v_mul_f32_e32 v109, 0xbfb8aa3b, v109
	v_mul_f32_e32 v110, 0xbfb8aa3b, v110
	v_mul_f32_e32 v111, 0xbfb8aa3b, v111
	v_mul_f32_e32 v112, 0xbfb8aa3b, v112
	v_mul_f32_e32 v102, 0xbfb8aa3b, v102
	v_exp_f32_e32 v103, v103
	v_exp_f32_e32 v3, v3
	v_exp_f32_e32 v108, v108
	v_exp_f32_e32 v109, v109
	v_exp_f32_e32 v110, v110
	v_exp_f32_e32 v111, v111
	v_exp_f32_e32 v112, v112
	v_exp_f32_e32 v102, v102
	v_add_f32_e32 v103, 1.0, v103
	v_add_f32_e32 v3, 1.0, v3
	v_add_f32_e32 v108, 1.0, v108
	v_add_f32_e32 v109, 1.0, v109
	v_add_f32_e32 v110, 1.0, v110
	v_add_f32_e32 v111, 1.0, v111
	v_add_f32_e32 v112, 1.0, v112
	v_add_f32_e32 v102, 1.0, v102
	v_rcp_f32_e32 v103, v103
	v_rcp_f32_e32 v3, v3
	v_rcp_f32_e32 v108, v108
	v_rcp_f32_e32 v109, v109
	v_rcp_f32_e32 v110, v110
	v_rcp_f32_e32 v111, v111
	v_rcp_f32_e32 v112, v112
	v_rcp_f32_e32 v102, v102
	v_mul_f32_e32 v97, v97, v103
	v_mul_f32_e32 v3, v98, v3
	v_mul_f32_e32 v98, v99, v108
	v_mul_f32_e32 v99, v100, v109
	v_mul_f32_e32 v100, v101, v110
	v_mul_f32_e32 v101, v94, v111
	v_mul_f32_e32 v108, v95, v112
	v_mul_f32_e32 v102, v96, v102
	v_cvt_pk_bf16_f32 v94, v3, v98
	v_cvt_pk_bf16_f32 v95, v99, v100
	v_cvt_pk_bf16_f32 v96, v101, v108
	v_cvt_pk_bf16_f32 v97, v102, v97
	global_store_dwordx4 v[104:105], v[94:97], off
	s_nop 1
	v_mov_b64_e32 v[94:95], v[182:183]
	v_cvt_pk_f32_fp8_e32 v[102:103], v94
	v_cvt_pk_f32_fp8_sdwa v[106:107], v94 src0_sel:WORD_1
	v_cvt_pk_f32_fp8_e32 v[108:109], v95
	v_cvt_pk_f32_fp8_sdwa v[94:95], v95 src0_sel:WORD_1
	v_max_f32_e32 v3, v102, v102
	v_max_f32_e32 v97, v103, v103
	v_max_f32_e32 v102, v106, v106
	v_max_f32_e32 v95, v95, v95
	v_max_f32_e32 v103, v107, v107
	v_max_f32_e32 v106, v108, v108
	v_max_f32_e32 v107, v109, v109
	v_max_f32_e32 v94, v94, v94
	v_max_f32_e32 v95, 0xc2a00000, v95
	v_max_f32_e32 v3, 0xc2a00000, v3
	v_max_f32_e32 v97, 0xc2a00000, v97
	v_max_f32_e32 v102, 0xc2a00000, v102
	v_max_f32_e32 v103, 0xc2a00000, v103
	v_max_f32_e32 v106, 0xc2a00000, v106
	v_max_f32_e32 v107, 0xc2a00000, v107
	v_max_f32_e32 v94, 0xc2a00000, v94
	v_mul_f32_e32 v95, 0xbfb8aa3b, v95
	v_mul_f32_e32 v3, 0xbfb8aa3b, v3
	v_mul_f32_e32 v97, 0xbfb8aa3b, v97
	v_mul_f32_e32 v102, 0xbfb8aa3b, v102
	v_mul_f32_e32 v103, 0xbfb8aa3b, v103
	v_mul_f32_e32 v106, 0xbfb8aa3b, v106
	v_mul_f32_e32 v107, 0xbfb8aa3b, v107
	v_mul_f32_e32 v94, 0xbfb8aa3b, v94
	v_exp_f32_e32 v95, v95
	v_exp_f32_e32 v3, v3
	v_exp_f32_e32 v97, v97
	v_exp_f32_e32 v102, v102
	v_exp_f32_e32 v103, v103
	v_exp_f32_e32 v106, v106
	v_exp_f32_e32 v107, v107
	v_exp_f32_e32 v94, v94
	v_add_f32_e32 v95, 1.0, v95
	v_add_f32_e32 v3, 1.0, v3
	v_add_f32_e32 v97, 1.0, v97
	v_add_f32_e32 v102, 1.0, v102
	v_add_f32_e32 v103, 1.0, v103
	v_add_f32_e32 v106, 1.0, v106
	v_add_f32_e32 v107, 1.0, v107
	v_add_f32_e32 v94, 1.0, v94
	v_rcp_f32_e32 v95, v95
	v_add_u32_e32 v96, 48, v152
	v_rcp_f32_e32 v3, v3
	v_rcp_f32_e32 v97, v97
	v_rcp_f32_e32 v102, v102
	v_rcp_f32_e32 v103, v103
	v_rcp_f32_e32 v106, v106
	v_rcp_f32_e32 v107, v107
	v_rcp_f32_e32 v94, v94
	v_mad_i64_i32 v[98:99], s[24:25], v96, s50, v[154:155]
	v_lshl_add_u64 v[98:99], v[98:99], 0, v[150:151]
	v_add_co_u32_e32 v100, vcc, s51, v98
	v_mul_f32_e32 v89, v89, v95
	s_nop 0
	v_addc_co_u32_e32 v101, vcc, 0, v99, vcc
	v_mul_f32_e32 v3, v90, v3
	v_mul_f32_e32 v90, v91, v97
	v_mul_f32_e32 v91, v92, v102
	v_mul_f32_e32 v92, v93, v103
	v_mul_f32_e32 v93, v86, v106
	v_mul_f32_e32 v97, v87, v107
	v_mul_f32_e32 v94, v88, v94
	v_cvt_pk_bf16_f32 v86, v3, v90
	v_cvt_pk_bf16_f32 v87, v91, v92
	v_cvt_pk_bf16_f32 v88, v93, v97
	v_cvt_pk_bf16_f32 v89, v94, v89
	global_store_dwordx4 v[104:105], v[86:89], off offset:256
	s_nop 1
	v_mov_b64_e32 v[86:87], v[184:185]
	v_ashrrev_i32_e32 v97, 31, v96
	v_lshlrev_b64 v[88:89], 12, v[96:97]
	v_lshl_add_u64 v[88:89], s[6:7], 0, v[88:89]
	v_lshl_add_u64 v[88:89], v[88:89], 0, v[4:5]
	v_lshl_add_u64 v[90:91], v[98:99], 0, s[14:15]
	v_cvt_pk_f32_fp8_e32 v[92:93], v86
	v_cvt_pk_f32_fp8_sdwa v[94:95], v86 src0_sel:WORD_1
	v_cvt_pk_f32_fp8_e32 v[96:97], v87
	v_cvt_pk_f32_fp8_sdwa v[86:87], v87 src0_sel:WORD_1
	v_max_f32_e32 v3, v92, v92
	v_max_f32_e32 v92, v93, v93
	v_max_f32_e32 v93, v94, v94
	v_max_f32_e32 v87, v87, v87
	v_max_f32_e32 v94, v95, v95
	v_max_f32_e32 v95, v96, v96
; __device__ __forceinline__ unsigned cvt_pk_bf16(float lo, float hi) { unsigned r; asm volatile("v_cvt_pk_bf16_f32 %0, %1, %2" : "=v"(r) : "v"(lo), "v"(hi)); return r; }
;     static __device__ __forceinline__ float f8(unsigned w, int i) { const auto p = (i & 2) ? __builtin_amdgcn_cvt_pk_f32_fp8((int)w, true) : __builtin_amdgcn_cvt_pk_f32_fp8((int)w, false); return (i & 1) ? p[1] : p[0]; }
; __device__ __forceinline__ float sigmoidf_(float x) { return __builtin_amdgcn_rcpf(1.f + __builtin_amdgcn_exp2f(-1.4426950408889634f * x)); }
;     __device__ __forceinline__ void operator()(const f32x4 (&acc)[2][2][4][2], const Unit& u, int wr, int wc, int fr, int fq) const {
;     ...
;             for (int m = 0; m < 4; ++m) { const size_t row = (size_t)(row0 + ai * HALF + m * 16);
; #pragma unroll
;                 for (int bj = 0; bj < 2; ++bj) { const uint2 gb2 = *(const uint2*)(Z8 + row * Z8LD + zgb + col0 + bj * HALF); float y[8];
; #pragma unroll
;                     for (int n = 0; n < 2; ++n)
; #pragma unroll
;                         for (int i = 0; i < 4; ++i) { const float xb = f8(n ? gb2.y : gb2.x, i);
;                             y[4 * n + i] = acc[ai][bj][m][n][i] * sigmoidf_(fmaxf(xb, -80.f)); }
;                     u32x4 w; w.x = cvt_pk_bf16(y[0], y[1]); w.y = cvt_pk_bf16(y[2], y[3]); w.z = cvt_pk_bf16(y[4], y[5]); w.w = cvt_pk_bf16(y[6], y[7]);
;                     *(u32x4*)(Y + row * 2048 + col0 + bj * HALF) = w; } }
	v_max_f32_e32 v96, v97, v97
	v_max_f32_e32 v86, v86, v86
	v_max_f32_e32 v87, 0xc2a00000, v87
	v_max_f32_e32 v3, 0xc2a00000, v3
	v_max_f32_e32 v92, 0xc2a00000, v92
	v_max_f32_e32 v93, 0xc2a00000, v93
	v_max_f32_e32 v94, 0xc2a00000, v94
	v_max_f32_e32 v95, 0xc2a00000, v95
	v_max_f32_e32 v96, 0xc2a00000, v96
	v_max_f32_e32 v86, 0xc2a00000, v86
	v_mul_f32_e32 v87, 0xbfb8aa3b, v87
	v_mul_f32_e32 v3, 0xbfb8aa3b, v3
	v_mul_f32_e32 v92, 0xbfb8aa3b, v92
	v_mul_f32_e32 v93, 0xbfb8aa3b, v93
	v_mul_f32_e32 v94, 0xbfb8aa3b, v94
	v_mul_f32_e32 v95, 0xbfb8aa3b, v95
	v_mul_f32_e32 v96, 0xbfb8aa3b, v96
	v_mul_f32_e32 v86, 0xbfb8aa3b, v86
	v_exp_f32_e32 v87, v87
	v_exp_f32_e32 v3, v3
	v_exp_f32_e32 v92, v92
	v_exp_f32_e32 v93, v93
	v_exp_f32_e32 v94, v94
	v_exp_f32_e32 v95, v95
	v_exp_f32_e32 v96, v96
	v_exp_f32_e32 v86, v86
	v_add_f32_e32 v87, 1.0, v87
	v_add_f32_e32 v3, 1.0, v3
	v_add_f32_e32 v92, 1.0, v92
	v_add_f32_e32 v93, 1.0, v93
	v_add_f32_e32 v94, 1.0, v94
	v_add_f32_e32 v95, 1.0, v95
	v_add_f32_e32 v96, 1.0, v96
	v_add_f32_e32 v86, 1.0, v86
	v_rcp_f32_e32 v87, v87
	v_rcp_f32_e32 v3, v3
	v_rcp_f32_e32 v92, v92
	v_rcp_f32_e32 v93, v93
	v_rcp_f32_e32 v94, v94
	v_rcp_f32_e32 v95, v95
	v_rcp_f32_e32 v96, v96
	v_rcp_f32_e32 v86, v86
	v_mul_f32_e32 v81, v81, v87
	v_mul_f32_e32 v3, v82, v3
	v_mul_f32_e32 v82, v83, v92
	v_mul_f32_e32 v83, v84, v93
	v_mul_f32_e32 v84, v85, v94
	v_mul_f32_e32 v85, v78, v95
	v_mul_f32_e32 v92, v79, v96
	v_mul_f32_e32 v86, v80, v86
	v_cvt_pk_bf16_f32 v78, v3, v82
	v_cvt_pk_bf16_f32 v79, v83, v84
	v_cvt_pk_bf16_f32 v80, v85, v92
	v_cvt_pk_bf16_f32 v81, v86, v81
	global_store_dwordx4 v[88:89], v[78:81], off
	s_nop 1
	v_mov_b64_e32 v[78:79], v[186:187]
	v_cvt_pk_f32_fp8_e32 v[86:87], v78
	v_cvt_pk_f32_fp8_sdwa v[90:91], v78 src0_sel:WORD_1
	v_cvt_pk_f32_fp8_e32 v[92:93], v79
	v_cvt_pk_f32_fp8_sdwa v[78:79], v79 src0_sel:WORD_1
	v_max_f32_e32 v3, v86, v86
	v_max_f32_e32 v81, v87, v87
	v_max_f32_e32 v86, v90, v90
	v_max_f32_e32 v79, v79, v79
	v_max_f32_e32 v87, v91, v91
	v_max_f32_e32 v90, v92, v92
	v_max_f32_e32 v91, v93, v93
	v_max_f32_e32 v78, v78, v78
	v_max_f32_e32 v79, 0xc2a00000, v79
	v_max_f32_e32 v3, 0xc2a00000, v3
	v_max_f32_e32 v81, 0xc2a00000, v81
	v_max_f32_e32 v86, 0xc2a00000, v86
	v_max_f32_e32 v87, 0xc2a00000, v87
	v_max_f32_e32 v90, 0xc2a00000, v90
	v_max_f32_e32 v91, 0xc2a00000, v91
	v_max_f32_e32 v78, 0xc2a00000, v78
	v_mul_f32_e32 v79, 0xbfb8aa3b, v79
	v_mul_f32_e32 v3, 0xbfb8aa3b, v3
	v_mul_f32_e32 v81, 0xbfb8aa3b, v81
	v_mul_f32_e32 v86, 0xbfb8aa3b, v86
	v_mul_f32_e32 v87, 0xbfb8aa3b, v87
	v_mul_f32_e32 v90, 0xbfb8aa3b, v90
	v_mul_f32_e32 v91, 0xbfb8aa3b, v91
	v_mul_f32_e32 v78, 0xbfb8aa3b, v78
	v_exp_f32_e32 v79, v79
	v_exp_f32_e32 v3, v3
	v_exp_f32_e32 v81, v81
	v_exp_f32_e32 v86, v86
	v_exp_f32_e32 v87, v87
	v_exp_f32_e32 v90, v90
	v_exp_f32_e32 v91, v91
	v_exp_f32_e32 v78, v78
	v_add_f32_e32 v79, 1.0, v79
	v_add_f32_e32 v3, 1.0, v3
	v_add_f32_e32 v81, 1.0, v81
	v_add_f32_e32 v86, 1.0, v86
	v_add_f32_e32 v87, 1.0, v87
	v_add_f32_e32 v90, 1.0, v90
	v_add_f32_e32 v91, 1.0, v91
	v_add_f32_e32 v78, 1.0, v78
	v_rcp_f32_e32 v79, v79
	v_add_u32_e32 v80, 0x80, v152
	v_rcp_f32_e32 v3, v3
	v_rcp_f32_e32 v81, v81
	v_rcp_f32_e32 v86, v86
	v_rcp_f32_e32 v87, v87
	v_rcp_f32_e32 v90, v90
	v_rcp_f32_e32 v91, v91
	v_rcp_f32_e32 v78, v78
	v_mad_i64_i32 v[82:83], s[24:25], v80, s50, v[154:155]
	v_lshl_add_u64 v[82:83], v[82:83], 0, v[150:151]
	v_add_co_u32_e32 v84, vcc, s51, v82
	v_mul_f32_e32 v73, v73, v79
	s_nop 0
	v_addc_co_u32_e32 v85, vcc, 0, v83, vcc
	v_mul_f32_e32 v3, v74, v3
	v_mul_f32_e32 v74, v75, v81
	v_mul_f32_e32 v75, v76, v86
	v_mul_f32_e32 v76, v77, v87
	v_mul_f32_e32 v77, v70, v90
	v_mul_f32_e32 v81, v71, v91
	v_mul_f32_e32 v78, v72, v78
	v_cvt_pk_bf16_f32 v70, v3, v74
	v_cvt_pk_bf16_f32 v71, v75, v76
	v_cvt_pk_bf16_f32 v72, v77, v81
	v_cvt_pk_bf16_f32 v73, v78, v73
	global_store_dwordx4 v[88:89], v[70:73], off offset:256
	s_nop 1
	v_mov_b64_e32 v[70:71], v[188:189]
	v_ashrrev_i32_e32 v81, 31, v80
	v_lshlrev_b64 v[72:73], 12, v[80:81]
	v_lshl_add_u64 v[72:73], s[6:7], 0, v[72:73]
	v_lshl_add_u64 v[72:73], v[72:73], 0, v[4:5]
	v_lshl_add_u64 v[74:75], v[82:83], 0, s[14:15]
	v_cvt_pk_f32_fp8_e32 v[76:77], v70
	v_cvt_pk_f32_fp8_sdwa v[78:79], v70 src0_sel:WORD_1
	v_cvt_pk_f32_fp8_e32 v[80:81], v71
	v_cvt_pk_f32_fp8_sdwa v[70:71], v71 src0_sel:WORD_1
	v_max_f32_e32 v3, v76, v76
	v_max_f32_e32 v76, v77, v77
	v_max_f32_e32 v77, v78, v78
	v_max_f32_e32 v71, v71, v71
	v_max_f32_e32 v78, v79, v79
	v_max_f32_e32 v79, v80, v80
	v_max_f32_e32 v80, v81, v81
	v_max_f32_e32 v70, v70, v70
	v_max_f32_e32 v71, 0xc2a00000, v71
	v_max_f32_e32 v3, 0xc2a00000, v3
	v_max_f32_e32 v76, 0xc2a00000, v76
	v_max_f32_e32 v77, 0xc2a00000, v77
	v_max_f32_e32 v78, 0xc2a00000, v78
	v_max_f32_e32 v79, 0xc2a00000, v79
	v_max_f32_e32 v80, 0xc2a00000, v80
	v_max_f32_e32 v70, 0xc2a00000, v70
	v_mul_f32_e32 v71, 0xbfb8aa3b, v71
	v_mul_f32_e32 v3, 0xbfb8aa3b, v3
	v_mul_f32_e32 v76, 0xbfb8aa3b, v76
	v_mul_f32_e32 v77, 0xbfb8aa3b, v77
	v_mul_f32_e32 v78, 0xbfb8aa3b, v78
	v_mul_f32_e32 v79, 0xbfb8aa3b, v79
	v_mul_f32_e32 v80, 0xbfb8aa3b, v80
	v_mul_f32_e32 v70, 0xbfb8aa3b, v70
	v_exp_f32_e32 v71, v71
	v_exp_f32_e32 v3, v3
	v_exp_f32_e32 v76, v76
	v_exp_f32_e32 v77, v77
	v_exp_f32_e32 v78, v78
	v_exp_f32_e32 v79, v79
	v_exp_f32_e32 v80, v80
	v_exp_f32_e32 v70, v70
	v_add_f32_e32 v71, 1.0, v71
	v_add_f32_e32 v3, 1.0, v3
	v_add_f32_e32 v76, 1.0, v76
	v_add_f32_e32 v77, 1.0, v77
	v_add_f32_e32 v78, 1.0, v78
	v_add_f32_e32 v79, 1.0, v79
	v_add_f32_e32 v80, 1.0, v80
	v_add_f32_e32 v70, 1.0, v70
	v_rcp_f32_e32 v71, v71
	v_rcp_f32_e32 v3, v3
	v_rcp_f32_e32 v76, v76
; __device__ __forceinline__ unsigned cvt_pk_bf16(float lo, float hi) { unsigned r; asm volatile("v_cvt_pk_bf16_f32 %0, %1, %2" : "=v"(r) : "v"(lo), "v"(hi)); return r; }
;     static __device__ __forceinline__ float f8(unsigned w, int i) { const auto p = (i & 2) ? __builtin_amdgcn_cvt_pk_f32_fp8((int)w, true) : __builtin_amdgcn_cvt_pk_f32_fp8((int)w, false); return (i & 1) ? p[1] : p[0]; }
; __device__ __forceinline__ float sigmoidf_(float x) { return __builtin_amdgcn_rcpf(1.f + __builtin_amdgcn_exp2f(-1.4426950408889634f * x)); }
;     __device__ __forceinline__ void operator()(const f32x4 (&acc)[2][2][4][2], const Unit& u, int wr, int wc, int fr, int fq) const {
;     ...
;             for (int m = 0; m < 4; ++m) { const size_t row = (size_t)(row0 + ai * HALF + m * 16);
; #pragma unroll
;                 for (int bj = 0; bj < 2; ++bj) { const uint2 gb2 = *(const uint2*)(Z8 + row * Z8LD + zgb + col0 + bj * HALF); float y[8];
; #pragma unroll
;                     for (int n = 0; n < 2; ++n)
; #pragma unroll
;                         for (int i = 0; i < 4; ++i) { const float xb = f8(n ? gb2.y : gb2.x, i);
;                             y[4 * n + i] = acc[ai][bj][m][n][i] * sigmoidf_(fmaxf(xb, -80.f)); }
;                     u32x4 w; w.x = cvt_pk_bf16(y[0], y[1]); w.y = cvt_pk_bf16(y[2], y[3]); w.z = cvt_pk_bf16(y[4], y[5]); w.w = cvt_pk_bf16(y[6], y[7]);
;                     *(u32x4*)(Y + row * 2048 + col0 + bj * HALF) = w; } }
	v_rcp_f32_e32 v77, v77
	v_rcp_f32_e32 v78, v78
	v_rcp_f32_e32 v79, v79
	v_rcp_f32_e32 v80, v80
	v_rcp_f32_e32 v70, v70
	v_mul_f32_e32 v65, v65, v71
	v_mul_f32_e32 v3, v66, v3
	v_mul_f32_e32 v66, v67, v76
	v_mul_f32_e32 v67, v68, v77
	v_mul_f32_e32 v68, v69, v78
	v_mul_f32_e32 v69, v62, v79
	v_mul_f32_e32 v76, v63, v80
	v_mul_f32_e32 v70, v64, v70
	v_cvt_pk_bf16_f32 v62, v3, v66
	v_cvt_pk_bf16_f32 v63, v67, v68
	v_cvt_pk_bf16_f32 v64, v69, v76
	v_cvt_pk_bf16_f32 v65, v70, v65
	global_store_dwordx4 v[72:73], v[62:65], off
	s_nop 1
	v_mov_b64_e32 v[62:63], v[190:191]
	v_cvt_pk_f32_fp8_e32 v[70:71], v62
	v_cvt_pk_f32_fp8_sdwa v[74:75], v62 src0_sel:WORD_1
	v_cvt_pk_f32_fp8_e32 v[76:77], v63
	v_cvt_pk_f32_fp8_sdwa v[62:63], v63 src0_sel:WORD_1
	v_max_f32_e32 v3, v70, v70
	v_max_f32_e32 v65, v71, v71
	v_max_f32_e32 v70, v74, v74
	v_max_f32_e32 v63, v63, v63
	v_max_f32_e32 v71, v75, v75
	v_max_f32_e32 v74, v76, v76
	v_max_f32_e32 v75, v77, v77
	v_max_f32_e32 v62, v62, v62
	v_max_f32_e32 v63, 0xc2a00000, v63
	v_max_f32_e32 v3, 0xc2a00000, v3
	v_max_f32_e32 v65, 0xc2a00000, v65
	v_max_f32_e32 v70, 0xc2a00000, v70
	v_max_f32_e32 v71, 0xc2a00000, v71
	v_max_f32_e32 v74, 0xc2a00000, v74
	v_max_f32_e32 v75, 0xc2a00000, v75
	v_max_f32_e32 v62, 0xc2a00000, v62
	v_mul_f32_e32 v63, 0xbfb8aa3b, v63
	v_mul_f32_e32 v3, 0xbfb8aa3b, v3
	v_mul_f32_e32 v65, 0xbfb8aa3b, v65
	v_mul_f32_e32 v70, 0xbfb8aa3b, v70
	v_mul_f32_e32 v71, 0xbfb8aa3b, v71
	v_mul_f32_e32 v74, 0xbfb8aa3b, v74
	v_mul_f32_e32 v75, 0xbfb8aa3b, v75
	v_mul_f32_e32 v62, 0xbfb8aa3b, v62
	v_exp_f32_e32 v63, v63
	v_exp_f32_e32 v3, v3
	v_exp_f32_e32 v65, v65
	v_exp_f32_e32 v70, v70
	v_exp_f32_e32 v71, v71
	v_exp_f32_e32 v74, v74
	v_exp_f32_e32 v75, v75
	v_exp_f32_e32 v62, v62
	v_add_f32_e32 v63, 1.0, v63
	v_add_f32_e32 v3, 1.0, v3
	v_add_f32_e32 v65, 1.0, v65
	v_add_f32_e32 v70, 1.0, v70
	v_add_f32_e32 v71, 1.0, v71
	v_add_f32_e32 v74, 1.0, v74
	v_add_f32_e32 v75, 1.0, v75
	v_add_f32_e32 v62, 1.0, v62
	v_rcp_f32_e32 v63, v63
	v_add_u32_e32 v64, 0x90, v152
	v_rcp_f32_e32 v3, v3
	v_rcp_f32_e32 v65, v65
	v_rcp_f32_e32 v70, v70
	v_rcp_f32_e32 v71, v71
	v_rcp_f32_e32 v74, v74
	v_rcp_f32_e32 v75, v75
	v_rcp_f32_e32 v62, v62
	v_mad_i64_i32 v[66:67], s[24:25], v64, s50, v[154:155]
	v_lshl_add_u64 v[66:67], v[66:67], 0, v[150:151]
	v_add_co_u32_e32 v68, vcc, s51, v66
	v_mul_f32_e32 v57, v57, v63
	s_nop 0
	v_addc_co_u32_e32 v69, vcc, 0, v67, vcc
	v_mul_f32_e32 v3, v58, v3
	v_mul_f32_e32 v58, v59, v65
	v_mul_f32_e32 v59, v60, v70
	v_mul_f32_e32 v60, v61, v71
	v_mul_f32_e32 v61, v54, v74
	v_mul_f32_e32 v65, v55, v75
	v_mul_f32_e32 v62, v56, v62
	v_cvt_pk_bf16_f32 v54, v3, v58
	v_cvt_pk_bf16_f32 v55, v59, v60
	v_cvt_pk_bf16_f32 v56, v61, v65
	v_cvt_pk_bf16_f32 v57, v62, v57
	global_store_dwordx4 v[72:73], v[54:57], off offset:256
	s_nop 1
	v_mov_b64_e32 v[54:55], v[192:193]
	v_ashrrev_i32_e32 v65, 31, v64
	v_lshlrev_b64 v[56:57], 12, v[64:65]
	v_lshl_add_u64 v[56:57], s[6:7], 0, v[56:57]
	v_lshl_add_u64 v[56:57], v[56:57], 0, v[4:5]
	v_lshl_add_u64 v[58:59], v[66:67], 0, s[14:15]
	v_cvt_pk_f32_fp8_e32 v[60:61], v54
	v_cvt_pk_f32_fp8_sdwa v[62:63], v54 src0_sel:WORD_1
	v_cvt_pk_f32_fp8_e32 v[64:65], v55
	v_cvt_pk_f32_fp8_sdwa v[54:55], v55 src0_sel:WORD_1
	v_max_f32_e32 v3, v60, v60
	v_max_f32_e32 v60, v61, v61
	v_max_f32_e32 v61, v62, v62
	v_max_f32_e32 v55, v55, v55
	v_max_f32_e32 v62, v63, v63
	v_max_f32_e32 v63, v64, v64
	v_max_f32_e32 v64, v65, v65
	v_max_f32_e32 v54, v54, v54
	v_max_f32_e32 v55, 0xc2a00000, v55
	v_max_f32_e32 v3, 0xc2a00000, v3
	v_max_f32_e32 v60, 0xc2a00000, v60
	v_max_f32_e32 v61, 0xc2a00000, v61
	v_max_f32_e32 v62, 0xc2a00000, v62
	v_max_f32_e32 v63, 0xc2a00000, v63
	v_max_f32_e32 v64, 0xc2a00000, v64
	v_max_f32_e32 v54, 0xc2a00000, v54
	v_mul_f32_e32 v55, 0xbfb8aa3b, v55
	v_mul_f32_e32 v3, 0xbfb8aa3b, v3
	v_mul_f32_e32 v60, 0xbfb8aa3b, v60
	v_mul_f32_e32 v61, 0xbfb8aa3b, v61
	v_mul_f32_e32 v62, 0xbfb8aa3b, v62
	v_mul_f32_e32 v63, 0xbfb8aa3b, v63
	v_mul_f32_e32 v64, 0xbfb8aa3b, v64
	v_mul_f32_e32 v54, 0xbfb8aa3b, v54
	v_exp_f32_e32 v55, v55
	v_exp_f32_e32 v3, v3
	v_exp_f32_e32 v60, v60
	v_exp_f32_e32 v61, v61
	v_exp_f32_e32 v62, v62
	v_exp_f32_e32 v63, v63
	v_exp_f32_e32 v64, v64
	v_exp_f32_e32 v54, v54
	v_add_f32_e32 v55, 1.0, v55
	v_add_f32_e32 v3, 1.0, v3
	v_add_f32_e32 v60, 1.0, v60
	v_add_f32_e32 v61, 1.0, v61
	v_add_f32_e32 v62, 1.0, v62
	v_add_f32_e32 v63, 1.0, v63
	v_add_f32_e32 v64, 1.0, v64
	v_add_f32_e32 v54, 1.0, v54
	v_rcp_f32_e32 v55, v55
	v_rcp_f32_e32 v3, v3
	v_rcp_f32_e32 v60, v60
	v_rcp_f32_e32 v61, v61
	v_rcp_f32_e32 v62, v62
	v_rcp_f32_e32 v63, v63
	v_rcp_f32_e32 v64, v64
	v_rcp_f32_e32 v54, v54
	v_mul_f32_e32 v49, v49, v55
	v_mul_f32_e32 v3, v50, v3
	v_mul_f32_e32 v50, v51, v60
	v_mul_f32_e32 v51, v52, v61
	v_mul_f32_e32 v52, v53, v62
	v_mul_f32_e32 v53, v46, v63
	v_mul_f32_e32 v60, v47, v64
	v_mul_f32_e32 v54, v48, v54
	v_cvt_pk_bf16_f32 v46, v3, v50
	v_cvt_pk_bf16_f32 v47, v51, v52
	v_cvt_pk_bf16_f32 v48, v53, v60
	v_cvt_pk_bf16_f32 v49, v54, v49
	global_store_dwordx4 v[56:57], v[46:49], off
	s_nop 1
	v_mov_b64_e32 v[46:47], v[194:195]
	v_cvt_pk_f32_fp8_e32 v[54:55], v46
	v_cvt_pk_f32_fp8_sdwa v[58:59], v46 src0_sel:WORD_1
	v_cvt_pk_f32_fp8_e32 v[60:61], v47
	v_cvt_pk_f32_fp8_sdwa v[46:47], v47 src0_sel:WORD_1
	v_max_f32_e32 v3, v54, v54
	v_max_f32_e32 v49, v55, v55
	v_max_f32_e32 v54, v58, v58
	v_max_f32_e32 v47, v47, v47
	v_max_f32_e32 v55, v59, v59
	v_max_f32_e32 v58, v60, v60
	v_max_f32_e32 v59, v61, v61
	v_max_f32_e32 v46, v46, v46
	v_max_f32_e32 v47, 0xc2a00000, v47
	v_max_f32_e32 v3, 0xc2a00000, v3
	v_max_f32_e32 v49, 0xc2a00000, v49
	v_max_f32_e32 v54, 0xc2a00000, v54
; __device__ __forceinline__ unsigned cvt_pk_bf16(float lo, float hi) { unsigned r; asm volatile("v_cvt_pk_bf16_f32 %0, %1, %2" : "=v"(r) : "v"(lo), "v"(hi)); return r; }
;     static __device__ __forceinline__ float f8(unsigned w, int i) { const auto p = (i & 2) ? __builtin_amdgcn_cvt_pk_f32_fp8((int)w, true) : __builtin_amdgcn_cvt_pk_f32_fp8((int)w, false); return (i & 1) ? p[1] : p[0]; }
; __device__ __forceinline__ float sigmoidf_(float x) { return __builtin_amdgcn_rcpf(1.f + __builtin_amdgcn_exp2f(-1.4426950408889634f * x)); }
;     __device__ __forceinline__ void operator()(const f32x4 (&acc)[2][2][4][2], const Unit& u, int wr, int wc, int fr, int fq) const {
;     ...
;             for (int m = 0; m < 4; ++m) { const size_t row = (size_t)(row0 + ai * HALF + m * 16);
; #pragma unroll
;                 for (int bj = 0; bj < 2; ++bj) { const uint2 gb2 = *(const uint2*)(Z8 + row * Z8LD + zgb + col0 + bj * HALF); float y[8];
; #pragma unroll
;                     for (int n = 0; n < 2; ++n)
; #pragma unroll
;                         for (int i = 0; i < 4; ++i) { const float xb = f8(n ? gb2.y : gb2.x, i);
;                             y[4 * n + i] = acc[ai][bj][m][n][i] * sigmoidf_(fmaxf(xb, -80.f)); }
;                     u32x4 w; w.x = cvt_pk_bf16(y[0], y[1]); w.y = cvt_pk_bf16(y[2], y[3]); w.z = cvt_pk_bf16(y[4], y[5]); w.w = cvt_pk_bf16(y[6], y[7]);
;                     *(u32x4*)(Y + row * 2048 + col0 + bj * HALF) = w; } }
	v_max_f32_e32 v55, 0xc2a00000, v55
	v_max_f32_e32 v58, 0xc2a00000, v58
	v_max_f32_e32 v59, 0xc2a00000, v59
	v_max_f32_e32 v46, 0xc2a00000, v46
	v_mul_f32_e32 v47, 0xbfb8aa3b, v47
	v_mul_f32_e32 v3, 0xbfb8aa3b, v3
	v_mul_f32_e32 v49, 0xbfb8aa3b, v49
	v_mul_f32_e32 v54, 0xbfb8aa3b, v54
	v_mul_f32_e32 v55, 0xbfb8aa3b, v55
	v_mul_f32_e32 v58, 0xbfb8aa3b, v58
	v_mul_f32_e32 v59, 0xbfb8aa3b, v59
	v_mul_f32_e32 v46, 0xbfb8aa3b, v46
	v_exp_f32_e32 v47, v47
	v_exp_f32_e32 v3, v3
	v_exp_f32_e32 v49, v49
	v_exp_f32_e32 v54, v54
	v_exp_f32_e32 v55, v55
	v_exp_f32_e32 v58, v58
	v_exp_f32_e32 v59, v59
	v_exp_f32_e32 v46, v46
	v_add_f32_e32 v47, 1.0, v47
	v_add_f32_e32 v3, 1.0, v3
	v_add_f32_e32 v49, 1.0, v49
	v_add_f32_e32 v54, 1.0, v54
	v_add_f32_e32 v55, 1.0, v55
	v_add_f32_e32 v58, 1.0, v58
	v_add_f32_e32 v59, 1.0, v59
	v_add_f32_e32 v46, 1.0, v46
	v_rcp_f32_e32 v47, v47
	v_add_u32_e32 v48, 0xa0, v152
	v_rcp_f32_e32 v3, v3
	v_rcp_f32_e32 v49, v49
	v_rcp_f32_e32 v54, v54
	v_rcp_f32_e32 v55, v55
	v_rcp_f32_e32 v58, v58
	v_rcp_f32_e32 v59, v59
	v_rcp_f32_e32 v46, v46
	v_mad_i64_i32 v[50:51], s[24:25], v48, s50, v[154:155]
	v_lshl_add_u64 v[50:51], v[50:51], 0, v[150:151]
	v_add_co_u32_e32 v52, vcc, s51, v50
	v_mul_f32_e32 v41, v41, v47
	s_nop 0
	v_addc_co_u32_e32 v53, vcc, 0, v51, vcc
	v_mul_f32_e32 v3, v42, v3
	v_mul_f32_e32 v42, v43, v49
	v_mul_f32_e32 v43, v44, v54
	v_mul_f32_e32 v44, v45, v55
	v_mul_f32_e32 v45, v38, v58
	v_mul_f32_e32 v49, v39, v59
	v_mul_f32_e32 v46, v40, v46
	v_cvt_pk_bf16_f32 v38, v3, v42
	v_cvt_pk_bf16_f32 v39, v43, v44
	v_cvt_pk_bf16_f32 v40, v45, v49
	v_cvt_pk_bf16_f32 v41, v46, v41
	global_store_dwordx4 v[56:57], v[38:41], off offset:256
	s_nop 1
	v_mov_b64_e32 v[38:39], v[196:197]
	v_ashrrev_i32_e32 v49, 31, v48
	v_lshlrev_b64 v[40:41], 12, v[48:49]
	v_lshl_add_u64 v[40:41], s[6:7], 0, v[40:41]
	v_lshl_add_u64 v[40:41], v[40:41], 0, v[4:5]
	v_lshl_add_u64 v[42:43], v[50:51], 0, s[14:15]
	v_cvt_pk_f32_fp8_e32 v[44:45], v38
	v_cvt_pk_f32_fp8_sdwa v[46:47], v38 src0_sel:WORD_1
	v_cvt_pk_f32_fp8_e32 v[48:49], v39
	v_cvt_pk_f32_fp8_sdwa v[38:39], v39 src0_sel:WORD_1
	v_max_f32_e32 v3, v44, v44
	v_max_f32_e32 v44, v45, v45
	v_max_f32_e32 v45, v46, v46
	v_max_f32_e32 v39, v39, v39
	v_max_f32_e32 v46, v47, v47
	v_max_f32_e32 v47, v48, v48
	v_max_f32_e32 v48, v49, v49
	v_max_f32_e32 v38, v38, v38
	v_max_f32_e32 v39, 0xc2a00000, v39
	v_max_f32_e32 v3, 0xc2a00000, v3
	v_max_f32_e32 v44, 0xc2a00000, v44
	v_max_f32_e32 v45, 0xc2a00000, v45
	v_max_f32_e32 v46, 0xc2a00000, v46
	v_max_f32_e32 v47, 0xc2a00000, v47
	v_max_f32_e32 v48, 0xc2a00000, v48
	v_max_f32_e32 v38, 0xc2a00000, v38
	v_mul_f32_e32 v39, 0xbfb8aa3b, v39
	v_mul_f32_e32 v3, 0xbfb8aa3b, v3
	v_mul_f32_e32 v44, 0xbfb8aa3b, v44
	v_mul_f32_e32 v45, 0xbfb8aa3b, v45
	v_mul_f32_e32 v46, 0xbfb8aa3b, v46
	v_mul_f32_e32 v47, 0xbfb8aa3b, v47
	v_mul_f32_e32 v48, 0xbfb8aa3b, v48
	v_mul_f32_e32 v38, 0xbfb8aa3b, v38
	v_exp_f32_e32 v39, v39
	v_exp_f32_e32 v3, v3
	v_exp_f32_e32 v44, v44
	v_exp_f32_e32 v45, v45
	v_exp_f32_e32 v46, v46
	v_exp_f32_e32 v47, v47
	v_exp_f32_e32 v48, v48
	v_exp_f32_e32 v38, v38
	v_add_f32_e32 v39, 1.0, v39
	v_add_f32_e32 v3, 1.0, v3
	v_add_f32_e32 v44, 1.0, v44
	v_add_f32_e32 v45, 1.0, v45
	v_add_f32_e32 v46, 1.0, v46
	v_add_f32_e32 v47, 1.0, v47
	v_add_f32_e32 v48, 1.0, v48
	v_add_f32_e32 v38, 1.0, v38
	v_rcp_f32_e32 v39, v39
	v_rcp_f32_e32 v3, v3
	v_rcp_f32_e32 v44, v44
	v_rcp_f32_e32 v45, v45
	v_rcp_f32_e32 v46, v46
	v_rcp_f32_e32 v47, v47
	v_rcp_f32_e32 v48, v48
	v_rcp_f32_e32 v38, v38
	v_mul_f32_e32 v33, v33, v39
	v_mul_f32_e32 v3, v34, v3
	v_mul_f32_e32 v34, v35, v44
	v_mul_f32_e32 v35, v36, v45
	v_mul_f32_e32 v36, v37, v46
	v_mul_f32_e32 v37, v30, v47
	v_mul_f32_e32 v44, v31, v48
	v_mul_f32_e32 v38, v32, v38
	v_cvt_pk_bf16_f32 v30, v3, v34
	v_cvt_pk_bf16_f32 v31, v35, v36
	v_cvt_pk_bf16_f32 v32, v37, v44
	v_cvt_pk_bf16_f32 v33, v38, v33
	global_store_dwordx4 v[40:41], v[30:33], off
	s_nop 1
	v_mov_b64_e32 v[30:31], v[198:199]
	v_cvt_pk_f32_fp8_e32 v[38:39], v30
	v_cvt_pk_f32_fp8_sdwa v[42:43], v30 src0_sel:WORD_1
	v_cvt_pk_f32_fp8_e32 v[44:45], v31
	v_cvt_pk_f32_fp8_sdwa v[30:31], v31 src0_sel:WORD_1
	v_max_f32_e32 v3, v38, v38
	v_max_f32_e32 v33, v39, v39
	v_max_f32_e32 v38, v42, v42
	v_max_f32_e32 v31, v31, v31
	v_max_f32_e32 v39, v43, v43
	v_max_f32_e32 v42, v44, v44
	v_max_f32_e32 v43, v45, v45
	v_max_f32_e32 v30, v30, v30
	v_max_f32_e32 v31, 0xc2a00000, v31
	v_max_f32_e32 v3, 0xc2a00000, v3
	v_max_f32_e32 v33, 0xc2a00000, v33
	v_max_f32_e32 v38, 0xc2a00000, v38
	v_max_f32_e32 v39, 0xc2a00000, v39
	v_max_f32_e32 v42, 0xc2a00000, v42
	v_max_f32_e32 v43, 0xc2a00000, v43
	v_max_f32_e32 v30, 0xc2a00000, v30
	v_mul_f32_e32 v31, 0xbfb8aa3b, v31
	v_mul_f32_e32 v3, 0xbfb8aa3b, v3
	v_mul_f32_e32 v33, 0xbfb8aa3b, v33
	v_mul_f32_e32 v38, 0xbfb8aa3b, v38
	v_mul_f32_e32 v39, 0xbfb8aa3b, v39
	v_mul_f32_e32 v42, 0xbfb8aa3b, v42
	v_mul_f32_e32 v43, 0xbfb8aa3b, v43
	v_mul_f32_e32 v30, 0xbfb8aa3b, v30
	v_exp_f32_e32 v31, v31
	v_exp_f32_e32 v3, v3
	v_exp_f32_e32 v33, v33
	v_exp_f32_e32 v38, v38
	v_exp_f32_e32 v39, v39
	v_exp_f32_e32 v42, v42
	v_exp_f32_e32 v43, v43
	v_exp_f32_e32 v30, v30
	v_add_f32_e32 v31, 1.0, v31
	v_add_f32_e32 v3, 1.0, v3
	v_add_f32_e32 v33, 1.0, v33
	v_add_f32_e32 v38, 1.0, v38
	v_add_f32_e32 v39, 1.0, v39
; __device__ __forceinline__ unsigned cvt_pk_bf16(float lo, float hi) { unsigned r; asm volatile("v_cvt_pk_bf16_f32 %0, %1, %2" : "=v"(r) : "v"(lo), "v"(hi)); return r; }
; __device__ __forceinline__ float sigmoidf_(float x) { return __builtin_amdgcn_rcpf(1.f + __builtin_amdgcn_exp2f(-1.4426950408889634f * x)); }
;     static __device__ __forceinline__ float f8(unsigned w, int i) { const auto p = (i & 2) ? __builtin_amdgcn_cvt_pk_f32_fp8((int)w, true) : __builtin_amdgcn_cvt_pk_f32_fp8((int)w, false); return (i & 1) ? p[1] : p[0]; }
; #define PG8_BAR __builtin_amdgcn_s_barrier()
;     __device__ __forceinline__ void operator()(const f32x4 (&acc)[2][2][4][2], const Unit& u, int wr, int wc, int fr, int fq) const {
;     ...
;             for (int m = 0; m < 4; ++m) { const size_t row = (size_t)(row0 + ai * HALF + m * 16);
; #pragma unroll
;                 for (int bj = 0; bj < 2; ++bj) { const uint2 gb2 = *(const uint2*)(Z8 + row * Z8LD + zgb + col0 + bj * HALF); float y[8];
; #pragma unroll
;                     for (int n = 0; n < 2; ++n)
; #pragma unroll
;                         for (int i = 0; i < 4; ++i) { const float xb = f8(n ? gb2.y : gb2.x, i);
;                             y[4 * n + i] = acc[ai][bj][m][n][i] * sigmoidf_(fmaxf(xb, -80.f)); }
;                     u32x4 w; w.x = cvt_pk_bf16(y[0], y[1]); w.y = cvt_pk_bf16(y[2], y[3]); w.z = cvt_pk_bf16(y[4], y[5]); w.w = cvt_pk_bf16(y[6], y[7]);
;                     *(u32x4*)(Y + row * 2048 + col0 + bj * HALF) = w; } }
; template <class Epi, class Sched, bool ALIGN_EPI = false, bool SP2 = false, bool FP8 = false>
; __device__ __forceinline__ void gemm_phase(PG8_LAS unsigned char* lds, const Gemm g, const Sched& S, const Epi& E) {
;     ...
;         if constexpr (!Epi::AFTER_DRAIN) { E(acc, cur, wr, wc, fr, fq); S.done(cur); }
;         if (!has_next) break;
; #pragma unroll
;         for (int a = 0; a < 2; ++a)
; #pragma unroll
;             for (int b = 0; b < 2; ++b)
; #pragma unroll
;                 for (int m = 0; m < 4; ++m)
; #pragma unroll
;                     for (int n = 0; n < 2; ++n) acc[a][b][m][n] = (f32x4){0.f, 0.f, 0.f, 0.f};
;         cur = nxt; cA = nA; cB = nB; ++ui;
;         if constexpr (ALIGN_EPI) { if (wr == 1) PG8_BAR; }
;     }
	v_add_f32_e32 v42, 1.0, v42
	v_add_f32_e32 v43, 1.0, v43
	v_add_f32_e32 v30, 1.0, v30
	v_rcp_f32_e32 v31, v31
	v_add_u32_e32 v32, 0xb0, v152
	v_rcp_f32_e32 v3, v3
	v_rcp_f32_e32 v33, v33
	v_rcp_f32_e32 v38, v38
	v_rcp_f32_e32 v39, v39
	v_rcp_f32_e32 v42, v42
	v_rcp_f32_e32 v43, v43
	v_rcp_f32_e32 v30, v30
	v_mad_i64_i32 v[34:35], s[24:25], v32, s50, v[154:155]
	v_lshl_add_u64 v[34:35], v[34:35], 0, v[150:151]
	v_add_co_u32_e32 v36, vcc, s51, v34
	v_mul_f32_e32 v25, v25, v31
	s_nop 0
	v_addc_co_u32_e32 v37, vcc, 0, v35, vcc
	v_mul_f32_e32 v3, v26, v3
	v_mul_f32_e32 v26, v27, v33
	v_mul_f32_e32 v27, v28, v38
	v_mul_f32_e32 v28, v29, v39
	v_mul_f32_e32 v29, v22, v42
	v_mul_f32_e32 v33, v23, v43
	v_mul_f32_e32 v30, v24, v30
	v_cvt_pk_bf16_f32 v22, v3, v26
	v_cvt_pk_bf16_f32 v23, v27, v28
	v_cvt_pk_bf16_f32 v24, v29, v33
	v_cvt_pk_bf16_f32 v25, v30, v25
	global_store_dwordx4 v[40:41], v[22:25], off offset:256
	s_nop 1
	v_mov_b64_e32 v[22:23], v[200:201]
	v_ashrrev_i32_e32 v33, 31, v32
	v_lshlrev_b64 v[24:25], 12, v[32:33]
	v_lshl_add_u64 v[24:25], s[6:7], 0, v[24:25]
	v_lshl_add_u64 v[24:25], v[24:25], 0, v[4:5]
	v_lshl_add_u64 v[26:27], v[34:35], 0, s[14:15]
	s_andn2_b64 vcc, exec, s[2:3]
	s_mov_b64 s[2:3], -1
	v_cvt_pk_f32_fp8_e32 v[4:5], v22
	v_cvt_pk_f32_fp8_sdwa v[28:29], v22 src0_sel:WORD_1
	v_cvt_pk_f32_fp8_e32 v[30:31], v23
	v_cvt_pk_f32_fp8_sdwa v[22:23], v23 src0_sel:WORD_1
	v_max_f32_e32 v3, v4, v4
	v_max_f32_e32 v4, v5, v5
	v_max_f32_e32 v5, v28, v28
	v_max_f32_e32 v23, v23, v23
	v_max_f32_e32 v28, v29, v29
	v_max_f32_e32 v29, v30, v30
	v_max_f32_e32 v30, v31, v31
	v_max_f32_e32 v22, v22, v22
	v_max_f32_e32 v23, 0xc2a00000, v23
	v_max_f32_e32 v3, 0xc2a00000, v3
	v_max_f32_e32 v4, 0xc2a00000, v4
	v_max_f32_e32 v5, 0xc2a00000, v5
	v_max_f32_e32 v28, 0xc2a00000, v28
	v_max_f32_e32 v29, 0xc2a00000, v29
	v_max_f32_e32 v30, 0xc2a00000, v30
	v_max_f32_e32 v22, 0xc2a00000, v22
	v_mul_f32_e32 v23, 0xbfb8aa3b, v23
	v_mul_f32_e32 v3, 0xbfb8aa3b, v3
	v_mul_f32_e32 v4, 0xbfb8aa3b, v4
	v_mul_f32_e32 v5, 0xbfb8aa3b, v5
	v_mul_f32_e32 v28, 0xbfb8aa3b, v28
	v_mul_f32_e32 v29, 0xbfb8aa3b, v29
	v_mul_f32_e32 v30, 0xbfb8aa3b, v30
	v_mul_f32_e32 v22, 0xbfb8aa3b, v22
	v_exp_f32_e32 v23, v23
	v_exp_f32_e32 v3, v3
	v_exp_f32_e32 v4, v4
	v_exp_f32_e32 v5, v5
	v_exp_f32_e32 v28, v28
	v_exp_f32_e32 v29, v29
	v_exp_f32_e32 v30, v30
	v_exp_f32_e32 v22, v22
	v_add_f32_e32 v23, 1.0, v23
	v_add_f32_e32 v3, 1.0, v3
	v_add_f32_e32 v4, 1.0, v4
	v_add_f32_e32 v5, 1.0, v5
	v_add_f32_e32 v28, 1.0, v28
	v_add_f32_e32 v29, 1.0, v29
	v_add_f32_e32 v30, 1.0, v30
	v_add_f32_e32 v22, 1.0, v22
	v_rcp_f32_e32 v23, v23
	v_rcp_f32_e32 v3, v3
	v_rcp_f32_e32 v4, v4
	v_rcp_f32_e32 v5, v5
	v_rcp_f32_e32 v28, v28
	v_rcp_f32_e32 v29, v29
	v_rcp_f32_e32 v30, v30
	v_rcp_f32_e32 v22, v22
	v_mul_f32_e32 v17, v17, v23
	v_mul_f32_e32 v3, v18, v3
	v_mul_f32_e32 v4, v19, v4
	v_mul_f32_e32 v5, v20, v5
	v_mul_f32_e32 v18, v21, v28
	v_mul_f32_e32 v19, v14, v29
	v_mul_f32_e32 v20, v15, v30
	v_mul_f32_e32 v21, v16, v22
	v_cvt_pk_bf16_f32 v14, v3, v4
	v_cvt_pk_bf16_f32 v15, v5, v18
	v_cvt_pk_bf16_f32 v16, v19, v20
	v_cvt_pk_bf16_f32 v17, v21, v17
	global_store_dwordx4 v[24:25], v[14:17], off
	s_nop 1
	v_mov_b64_e32 v[4:5], v[202:203]
	v_cvt_pk_f32_fp8_sdwa v[18:19], v4 src0_sel:WORD_1
	v_cvt_pk_f32_fp8_sdwa v[14:15], v5 src0_sel:WORD_1
	v_cvt_pk_f32_fp8_e32 v[16:17], v5
	v_cvt_pk_f32_fp8_e32 v[4:5], v4
	v_max_f32_e32 v18, v18, v18
	v_max_f32_e32 v3, v14, v14
	v_max_f32_e32 v14, v17, v17
	v_max_f32_e32 v16, v16, v16
	v_max_f32_e32 v5, v5, v5
	v_max_f32_e32 v4, v4, v4
	v_max_f32_e32 v17, v19, v19
	v_max_f32_e32 v15, v15, v15
	v_max_f32_e32 v14, 0xc2a00000, v14
	v_max_f32_e32 v16, 0xc2a00000, v16
	v_max_f32_e32 v5, 0xc2a00000, v5
	v_max_f32_e32 v4, 0xc2a00000, v4
	v_max_f32_e32 v3, 0xc2a00000, v3
	v_max_f32_e32 v17, 0xc2a00000, v17
	v_max_f32_e32 v18, 0xc2a00000, v18
	v_max_f32_e32 v15, 0xc2a00000, v15
	v_mul_f32_e32 v14, 0xbfb8aa3b, v14
	v_mul_f32_e32 v16, 0xbfb8aa3b, v16
	v_mul_f32_e32 v5, 0xbfb8aa3b, v5
	v_mul_f32_e32 v4, 0xbfb8aa3b, v4
	v_mul_f32_e32 v3, 0xbfb8aa3b, v3
	v_mul_f32_e32 v17, 0xbfb8aa3b, v17
	v_mul_f32_e32 v18, 0xbfb8aa3b, v18
	v_mul_f32_e32 v15, 0xbfb8aa3b, v15
	v_exp_f32_e32 v14, v14
	v_exp_f32_e32 v16, v16
	v_exp_f32_e32 v5, v5
	v_exp_f32_e32 v4, v4
	v_exp_f32_e32 v3, v3
	v_exp_f32_e32 v17, v17
	v_exp_f32_e32 v18, v18
	v_exp_f32_e32 v15, v15
	v_add_f32_e32 v14, 1.0, v14
	v_add_f32_e32 v16, 1.0, v16
	v_add_f32_e32 v5, 1.0, v5
	v_add_f32_e32 v4, 1.0, v4
	v_add_f32_e32 v3, 1.0, v3
	v_add_f32_e32 v17, 1.0, v17
	v_add_f32_e32 v18, 1.0, v18
	v_add_f32_e32 v15, 1.0, v15
	v_rcp_f32_e32 v14, v14
	v_rcp_f32_e32 v16, v16
	v_rcp_f32_e32 v5, v5
	v_rcp_f32_e32 v4, v4
	v_rcp_f32_e32 v3, v3
	v_rcp_f32_e32 v17, v17
	v_rcp_f32_e32 v18, v18
	v_rcp_f32_e32 v15, v15
	v_mul_f32_e32 v7, v7, v14
	v_mul_f32_e32 v6, v6, v16
	v_mul_f32_e32 v5, v11, v5
	v_mul_f32_e32 v4, v10, v4
	v_mul_f32_e32 v3, v8, v3
	v_mul_f32_e32 v8, v13, v17
	v_mul_f32_e32 v12, v12, v18
	v_mul_f32_e32 v9, v9, v15
	v_cvt_pk_bf16_f32 v4, v4, v5
	v_cvt_pk_bf16_f32 v5, v12, v8
	v_cvt_pk_bf16_f32 v6, v6, v7
	v_cvt_pk_bf16_f32 v7, v3, v9
	global_store_dwordx4 v[24:25], v[4:7], off offset:256
	s_cbranch_vccnz .LBB0_1039
	s_andn2_b64 vcc, exec, s[4:5]
	s_cbranch_vccnz .LBB0_1038
	s_barrier
	s_branch .LBB0_1038
